# write-through (sc1) on the widened dwordx4 epilogue stores
# speedup vs baseline: 1.0656x; 1.0113x over previous
.LBB2_5:
	s_mul_i32 s4, s14, 0xc000
	s_add_i32 s5, s4, 0
	s_add_i32 s16, s5, s11
	s_add_i32 s5, s5, s13
	v_add_u32_e32 v134, s5, v89
	s_waitcnt vmcnt(6)
	s_barrier
	v_add_u32_e32 v118, v134, v87
	ds_read_b128 v[102:105], v118 offset:16384
	ds_read_b128 v[110:113], v118 offset:18432
	v_add_u32_e32 v130, s16, v89
	v_add_u32_e32 v126, v130, v87
	ds_read_b128 v[106:109], v126
	s_waitcnt lgkmcnt(0)
	v_mfma_f32_16x16x32_f16 v[18:21], v[102:105], v[106:109], v[18:21]
	ds_read_b128 v[114:117], v118 offset:20480
	v_add_u32_e32 v150, v130, v85
	v_add_u32_e32 v142, v134, v85
	v_mfma_f32_16x16x32_f16 v[22:25], v[110:113], v[106:109], v[22:25]
	ds_read_b128 v[118:121], v118 offset:22528
	s_add_i32 s4, s4, 0xffff4000
	s_cmp_lg_u32 s14, 0
	s_waitcnt lgkmcnt(0)
	v_mfma_f32_16x16x32_f16 v[26:29], v[114:117], v[106:109], v[26:29]
	ds_read_b128 v[122:125], v126 offset:2048
	s_cselect_b32 s4, s4, 0x18000
	s_add_i32 s4, s4, 0
	v_mfma_f32_16x16x32_f16 v[30:33], v[118:121], v[106:109], v[30:33]
	ds_read_b128 v[106:109], v126 offset:4096
	s_add_i32 s5, s4, s9
	s_mov_b32 m0, s5
	s_waitcnt lgkmcnt(0)
	v_mfma_f32_16x16x32_f16 v[38:41], v[102:105], v[122:125], v[38:41]
	ds_read_b128 v[126:129], v126 offset:6144
	s_add_i32 s4, s4, s12
	v_mfma_f32_16x16x32_f16 v[42:45], v[110:113], v[122:125], v[42:45]
	ds_read_b128 v[130:133], v150
	v_mfma_f32_16x16x32_f16 v[50:53], v[114:117], v[122:125], v[50:53]
	ds_read_b128 v[134:137], v142 offset:16384
	v_mfma_f32_16x16x32_f16 v[46:49], v[118:121], v[122:125], v[46:49]
	ds_read_b128 v[122:125], v142 offset:18432
	v_mfma_f32_16x16x32_f16 v[54:57], v[102:105], v[106:109], v[54:57]
	ds_read_b128 v[138:141], v142 offset:20480
	v_mfma_f32_16x16x32_f16 v[58:61], v[110:113], v[106:109], v[58:61]
	ds_read_b128 v[142:145], v142 offset:22528
	v_mfma_f32_16x16x32_f16 v[62:65], v[114:117], v[106:109], v[62:65]
	ds_read_b128 v[146:149], v150 offset:2048
	v_mfma_f32_16x16x32_f16 v[66:69], v[118:121], v[106:109], v[66:69]
	ds_read_b128 v[106:109], v150 offset:4096
	s_waitcnt lgkmcnt(0)
	v_mfma_f32_16x16x32_f16 v[70:73], v[102:105], v[126:129], v[70:73]
	ds_read_b128 v[102:105], v150 offset:6144
	v_mfma_f32_16x16x32_f16 v[74:77], v[110:113], v[126:129], v[74:77]
	v_lshl_add_u64 v[110:111], v[100:101], 0, s[2:3]
	v_mfma_f32_16x16x32_f16 v[34:37], v[114:117], v[126:129], v[34:37]
	v_mfma_f32_16x16x32_f16 v[78:81], v[118:121], v[126:129], v[78:81]
	global_load_lds_dwordx4 v[110:111], off
	v_lshl_add_u64 v[110:111], v[98:99], 0, s[2:3]
	s_add_i32 m0, s5, 0x400
	v_mfma_f32_16x16x32_f16 v[18:21], v[134:137], v[130:133], v[18:21]
	v_mfma_f32_16x16x32_f16 v[22:25], v[122:125], v[130:133], v[22:25]
	v_mfma_f32_16x16x32_f16 v[26:29], v[138:141], v[130:133], v[26:29]
	global_load_lds_dwordx4 v[110:111], off
	v_lshl_add_u64 v[110:111], v[96:97], 0, s[2:3]
	s_add_i32 m0, s4, 0x4000
	v_mfma_f32_16x16x32_f16 v[30:33], v[142:145], v[130:133], v[30:33]
	v_mfma_f32_16x16x32_f16 v[38:41], v[134:137], v[146:149], v[38:41]
	v_mfma_f32_16x16x32_f16 v[42:45], v[122:125], v[146:149], v[42:45]
	global_load_lds_dwordx4 v[110:111], off
	v_lshl_add_u64 v[110:111], v[94:95], 0, s[2:3]
	s_add_i32 m0, s4, 0x4400
	v_mfma_f32_16x16x32_f16 v[50:53], v[138:141], v[146:149], v[50:53]
	v_mfma_f32_16x16x32_f16 v[46:49], v[142:145], v[146:149], v[46:49]
	v_mfma_f32_16x16x32_f16 v[54:57], v[134:137], v[106:109], v[54:57]
	global_load_lds_dwordx4 v[110:111], off
	v_lshl_add_u64 v[110:111], v[92:93], 0, s[2:3]
	s_add_i32 m0, s4, 0x4800
	v_mfma_f32_16x16x32_f16 v[58:61], v[122:125], v[106:109], v[58:61]
	v_mfma_f32_16x16x32_f16 v[62:65], v[138:141], v[106:109], v[62:65]
	v_mfma_f32_16x16x32_f16 v[66:69], v[142:145], v[106:109], v[66:69]
	global_load_lds_dwordx4 v[110:111], off
	v_lshl_add_u64 v[106:107], v[90:91], 0, s[2:3]
	s_add_i32 m0, s4, 0x4c00
	s_waitcnt lgkmcnt(0)
	v_mfma_f32_16x16x32_f16 v[70:73], v[134:137], v[102:105], v[70:73]
	s_add_i32 s4, s14, 1
	s_cmp_lg_u32 s14, 2
	s_cselect_b32 s14, s4, 0
	v_mfma_f32_16x16x32_f16 v[74:77], v[122:125], v[102:105], v[74:77]
	s_add_u32 s2, s2, 0x80
	s_addc_u32 s3, s3, 0
	s_cmp_eq_u32 s10, s2
	v_mfma_f32_16x16x32_f16 v[34:37], v[138:141], v[102:105], v[34:37]
	global_load_lds_dwordx4 v[106:107], off
	v_mfma_f32_16x16x32_f16 v[78:81], v[142:145], v[102:105], v[78:81]
	s_cbranch_scc0 .LBB2_5
	s_mul_i32 s3, s14, 0xc000
	v_or_b32_e32 v1, s8, v1
	s_add_i32 s2, s3, 0
	v_lshlrev_b32_e32 v1, 7, v1
	v_add_u32_e32 v122, s2, v1
	s_waitcnt vmcnt(6)
	s_barrier
	v_add_u32_e32 v106, v122, v87
	ds_read_b128 v[90:93], v106 offset:16384
	v_lshlrev_b32_e32 v89, 7, v83
	ds_read_b128 v[98:101], v106 offset:18432
	v_add_u32_e32 v118, s2, v89
	v_add_u32_e32 v114, v118, v87
	ds_read_b128 v[94:97], v114
	s_waitcnt lgkmcnt(0)
	v_mfma_f32_16x16x32_f16 v[18:21], v[90:93], v[94:97], v[18:21]
	ds_read_b128 v[102:105], v106 offset:20480
	v_add_u32_e32 v138, v118, v85
	v_add_u32_e32 v130, v122, v85
	v_mfma_f32_16x16x32_f16 v[22:25], v[98:101], v[94:97], v[22:25]
	ds_read_b128 v[106:109], v106 offset:22528
	s_lshr_b32 s2, s15, 8
	s_add_i32 s3, s3, 0xc000
	s_waitcnt lgkmcnt(0)
	v_mfma_f32_16x16x32_f16 v[26:29], v[102:105], v[94:97], v[26:29]
	ds_read_b128 v[110:113], v114 offset:2048
	s_cmp_lg_u32 s14, 2
	s_cselect_b32 s3, s3, 0
	v_mfma_f32_16x16x32_f16 v[30:33], v[106:109], v[94:97], v[30:33]
	ds_read_b128 v[94:97], v114 offset:4096
	s_add_i32 s3, s3, 0
	v_add_u32_e32 v1, s3, v1
	s_waitcnt lgkmcnt(0)
	v_mfma_f32_16x16x32_f16 v[38:41], v[90:93], v[110:113], v[38:41]
	ds_read_b128 v[114:117], v114 offset:6144
	v_add_u32_e32 v89, s3, v89
	s_lshl_b64 s[0:1], s[0:1], 1
	v_mfma_f32_16x16x32_f16 v[42:45], v[98:101], v[110:113], v[42:45]
	ds_read_b128 v[118:121], v138
	s_add_u32 s0, s6, s0
	s_addc_u32 s1, s7, s1
	v_mfma_f32_16x16x32_f16 v[50:53], v[102:105], v[110:113], v[50:53]
	ds_read_b128 v[122:125], v130 offset:16384
	s_lshl_b32 s3, s8, 1
	s_add_u32 s0, s0, s3
	v_mfma_f32_16x16x32_f16 v[46:49], v[106:109], v[110:113], v[46:49]
	ds_read_b128 v[110:113], v130 offset:18432
	s_addc_u32 s1, s1, 0
	v_lshlrev_b32_e32 v0, 1, v0
	v_mfma_f32_16x16x32_f16 v[54:57], v[90:93], v[94:97], v[54:57]
	ds_read_b128 v[126:129], v130 offset:20480
	v_cmp_gt_u32_e32 vcc, s2, v83
	v_mfma_f32_16x16x32_f16 v[58:61], v[98:101], v[94:97], v[58:61]
	ds_read_b128 v[130:133], v130 offset:22528
	v_mfma_f32_16x16x32_f16 v[62:65], v[102:105], v[94:97], v[62:65]
	ds_read_b128 v[134:137], v138 offset:2048
	v_mfma_f32_16x16x32_f16 v[66:69], v[106:109], v[94:97], v[66:69]
	ds_read_b128 v[94:97], v138 offset:4096
	s_waitcnt lgkmcnt(0)
	v_mfma_f32_16x16x32_f16 v[70:73], v[90:93], v[114:117], v[70:73]
	ds_read_b128 v[90:93], v138 offset:6144
	s_waitcnt vmcnt(0)
	s_barrier
	v_mfma_f32_16x16x32_f16 v[74:77], v[98:101], v[114:117], v[74:77]
	v_mfma_f32_16x16x32_f16 v[34:37], v[102:105], v[114:117], v[34:37]
	v_mfma_f32_16x16x32_f16 v[78:81], v[106:109], v[114:117], v[78:81]
	v_add_u32_e32 v106, v1, v87
	v_add_u32_e32 v87, v89, v87
	v_add_u32_e32 v1, v1, v85
	v_mfma_f32_16x16x32_f16 v[18:21], v[122:125], v[118:121], v[18:21]
	v_mfma_f32_16x16x32_f16 v[22:25], v[110:113], v[118:121], v[22:25]
	v_mfma_f32_16x16x32_f16 v[26:29], v[126:129], v[118:121], v[26:29]
	v_mfma_f32_16x16x32_f16 v[30:33], v[130:133], v[118:121], v[30:33]
	v_mfma_f32_16x16x32_f16 v[38:41], v[122:125], v[134:137], v[38:41]
	v_mfma_f32_16x16x32_f16 v[42:45], v[110:113], v[134:137], v[42:45]
	v_mfma_f32_16x16x32_f16 v[50:53], v[126:129], v[134:137], v[50:53]
	v_mfma_f32_16x16x32_f16 v[46:49], v[130:133], v[134:137], v[46:49]
	v_mfma_f32_16x16x32_f16 v[54:57], v[122:125], v[94:97], v[54:57]
	v_mfma_f32_16x16x32_f16 v[58:61], v[110:113], v[94:97], v[58:61]
	v_mfma_f32_16x16x32_f16 v[62:65], v[126:129], v[94:97], v[62:65]
	v_mfma_f32_16x16x32_f16 v[66:69], v[130:133], v[94:97], v[66:69]
	s_waitcnt lgkmcnt(0)
	v_mfma_f32_16x16x32_f16 v[70:73], v[122:125], v[90:93], v[70:73]
	v_mfma_f32_16x16x32_f16 v[74:77], v[110:113], v[90:93], v[74:77]
	v_mfma_f32_16x16x32_f16 v[34:37], v[126:129], v[90:93], v[34:37]
	v_mfma_f32_16x16x32_f16 v[78:81], v[130:133], v[90:93], v[78:81]
	ds_read_b128 v[90:93], v106 offset:16384
	ds_read_b128 v[98:101], v106 offset:18432
	ds_read_b128 v[94:97], v87
	s_waitcnt lgkmcnt(0)
	v_mfma_f32_16x16x32_f16 v[18:21], v[90:93], v[94:97], v[18:21]
	ds_read_b128 v[102:105], v106 offset:20480
	v_mfma_f32_16x16x32_f16 v[22:25], v[98:101], v[94:97], v[22:25]
	ds_read_b128 v[106:109], v106 offset:22528
	s_waitcnt lgkmcnt(0)
	v_mfma_f32_16x16x32_f16 v[26:29], v[102:105], v[94:97], v[26:29]
	ds_read_b128 v[110:113], v87 offset:2048
	v_mfma_f32_16x16x32_f16 v[30:33], v[106:109], v[94:97], v[30:33]
	ds_read_b128 v[94:97], v87 offset:4096
	s_waitcnt lgkmcnt(0)
	v_mfma_f32_16x16x32_f16 v[38:41], v[90:93], v[110:113], v[38:41]
	ds_read_b128 v[114:117], v87 offset:6144
	v_add_u32_e32 v87, v89, v85
	v_mfma_f32_16x16x32_f16 v[42:45], v[98:101], v[110:113], v[42:45]
	ds_read_b128 v[118:121], v87
	v_mfma_f32_16x16x32_f16 v[50:53], v[102:105], v[110:113], v[50:53]
	ds_read_b128 v[122:125], v1 offset:16384
	v_mfma_f32_16x16x32_f16 v[46:49], v[106:109], v[110:113], v[46:49]
	ds_read_b128 v[110:113], v1 offset:18432
	v_mfma_f32_16x16x32_f16 v[126:129], v[90:93], v[94:97], v[54:57]
	ds_read_b128 v[130:133], v1 offset:20480
	v_mfma_f32_16x16x32_f16 v[134:137], v[98:101], v[94:97], v[58:61]
	ds_read_b128 v[138:141], v1 offset:22528
	v_mov_b32_e32 v1, 0
	v_lshl_add_u64 v[0:1], s[0:1], 0, v[0:1]
	v_mfma_f32_16x16x32_f16 v[142:145], v[102:105], v[94:97], v[62:65]
	ds_read_b128 v[146:149], v87 offset:2048
	v_mfma_f32_16x16x32_f16 v[94:97], v[106:109], v[94:97], v[66:69]
	ds_read_b128 v[150:153], v87 offset:4096
	s_waitcnt lgkmcnt(0)
	v_mfma_f32_16x16x32_f16 v[90:93], v[90:93], v[114:117], v[70:73]
	ds_read_b128 v[154:157], v87 offset:6144
	v_mfma_f32_16x16x32_f16 v[98:101], v[98:101], v[114:117], v[74:77]
	v_mfma_f32_16x16x32_f16 v[102:105], v[102:105], v[114:117], v[34:37]
	v_mfma_f32_16x16x32_f16 v[106:109], v[106:109], v[114:117], v[78:81]
	v_mfma_f32_16x16x32_f16 v[78:81], v[122:125], v[118:121], v[18:21]
	v_mfma_f32_16x16x32_f16 v[74:77], v[110:113], v[118:121], v[22:25]
	v_mfma_f32_16x16x32_f16 v[70:73], v[130:133], v[118:121], v[26:29]
	v_mfma_f32_16x16x32_f16 v[66:69], v[138:141], v[118:121], v[30:33]
	v_mfma_f32_16x16x32_f16 v[62:65], v[122:125], v[146:149], v[38:41]
	v_mfma_f32_16x16x32_f16 v[58:61], v[110:113], v[146:149], v[42:45]
	v_mfma_f32_16x16x32_f16 v[54:57], v[130:133], v[146:149], v[50:53]
	v_mfma_f32_16x16x32_f16 v[50:53], v[138:141], v[146:149], v[46:49]
	v_mfma_f32_16x16x32_f16 v[46:49], v[122:125], v[150:153], v[126:129]
	v_mfma_f32_16x16x32_f16 v[42:45], v[110:113], v[150:153], v[134:137]
	v_mfma_f32_16x16x32_f16 v[38:41], v[130:133], v[150:153], v[142:145]
	v_mfma_f32_16x16x32_f16 v[34:37], v[138:141], v[150:153], v[94:97]
	s_waitcnt lgkmcnt(0)
	v_mfma_f32_16x16x32_f16 v[26:29], v[122:125], v[154:157], v[90:93]
	v_mfma_f32_16x16x32_f16 v[22:25], v[110:113], v[154:157], v[98:101]
	v_mfma_f32_16x16x32_f16 v[18:21], v[130:133], v[154:157], v[102:105]
	v_mfma_f32_16x16x32_f16 v[30:33], v[138:141], v[154:157], v[106:109]
	v_mbcnt_lo_u32_b32 v158, -1, 0
	v_mbcnt_hi_u32_b32 v158, -1, v158
	v_and_b32_e32 v159, 15, v158
	v_lshrrev_b32_e32 v160, 4, v158
	s_lshl_b32 s36, s23, 2
	s_add_u32 s36, s36, s22
	s_mulk_i32 s36, 0x900
	s_add_u32 s36, s36, 0x18000
	v_mul_u32_u24_e32 v161, 0x90, v159
	v_lshl_add_u32 v161, v160, 3, v161
	v_add_u32_e32 v161, s36, v161
	v_lshrrev_b32_e32 v162, 3, v158
	v_and_b32_e32 v163, 7, v158
	v_mul_u32_u24_e32 v164, 0x90, v162
	v_lshl_add_u32 v164, v163, 4, v164
	v_add_u32_e32 v164, s36, v164
	v_lshlrev_b32_e32 v165, 2, v162
	v_add_u32_e32 v166, 32, v165
	v_lshlrev_b32_e32 v182, 4, v163
	v_mov_b32_e32 v183, 0
	s_lshl_b32 s37, s23, 6
	v_add_u32_e32 v167, s37, v162
	s_mov_b64 s[0:1], exec
	s_cbranch_execz .LBB2_8
	s_waitcnt vmcnt(0)
	v_add_f32_e32 v79, v15, v79
	v_ashrrev_i32_e32 v89, 31, v88
	v_add_f32_e32 v78, v14, v78
	v_max_f32_e32 v85, 0, v79
	v_add_f32_e32 v79, v16, v80
	v_add_f32_e32 v80, v17, v81
	v_lshlrev_b64 v[88:89], 11, v[88:89]
	v_max_f32_e32 v78, 0, v78
	v_max_f32_e32 v79, 0, v79
	v_max_f32_e32 v80, 0, v80
	v_lshl_add_u64 v[88:89], v[0:1], 0, v[88:89]
	v_cvt_pk_f16_f32 v79, v79, v80
	v_cvt_pk_f16_f32 v78, v78, v85
	v_add_f32_e32 v75, v11, v75
	ds_write_b64 v161, v[78:79]
	v_add_f32_e32 v74, v10, v74
	v_max_f32_e32 v78, 0, v75
	v_add_f32_e32 v75, v12, v76
	v_add_f32_e32 v76, v13, v77
	v_max_f32_e32 v74, 0, v74
	v_max_f32_e32 v75, 0, v75
	v_max_f32_e32 v76, 0, v76
	v_cvt_pk_f16_f32 v75, v75, v76
	v_cvt_pk_f16_f32 v74, v74, v78
	v_add_f32_e32 v71, v7, v71
	ds_write_b64 v161, v[74:75] offset:32
	v_add_f32_e32 v70, v6, v70
	v_max_f32_e32 v74, 0, v71
	v_add_f32_e32 v71, v8, v72
	v_add_f32_e32 v72, v9, v73
	v_max_f32_e32 v70, 0, v70
	v_max_f32_e32 v71, 0, v71
	v_max_f32_e32 v72, 0, v72
	v_cvt_pk_f16_f32 v71, v71, v72
	v_cvt_pk_f16_f32 v70, v70, v74
	v_add_f32_e32 v67, v3, v67
	ds_write_b64 v161, v[70:71] offset:64
	v_add_f32_e32 v66, v2, v66
	v_max_f32_e32 v70, 0, v67
	v_add_f32_e32 v67, v4, v68
	v_add_f32_e32 v68, v5, v69
	v_max_f32_e32 v66, 0, v66
	v_max_f32_e32 v67, 0, v67
	v_max_f32_e32 v68, 0, v68
	v_cvt_pk_f16_f32 v67, v67, v68
	v_cvt_pk_f16_f32 v66, v66, v70
	ds_write_b64 v161, v[66:67] offset:96
	s_waitcnt lgkmcnt(0)
	ds_read_b128 v[170:173], v164
	ds_read_b128 v[174:177], v164 offset:1152
	ds_bpermute_b32 v178, v165, v88
	ds_bpermute_b32 v179, v165, v89
	ds_bpermute_b32 v180, v166, v88
	ds_bpermute_b32 v181, v166, v89
	v_add_u32_e32 v184, 0, v167
	v_cmp_gt_u32_e64 s[38:39], s2, v184
	v_add_u32_e32 v184, 8, v184
	v_cmp_gt_u32_e64 s[40:41], s2, v184
	s_waitcnt lgkmcnt(0)
	v_lshl_add_u64 v[178:179], v[178:179], 0, v[182:183]
	v_lshl_add_u64 v[180:181], v[180:181], 0, v[182:183]
	s_mov_b64 s[42:43], exec
	s_and_b64 exec, s[42:43], s[38:39]
	global_store_dwordx4 v[178:179], v[170:173], off sc1
	s_and_b64 exec, s[42:43], s[40:41]
	global_store_dwordx4 v[180:181], v[174:177], off sc1
	s_mov_b64 exec, s[42:43]
.LBB2_8:
	s_or_b64 exec, exec, s[0:1]
	v_or_b32_e32 v66, 16, v83
	v_cmp_gt_u32_e32 vcc, s2, v66
	s_mov_b64 s[0:1], exec
	s_cbranch_execz .LBB2_10
	s_waitcnt vmcnt(0)
	v_add_f32_e32 v63, v15, v63
	v_ashrrev_i32_e32 v87, 31, v86
	v_add_f32_e32 v62, v14, v62
	v_max_f32_e32 v68, 0, v63
	v_add_f32_e32 v63, v16, v64
	v_add_f32_e32 v64, v17, v65
	v_lshlrev_b64 v[66:67], 11, v[86:87]
	v_max_f32_e32 v62, 0, v62
	v_max_f32_e32 v63, 0, v63
	v_max_f32_e32 v64, 0, v64
	v_lshl_add_u64 v[66:67], v[0:1], 0, v[66:67]
	v_cvt_pk_f16_f32 v63, v63, v64
	v_cvt_pk_f16_f32 v62, v62, v68
	v_add_f32_e32 v59, v11, v59
	ds_write_b64 v161, v[62:63]
	v_add_f32_e32 v58, v10, v58
	v_max_f32_e32 v62, 0, v59
	v_add_f32_e32 v59, v12, v60
	v_add_f32_e32 v60, v13, v61
	v_max_f32_e32 v58, 0, v58
	v_max_f32_e32 v59, 0, v59
	v_max_f32_e32 v60, 0, v60
	v_cvt_pk_f16_f32 v59, v59, v60
	v_cvt_pk_f16_f32 v58, v58, v62
	v_add_f32_e32 v55, v7, v55
	ds_write_b64 v161, v[58:59] offset:32
	v_add_f32_e32 v54, v6, v54
	v_max_f32_e32 v58, 0, v55
	v_add_f32_e32 v55, v8, v56
	v_add_f32_e32 v56, v9, v57
	v_max_f32_e32 v54, 0, v54
	v_max_f32_e32 v55, 0, v55
	v_max_f32_e32 v56, 0, v56
	v_cvt_pk_f16_f32 v55, v55, v56
	v_cvt_pk_f16_f32 v54, v54, v58
	v_add_f32_e32 v51, v3, v51
	ds_write_b64 v161, v[54:55] offset:64
	v_add_f32_e32 v50, v2, v50
	v_max_f32_e32 v54, 0, v51
	v_add_f32_e32 v51, v4, v52
	v_add_f32_e32 v52, v5, v53
	v_max_f32_e32 v50, 0, v50
	v_max_f32_e32 v51, 0, v51
	v_max_f32_e32 v52, 0, v52
	v_cvt_pk_f16_f32 v51, v51, v52
	v_cvt_pk_f16_f32 v50, v50, v54
	ds_write_b64 v161, v[50:51] offset:96
	s_waitcnt lgkmcnt(0)
	ds_read_b128 v[170:173], v164
	ds_read_b128 v[174:177], v164 offset:1152
	ds_bpermute_b32 v178, v165, v66
	ds_bpermute_b32 v179, v165, v67
	ds_bpermute_b32 v180, v166, v66
	ds_bpermute_b32 v181, v166, v67
	v_add_u32_e32 v184, 16, v167
	v_cmp_gt_u32_e64 s[38:39], s2, v184
	v_add_u32_e32 v184, 8, v184
	v_cmp_gt_u32_e64 s[40:41], s2, v184
	s_waitcnt lgkmcnt(0)
	v_lshl_add_u64 v[178:179], v[178:179], 0, v[182:183]
	v_lshl_add_u64 v[180:181], v[180:181], 0, v[182:183]
	s_mov_b64 s[42:43], exec
	s_and_b64 exec, s[42:43], s[38:39]
	global_store_dwordx4 v[178:179], v[170:173], off sc1
	s_and_b64 exec, s[42:43], s[40:41]
	global_store_dwordx4 v[180:181], v[174:177], off sc1
	s_mov_b64 exec, s[42:43]
.LBB2_10:
	s_or_b64 exec, exec, s[0:1]
	v_or_b32_e32 v50, 32, v83
	v_cmp_gt_u32_e32 vcc, s2, v50
	s_mov_b64 s[0:1], exec
	s_cbranch_execz .LBB2_12
	s_waitcnt vmcnt(0)
	v_add_f32_e32 v47, v15, v47
	v_ashrrev_i32_e32 v85, 31, v84
	v_add_f32_e32 v46, v14, v46
	v_max_f32_e32 v52, 0, v47
	v_add_f32_e32 v47, v16, v48
	v_add_f32_e32 v48, v17, v49
	v_lshlrev_b64 v[50:51], 11, v[84:85]
	v_max_f32_e32 v46, 0, v46
	v_max_f32_e32 v47, 0, v47
	v_max_f32_e32 v48, 0, v48
	v_lshl_add_u64 v[50:51], v[0:1], 0, v[50:51]
	v_cvt_pk_f16_f32 v47, v47, v48
	v_cvt_pk_f16_f32 v46, v46, v52
	v_add_f32_e32 v43, v11, v43
	ds_write_b64 v161, v[46:47]
	v_add_f32_e32 v42, v10, v42
	v_max_f32_e32 v46, 0, v43
	v_add_f32_e32 v43, v12, v44
	v_add_f32_e32 v44, v13, v45
	v_max_f32_e32 v42, 0, v42
	v_max_f32_e32 v43, 0, v43
	v_max_f32_e32 v44, 0, v44
	v_cvt_pk_f16_f32 v43, v43, v44
	v_cvt_pk_f16_f32 v42, v42, v46
	v_add_f32_e32 v39, v7, v39
	ds_write_b64 v161, v[42:43] offset:32
	v_add_f32_e32 v38, v6, v38
	v_max_f32_e32 v42, 0, v39
	v_add_f32_e32 v39, v8, v40
	v_add_f32_e32 v40, v9, v41
	v_max_f32_e32 v38, 0, v38
	v_max_f32_e32 v39, 0, v39
	v_max_f32_e32 v40, 0, v40
	v_cvt_pk_f16_f32 v39, v39, v40
	v_cvt_pk_f16_f32 v38, v38, v42
	v_add_f32_e32 v35, v3, v35
	ds_write_b64 v161, v[38:39] offset:64
	v_add_f32_e32 v34, v2, v34
	v_max_f32_e32 v38, 0, v35
	v_add_f32_e32 v35, v4, v36
	v_add_f32_e32 v36, v5, v37
	v_max_f32_e32 v34, 0, v34
	v_max_f32_e32 v35, 0, v35
	v_max_f32_e32 v36, 0, v36
	v_cvt_pk_f16_f32 v35, v35, v36
	v_cvt_pk_f16_f32 v34, v34, v38
	ds_write_b64 v161, v[34:35] offset:96
	s_waitcnt lgkmcnt(0)
	ds_read_b128 v[170:173], v164
	ds_read_b128 v[174:177], v164 offset:1152
	ds_bpermute_b32 v178, v165, v50
	ds_bpermute_b32 v179, v165, v51
	ds_bpermute_b32 v180, v166, v50
	ds_bpermute_b32 v181, v166, v51
	v_add_u32_e32 v184, 32, v167
	v_cmp_gt_u32_e64 s[38:39], s2, v184
	v_add_u32_e32 v184, 8, v184
	v_cmp_gt_u32_e64 s[40:41], s2, v184
	s_waitcnt lgkmcnt(0)
	v_lshl_add_u64 v[178:179], v[178:179], 0, v[182:183]
	v_lshl_add_u64 v[180:181], v[180:181], 0, v[182:183]
	s_mov_b64 s[42:43], exec
	s_and_b64 exec, s[42:43], s[38:39]
	global_store_dwordx4 v[178:179], v[170:173], off sc1
	s_and_b64 exec, s[42:43], s[40:41]
	global_store_dwordx4 v[180:181], v[174:177], off sc1
	s_mov_b64 exec, s[42:43]
.LBB2_12:
	s_or_b64 exec, exec, s[0:1]
	v_or_b32_e32 v34, 48, v83
	v_cmp_gt_u32_e32 vcc, s2, v34
	s_mov_b64 s[0:1], exec
	s_cbranch_execz .LBB2_14
	s_waitcnt vmcnt(0)
	v_add_f32_e32 v15, v15, v27
	v_ashrrev_i32_e32 v83, 31, v82
	v_add_f32_e32 v14, v14, v26
	v_max_f32_e32 v26, 0, v15
	v_add_f32_e32 v15, v16, v28
	v_add_f32_e32 v16, v17, v29
	v_lshlrev_b64 v[34:35], 11, v[82:83]
	v_max_f32_e32 v14, 0, v14
	v_max_f32_e32 v15, 0, v15
	v_max_f32_e32 v16, 0, v16
	v_lshl_add_u64 v[0:1], v[0:1], 0, v[34:35]
	v_cvt_pk_f16_f32 v15, v15, v16
	v_cvt_pk_f16_f32 v14, v14, v26
	v_add_f32_e32 v11, v11, v23
	ds_write_b64 v161, v[14:15]
	v_add_f32_e32 v10, v10, v22
	v_max_f32_e32 v14, 0, v11
	v_add_f32_e32 v11, v12, v24
	v_add_f32_e32 v12, v13, v25
	v_max_f32_e32 v10, 0, v10
	v_max_f32_e32 v11, 0, v11
	v_max_f32_e32 v12, 0, v12
	v_cvt_pk_f16_f32 v11, v11, v12
	v_cvt_pk_f16_f32 v10, v10, v14
	v_add_f32_e32 v7, v7, v19
	ds_write_b64 v161, v[10:11] offset:32
	v_add_f32_e32 v6, v6, v18
	v_max_f32_e32 v10, 0, v7
	v_add_f32_e32 v7, v8, v20
	v_add_f32_e32 v8, v9, v21
	v_max_f32_e32 v6, 0, v6
	v_max_f32_e32 v7, 0, v7
	v_max_f32_e32 v8, 0, v8
	v_cvt_pk_f16_f32 v7, v7, v8
	v_cvt_pk_f16_f32 v6, v6, v10
	v_add_f32_e32 v3, v3, v31
	ds_write_b64 v161, v[6:7] offset:64
	v_add_f32_e32 v2, v2, v30
	v_max_f32_e32 v6, 0, v3
	v_add_f32_e32 v3, v4, v32
	v_add_f32_e32 v4, v5, v33
	v_max_f32_e32 v2, 0, v2
	v_max_f32_e32 v3, 0, v3
	v_max_f32_e32 v4, 0, v4
	v_cvt_pk_f16_f32 v3, v3, v4
	v_cvt_pk_f16_f32 v2, v2, v6
	ds_write_b64 v161, v[2:3] offset:96
	s_waitcnt lgkmcnt(0)
	ds_read_b128 v[170:173], v164
	ds_read_b128 v[174:177], v164 offset:1152
	ds_bpermute_b32 v178, v165, v0
	ds_bpermute_b32 v179, v165, v1
	ds_bpermute_b32 v180, v166, v0
	ds_bpermute_b32 v181, v166, v1
	v_add_u32_e32 v184, 48, v167
	v_cmp_gt_u32_e64 s[38:39], s2, v184
	v_add_u32_e32 v184, 8, v184
	v_cmp_gt_u32_e64 s[40:41], s2, v184
	s_waitcnt lgkmcnt(0)
	v_lshl_add_u64 v[178:179], v[178:179], 0, v[182:183]
	v_lshl_add_u64 v[180:181], v[180:181], 0, v[182:183]
	s_mov_b64 s[42:43], exec
	s_and_b64 exec, s[42:43], s[38:39]
	global_store_dwordx4 v[178:179], v[170:173], off sc1
	s_and_b64 exec, s[42:43], s[40:41]
	global_store_dwordx4 v[180:181], v[174:177], off sc1
	s_mov_b64 exec, s[42:43]

.LBB3_38:
	ds_read_b128 v[6:9], v196 offset:49152
	ds_read_b128 v[18:21], v196 offset:51200
	ds_read_b128 v[34:37], v194
	ds_read_b128 v[150:153], v194 offset:2048
	ds_read_b128 v[154:157], v196 offset:53248
	ds_read_b128 v[158:161], v196 offset:55296
	s_waitcnt vmcnt(6)
	v_pk_add_f16 v2, v30, v2
	s_waitcnt lgkmcnt(3)
	v_mfma_f32_16x16x32_f16 v[106:109], v[6:9], v[34:37], v[106:109]
	v_pk_add_f16 v3, v31, v3
	v_pk_add_f16 v4, v32, v4
	v_pk_add_f16 v5, v33, v5
	v_mfma_f32_16x16x32_f16 v[102:105], v[18:21], v[34:37], v[102:105]
	v_cndmask_b32_e64 v5, v33, v5, s[2:3]
	v_cndmask_b32_e64 v4, v32, v4, s[2:3]
	v_cndmask_b32_e64 v3, v31, v3, s[2:3]
	s_waitcnt lgkmcnt(1)
	v_mfma_f32_16x16x32_f16 v[98:101], v[154:157], v[34:37], v[98:101]
	v_cndmask_b32_e64 v2, v30, v2, s[2:3]
	v_cmp_gt_u32_e32 vcc, s18, v184
	s_waitcnt lgkmcnt(0)
	v_mfma_f32_16x16x32_f16 v[34:37], v[158:161], v[34:37], v[94:97]
	v_mfma_f32_16x16x32_f16 v[90:93], v[6:9], v[150:153], v[90:93]
	v_mfma_f32_16x16x32_f16 v[86:89], v[18:21], v[150:153], v[86:89]
	v_mfma_f32_16x16x32_f16 v[82:85], v[154:157], v[150:153], v[82:85]
	v_mfma_f32_16x16x32_f16 v[78:81], v[158:161], v[150:153], v[78:81]
	ds_read_b128 v[94:97], v194 offset:4096
	ds_read_b128 v[150:153], v194 offset:6144
	s_waitcnt lgkmcnt(1)
	v_mfma_f32_16x16x32_f16 v[62:65], v[6:9], v[94:97], v[62:65]
	v_mfma_f32_16x16x32_f16 v[58:61], v[18:21], v[94:97], v[58:61]
	v_mfma_f32_16x16x32_f16 v[54:57], v[154:157], v[94:97], v[54:57]
	v_mfma_f32_16x16x32_f16 v[74:77], v[158:161], v[94:97], v[74:77]
	s_waitcnt lgkmcnt(0)
	v_mfma_f32_16x16x32_f16 v[66:69], v[6:9], v[150:153], v[66:69]
	v_mfma_f32_16x16x32_f16 v[70:73], v[18:21], v[150:153], v[70:73]
	v_mfma_f32_16x16x32_f16 v[94:97], v[154:157], v[150:153], v[110:113]
	v_mfma_f32_16x16x32_f16 v[110:113], v[158:161], v[150:153], v[114:117]
	s_nop 2
	ds_read_b128 v[114:117], v194 offset:8192
	ds_read_b128 v[150:153], v194 offset:10240
	s_waitcnt lgkmcnt(1)
	v_mfma_f32_16x16x32_f16 v[118:121], v[6:9], v[114:117], v[118:121]
	v_mfma_f32_16x16x32_f16 v[122:125], v[18:21], v[114:117], v[122:125]
	v_mfma_f32_16x16x32_f16 v[126:129], v[154:157], v[114:117], v[126:129]
	v_mfma_f32_16x16x32_f16 v[114:117], v[158:161], v[114:117], v[130:133]
	s_waitcnt lgkmcnt(0)
	v_mfma_f32_16x16x32_f16 v[6:9], v[6:9], v[150:153], v[134:137]
	v_mfma_f32_16x16x32_f16 v[18:21], v[18:21], v[150:153], v[138:141]
	s_nop 1
	ds_read_b128 v[134:137], v197 offset:49152
	v_mfma_f32_16x16x32_f16 v[130:133], v[154:157], v[150:153], v[146:149]
	v_mfma_f32_16x16x32_f16 v[138:141], v[158:161], v[150:153], v[142:145]
	s_nop 2
	ds_read_b128 v[142:145], v197 offset:51200
	ds_read_b128 v[146:149], v195
	ds_read_b128 v[150:153], v195 offset:2048
	ds_read_b128 v[154:157], v197 offset:53248
	ds_read_b128 v[158:161], v197 offset:55296
	s_waitcnt lgkmcnt(3)
	v_mfma_f32_16x16x32_f16 v[106:109], v[134:137], v[146:149], v[106:109]
	v_mfma_f32_16x16x32_f16 v[102:105], v[142:145], v[146:149], v[102:105]
	s_waitcnt lgkmcnt(1)
	v_mfma_f32_16x16x32_f16 v[98:101], v[154:157], v[146:149], v[98:101]
	s_waitcnt lgkmcnt(0)
	v_mfma_f32_16x16x32_f16 v[34:37], v[158:161], v[146:149], v[34:37]
	v_mfma_f32_16x16x32_f16 v[90:93], v[134:137], v[150:153], v[90:93]
	v_mfma_f32_16x16x32_f16 v[86:89], v[142:145], v[150:153], v[86:89]
	v_mfma_f32_16x16x32_f16 v[82:85], v[154:157], v[150:153], v[82:85]
	v_mfma_f32_16x16x32_f16 v[78:81], v[158:161], v[150:153], v[78:81]
	ds_read_b128 v[146:149], v195 offset:4096
	ds_read_b128 v[150:153], v195 offset:6144
	s_waitcnt lgkmcnt(1)
	v_mfma_f32_16x16x32_f16 v[62:65], v[134:137], v[146:149], v[62:65]
	v_mfma_f32_16x16x32_f16 v[58:61], v[142:145], v[146:149], v[58:61]
	v_mfma_f32_16x16x32_f16 v[54:57], v[154:157], v[146:149], v[54:57]
	v_mfma_f32_16x16x32_f16 v[74:77], v[158:161], v[146:149], v[74:77]
	s_waitcnt lgkmcnt(0)
	v_mfma_f32_16x16x32_f16 v[66:69], v[134:137], v[150:153], v[66:69]
	v_mfma_f32_16x16x32_f16 v[70:73], v[142:145], v[150:153], v[70:73]
	v_mfma_f32_16x16x32_f16 v[94:97], v[154:157], v[150:153], v[94:97]
	v_mfma_f32_16x16x32_f16 v[110:113], v[158:161], v[150:153], v[110:113]
	ds_read_b128 v[146:149], v195 offset:8192
	ds_read_b128 v[150:153], v195 offset:10240
	ds_write_b128 v187, v[2:5] offset:24576
	s_waitcnt vmcnt(5)
	v_pk_add_f16 v2, v26, v10
	v_pk_add_f16 v3, v27, v11
	v_pk_add_f16 v4, v28, v12
	v_pk_add_f16 v5, v29, v13
	v_cndmask_b32_e64 v4, v28, v4, s[2:3]
	v_cndmask_b32_e64 v5, v29, v5, s[2:3]
	v_cndmask_b32_e64 v3, v27, v3, s[2:3]
	v_cndmask_b32_e64 v2, v26, v2, s[2:3]
	ds_write_b128 v187, v[2:5] offset:32768
	s_waitcnt vmcnt(4)
	v_pk_add_f16 v2, v22, v14
	v_pk_add_f16 v3, v23, v15
	v_pk_add_f16 v4, v24, v16
	v_pk_add_f16 v5, v25, v17
	v_cndmask_b32_e64 v4, v24, v4, s[2:3]
	v_cndmask_b32_e64 v5, v25, v5, s[2:3]
	v_cndmask_b32_e64 v3, v23, v3, s[2:3]
	v_cndmask_b32_e64 v2, v22, v2, s[2:3]
	s_waitcnt lgkmcnt(3)
	v_mfma_f32_16x16x32_f16 v[118:121], v[134:137], v[146:149], v[118:121]
	s_lshl_b32 s2, s15, 12
	s_add_u32 s4, s12, s2
	s_addc_u32 s5, s13, 0
	s_waitcnt lgkmcnt(2)
	v_mfma_f32_16x16x32_f16 v[6:9], v[134:137], v[150:153], v[6:9]
	v_add_u32_e32 v134, 0x14000, v187
	ds_write_b128 v187, v[2:5] offset:40960
	s_waitcnt vmcnt(3)
	ds_write_b128 v134, v[38:41]
	s_waitcnt vmcnt(2)
	ds_write_b128 v134, v[42:45] offset:8192
	s_waitcnt vmcnt(1)
	ds_write_b128 v134, v[46:49] offset:16384
	s_waitcnt vmcnt(0)
	ds_write_b128 v134, v[50:53] offset:24576
	s_waitcnt lgkmcnt(0)
	s_barrier
	ds_read_b128 v[2:5], v176 offset:32768
	ds_read_b128 v[14:17], v176 offset:34816
	ds_read_b128 v[22:25], v194 offset:24576
	ds_read_b128 v[26:29], v194 offset:26624
	ds_read_b128 v[38:41], v176 offset:36864
	ds_read_b128 v[46:49], v176 offset:38912
	s_waitcnt lgkmcnt(3)
	v_mfma_f32_16x16x32_f16 v[30:33], v[2:5], v[22:25], v[106:109]
	s_ashr_i32 s15, s14, 31
	s_lshl_b64 s[2:3], s[14:15], 2
	s_add_u32 s2, s4, s2
	v_mfma_f32_16x16x32_f16 v[42:45], v[14:17], v[22:25], v[102:105]
	s_addc_u32 s3, s5, s3
	s_waitcnt lgkmcnt(1)
	v_mfma_f32_16x16x32_f16 v[50:53], v[38:41], v[22:25], v[98:101]
	s_waitcnt lgkmcnt(0)
	v_mfma_f32_16x16x32_f16 v[22:25], v[46:49], v[22:25], v[34:37]
	v_mfma_f32_16x16x32_f16 v[34:37], v[2:5], v[26:29], v[90:93]
	v_mfma_f32_16x16x32_f16 v[86:89], v[14:17], v[26:29], v[86:89]
	v_mfma_f32_16x16x32_f16 v[82:85], v[38:41], v[26:29], v[82:85]
	v_mfma_f32_16x16x32_f16 v[26:29], v[46:49], v[26:29], v[78:81]
	s_nop 2
	ds_read_b128 v[78:81], v194 offset:28672
	ds_read_b128 v[90:93], v194 offset:30720
	v_mfma_f32_16x16x32_f16 v[122:125], v[142:145], v[146:149], v[122:125]
	v_mfma_f32_16x16x32_f16 v[18:21], v[142:145], v[150:153], v[18:21]
	v_mfma_f32_16x16x32_f16 v[10:13], v[158:161], v[150:153], v[138:141]
	s_waitcnt lgkmcnt(0)
	v_mfma_f32_16x16x32_f16 v[138:141], v[2:5], v[90:93], v[66:69]
	v_mfma_f32_16x16x32_f16 v[142:145], v[14:17], v[90:93], v[70:73]
	s_nop 1
	ds_read_b128 v[66:69], v194 offset:32768
	ds_read_b128 v[70:73], v194 offset:34816
	v_mfma_f32_16x16x32_f16 v[126:129], v[154:157], v[146:149], v[126:129]
	v_mfma_f32_16x16x32_f16 v[130:133], v[154:157], v[150:153], v[130:133]
	v_mfma_f32_16x16x32_f16 v[114:117], v[158:161], v[146:149], v[114:117]
	v_mfma_f32_16x16x32_f16 v[62:65], v[2:5], v[78:81], v[62:65]
	v_mfma_f32_16x16x32_f16 v[58:61], v[14:17], v[78:81], v[58:61]
	v_mfma_f32_16x16x32_f16 v[54:57], v[38:41], v[78:81], v[54:57]
	v_mfma_f32_16x16x32_f16 v[146:149], v[38:41], v[90:93], v[94:97]
	s_waitcnt lgkmcnt(1)
	v_mfma_f32_16x16x32_f16 v[118:121], v[2:5], v[66:69], v[118:121]
	v_mfma_f32_16x16x32_f16 v[154:157], v[14:17], v[66:69], v[122:125]
	v_mfma_f32_16x16x32_f16 v[158:161], v[38:41], v[66:69], v[126:129]
	s_waitcnt lgkmcnt(0)
	v_mfma_f32_16x16x32_f16 v[2:5], v[2:5], v[70:73], v[6:9]
	s_nop 0
	v_lshlrev_b32_e32 v126, 2, v184
	v_mov_b32_e32 v129, 0
	v_lshlrev_b32_e32 v128, 8, v186
	v_mfma_f32_16x16x32_f16 v[14:17], v[14:17], v[70:73], v[18:21]
	ds_read_b128 v[6:9], v162 offset:32768
	v_mfma_f32_16x16x32_f16 v[130:133], v[38:41], v[70:73], v[130:133]
	ds_read_b128 v[168:171], v162 offset:34816
	ds_read_b128 v[18:21], v195 offset:24576
	ds_read_b128 v[38:41], v195 offset:26624
	ds_read_b128 v[172:175], v162 offset:36864
	ds_read_b128 v[176:179], v162 offset:38912
	v_mfma_f32_16x16x32_f16 v[134:137], v[46:49], v[78:81], v[74:77]
	v_mfma_f32_16x16x32_f16 v[150:153], v[46:49], v[90:93], v[110:113]
	s_waitcnt lgkmcnt(3)
	v_mfma_f32_16x16x32_f16 v[110:113], v[6:9], v[18:21], v[30:33]
	v_mfma_f32_16x16x32_f16 v[106:109], v[168:171], v[18:21], v[42:45]
	s_waitcnt lgkmcnt(1)
	v_mfma_f32_16x16x32_f16 v[102:105], v[172:175], v[18:21], v[50:53]
	s_waitcnt lgkmcnt(0)
	v_mfma_f32_16x16x32_f16 v[98:101], v[176:179], v[18:21], v[22:25]
	ds_read_b128 v[18:21], v195 offset:28672
	s_nop 1
	ds_read_b128 v[22:25], v195 offset:30720
	v_mfma_f32_16x16x32_f16 v[164:167], v[46:49], v[66:69], v[114:117]
	v_mfma_f32_16x16x32_f16 v[10:13], v[46:49], v[70:73], v[10:13]
	s_waitcnt lgkmcnt(1)
	v_mfma_f32_16x16x32_f16 v[78:81], v[6:9], v[18:21], v[62:65]
	v_mfma_f32_16x16x32_f16 v[74:77], v[168:171], v[18:21], v[58:61]
	v_mfma_f32_16x16x32_f16 v[70:73], v[172:175], v[18:21], v[54:57]
	v_mfma_f32_16x16x32_f16 v[66:69], v[176:179], v[18:21], v[134:137]
	ds_read_b128 v[18:21], v195 offset:32768
	s_nop 1
	ds_read_b128 v[134:137], v195 offset:34816
	s_waitcnt lgkmcnt(1)
	v_mfma_f32_16x16x32_f16 v[46:49], v[6:9], v[18:21], v[118:121]
	global_load_dword v124, v126, s[6:7] offset:64
	global_load_dword v122, v126, s[6:7] offset:128
	s_nop 0
	global_load_dword v120, v126, s[6:7] offset:192
	global_load_dword v118, v126, s[6:7] offset:256
	global_load_dword v114, v126, s[6:7] offset:320
	v_mfma_f32_16x16x32_f16 v[62:65], v[6:9], v[22:25], v[138:141]
	v_mfma_f32_16x16x32_f16 v[58:61], v[168:171], v[22:25], v[142:145]
	v_mfma_f32_16x16x32_f16 v[54:57], v[172:175], v[22:25], v[146:149]
	v_mfma_f32_16x16x32_f16 v[50:53], v[176:179], v[22:25], v[150:153]
	v_lshl_add_u64 v[22:23], s[2:3], 0, v[128:129]
	v_lshlrev_b32_e32 v128, 4, v185
	v_lshl_add_u64 v[22:23], v[22:23], 0, v[128:129]
	v_mfma_f32_16x16x32_f16 v[94:97], v[6:9], v[38:41], v[34:37]
	s_lshl_b64 s[2:3], s[14:15], 1
	s_add_u32 s2, s10, s2
	s_addc_u32 s3, s11, s3
	v_mfma_f32_16x16x32_f16 v[90:93], v[168:171], v[38:41], v[86:89]
	v_lshlrev_b32_e32 v128, 7, v186
	v_lshl_add_u64 v[116:117], s[2:3], 0, v[128:129]
	v_lshlrev_b32_e32 v128, 3, v185
	v_mfma_f32_16x16x32_f16 v[86:89], v[172:175], v[38:41], v[82:85]
	v_lshl_add_u64 v[116:117], v[116:117], 0, v[128:129]
	v_mfma_f32_16x16x32_f16 v[82:85], v[176:179], v[38:41], v[26:29]
	v_mfma_f32_16x16x32_f16 v[42:45], v[168:171], v[18:21], v[154:157]
	v_mfma_f32_16x16x32_f16 v[38:41], v[172:175], v[18:21], v[158:161]
	v_mfma_f32_16x16x32_f16 v[34:37], v[176:179], v[18:21], v[164:167]
	global_load_dwordx4 v[26:29], v[22:23], off
	global_load_dwordx4 v[18:21], v[22:23], off offset:64
	s_waitcnt lgkmcnt(0)
	v_mfma_f32_16x16x32_f16 v[30:33], v[6:9], v[134:137], v[2:5]
	global_load_dwordx4 v[6:9], v[22:23], off offset:128
	s_nop 1
	global_load_dwordx4 v[2:5], v[22:23], off offset:192
	v_mfma_f32_16x16x32_f16 v[22:25], v[168:171], v[134:137], v[14:17]
	v_mfma_f32_16x16x32_f16 v[14:17], v[172:175], v[134:137], v[130:133]
	v_mfma_f32_16x16x32_f16 v[10:13], v[176:179], v[134:137], v[10:13]
	v_mbcnt_lo_u32_b32 v196, -1, 0
	v_mbcnt_hi_u32_b32 v196, -1, v196
	v_and_b32_e32 v197, 15, v196
	v_lshrrev_b32_e32 v198, 4, v196
	v_lshrrev_b32_e32 v222, 10, v187
	s_nop 0
	v_readfirstlane_b32 s36, v222
	s_nop 3
	s_and_b32 s36, s36, 7
	s_mulk_i32 s36, 0x900
	v_mul_u32_u24_e32 v199, 0x90, v197
	v_lshl_add_u32 v199, v198, 3, v199
	v_add_u32_e32 v199, s36, v199
	v_lshrrev_b32_e32 v200, 3, v196
	v_and_b32_e32 v201, 7, v196
	v_mul_u32_u24_e32 v202, 0x90, v200
	v_lshl_add_u32 v202, v201, 4, v202
	v_add_u32_e32 v202, s36, v202
	v_lshlrev_b32_e32 v203, 2, v200
	v_add_u32_e32 v204, 32, v203
	v_lshlrev_b32_e32 v220, 4, v201
	v_mov_b32_e32 v221, 0
	v_sub_u32_e32 v205, v184, v197
	v_add_u32_e32 v205, v205, v200
	s_mov_b64 s[2:3], exec
	s_cbranch_execz .LBB3_40
	v_mov_b32_e32 v127, v129
	v_lshl_add_u64 v[126:127], s[6:7], 0, v[126:127]
	global_load_dword v126, v[126:127], off
	s_waitcnt vmcnt(3)
	v_add_f32_e32 v106, v106, v18
	v_add_f32_e32 v107, v107, v19
	v_add_f32_e32 v110, v110, v26
	v_add_f32_e32 v111, v111, v27
	v_add_f32_e32 v112, v112, v28
	v_add_f32_e32 v113, v113, v29
	s_waitcnt vmcnt(2)
	v_add_f32_e32 v103, v103, v7
	v_add_f32_e32 v104, v104, v8
	v_add_f32_e32 v105, v105, v9
	s_waitcnt vmcnt(1)
	v_add_f32_e32 v100, v100, v4
	v_max_f32_e32 v106, 0, v106
	v_max_f32_e32 v107, 0, v107
	v_add_f32_e32 v108, v108, v20
	v_add_f32_e32 v109, v109, v21
	v_add_f32_e32 v102, v102, v6
	v_add_f32_e32 v98, v98, v2
	v_add_f32_e32 v99, v99, v3
	v_add_f32_e32 v101, v101, v5
	v_max_f32_e32 v110, 0, v110
	v_max_f32_e32 v111, 0, v111
	v_max_f32_e32 v112, 0, v112
	v_max_f32_e32 v113, 0, v113
	v_max_f32_e32 v115, 0, v103
	v_max_f32_e32 v103, 0, v104
	v_max_f32_e32 v104, 0, v105
	v_max_f32_e32 v105, 0, v100
	v_cvt_pk_f16_f32 v100, v106, v107
	v_max_f32_e32 v108, 0, v108
	v_max_f32_e32 v109, 0, v109
	v_max_f32_e32 v102, 0, v102
	v_max_f32_e32 v119, 0, v98
	v_max_f32_e32 v121, 0, v99
	v_max_f32_e32 v123, 0, v101
	v_cvt_pk_f16_f32 v99, v112, v113
	v_cvt_pk_f16_f32 v98, v110, v111
	v_cvt_pk_f16_f32 v101, v108, v109
	v_cvt_pk_f16_f32 v103, v103, v104
	v_cvt_pk_f16_f32 v102, v102, v115
	v_cvt_pk_f16_f32 v105, v105, v123
	v_cvt_pk_f16_f32 v104, v119, v121
	s_waitcnt vmcnt(0)
	v_ashrrev_i32_e32 v127, 31, v126
	v_lshlrev_b64 v[106:107], 11, v[126:127]
	v_lshl_add_u64 v[106:107], v[116:117], 0, v[106:107]
	ds_write_b64 v199, v[98:99]
	ds_write_b64 v199, v[100:101] offset:32
	ds_write_b64 v199, v[102:103] offset:64
	ds_write_b64 v199, v[104:105] offset:96
	s_waitcnt lgkmcnt(0)
	ds_read_b128 v[208:211], v202
	ds_read_b128 v[212:215], v202 offset:1152
	ds_bpermute_b32 v216, v203, v106
	ds_bpermute_b32 v217, v203, v107
	ds_bpermute_b32 v218, v204, v106
	ds_bpermute_b32 v219, v204, v107
	v_add_u32_e32 v222, 0, v205
	v_cmp_gt_u32_e64 s[38:39], s18, v222
	v_add_u32_e32 v222, 8, v222
	v_cmp_gt_u32_e64 s[40:41], s18, v222
	s_waitcnt lgkmcnt(0)
	v_lshl_add_u64 v[216:217], v[216:217], 0, v[220:221]
	v_lshl_add_u64 v[218:219], v[218:219], 0, v[220:221]
	s_mov_b64 s[42:43], exec
	s_and_b64 exec, s[42:43], s[38:39]
	global_store_dwordx4 v[216:217], v[208:211], off sc1
	s_and_b64 exec, s[42:43], s[40:41]
	global_store_dwordx4 v[218:219], v[212:215], off sc1
	s_mov_b64 exec, s[42:43]
.LBB3_40:
	s_or_b64 exec, exec, s[2:3]
	v_or_b32_e32 v98, 16, v184
	v_cmp_gt_u32_e32 vcc, s18, v98
	s_mov_b64 s[2:3], exec
	s_cbranch_execz .LBB3_42
	s_waitcnt vmcnt(3)
	v_add_f32_e32 v95, v95, v27
	v_ashrrev_i32_e32 v125, 31, v124
	v_add_f32_e32 v94, v94, v26
	v_max_f32_e32 v100, 0, v95
	v_add_f32_e32 v95, v96, v28
	v_add_f32_e32 v96, v97, v29
	v_lshlrev_b64 v[98:99], 11, v[124:125]
	v_max_f32_e32 v94, 0, v94
	v_max_f32_e32 v95, 0, v95
	v_max_f32_e32 v96, 0, v96
	v_lshl_add_u64 v[98:99], v[116:117], 0, v[98:99]
	v_cvt_pk_f16_f32 v95, v95, v96
	v_cvt_pk_f16_f32 v94, v94, v100
	s_waitcnt vmcnt(2)
	v_add_f32_e32 v91, v91, v19
	ds_write_b64 v199, v[94:95]
	v_add_f32_e32 v90, v90, v18
	v_max_f32_e32 v94, 0, v91
	v_add_f32_e32 v91, v92, v20
	v_add_f32_e32 v92, v93, v21
	v_max_f32_e32 v90, 0, v90
	v_max_f32_e32 v91, 0, v91
	v_max_f32_e32 v92, 0, v92
	v_cvt_pk_f16_f32 v91, v91, v92
	v_cvt_pk_f16_f32 v90, v90, v94
	s_waitcnt vmcnt(2)
	v_add_f32_e32 v87, v87, v7
	ds_write_b64 v199, v[90:91] offset:32
	v_add_f32_e32 v86, v86, v6
	v_max_f32_e32 v90, 0, v87
	v_add_f32_e32 v87, v88, v8
	v_add_f32_e32 v88, v89, v9
	v_max_f32_e32 v86, 0, v86
	v_max_f32_e32 v87, 0, v87
	v_max_f32_e32 v88, 0, v88
	v_cvt_pk_f16_f32 v87, v87, v88
	v_cvt_pk_f16_f32 v86, v86, v90
	s_waitcnt vmcnt(2)
	v_add_f32_e32 v83, v83, v3
	ds_write_b64 v199, v[86:87] offset:64
	v_add_f32_e32 v82, v82, v2
	v_max_f32_e32 v86, 0, v83
	v_add_f32_e32 v83, v84, v4
	v_add_f32_e32 v84, v85, v5
	v_max_f32_e32 v82, 0, v82
	v_max_f32_e32 v83, 0, v83
	v_max_f32_e32 v84, 0, v84
	v_cvt_pk_f16_f32 v83, v83, v84
	v_cvt_pk_f16_f32 v82, v82, v86
	ds_write_b64 v199, v[82:83] offset:96
	s_waitcnt lgkmcnt(0)
	ds_read_b128 v[208:211], v202
	ds_read_b128 v[212:215], v202 offset:1152
	ds_bpermute_b32 v216, v203, v98
	ds_bpermute_b32 v217, v203, v99
	ds_bpermute_b32 v218, v204, v98
	ds_bpermute_b32 v219, v204, v99
	v_add_u32_e32 v222, 16, v205
	v_cmp_gt_u32_e64 s[38:39], s18, v222
	v_add_u32_e32 v222, 8, v222
	v_cmp_gt_u32_e64 s[40:41], s18, v222
	s_waitcnt lgkmcnt(0)
	v_lshl_add_u64 v[216:217], v[216:217], 0, v[220:221]
	v_lshl_add_u64 v[218:219], v[218:219], 0, v[220:221]
	s_mov_b64 s[42:43], exec
	s_and_b64 exec, s[42:43], s[38:39]
	global_store_dwordx4 v[216:217], v[208:211], off sc1
	s_and_b64 exec, s[42:43], s[40:41]
	global_store_dwordx4 v[218:219], v[212:215], off sc1
	s_mov_b64 exec, s[42:43]
.LBB3_42:
	s_or_b64 exec, exec, s[2:3]
	v_add_u32_e32 v82, 32, v184
	v_cmp_gt_u32_e32 vcc, s18, v82
	s_mov_b64 s[2:3], exec
	s_cbranch_execz .LBB3_44
	s_waitcnt vmcnt(3)
	v_add_f32_e32 v79, v79, v27
	v_ashrrev_i32_e32 v123, 31, v122
	v_add_f32_e32 v78, v78, v26
	v_max_f32_e32 v84, 0, v79
	v_add_f32_e32 v79, v80, v28
	v_add_f32_e32 v80, v81, v29
	v_lshlrev_b64 v[82:83], 11, v[122:123]
	v_max_f32_e32 v78, 0, v78
	v_max_f32_e32 v79, 0, v79
	v_max_f32_e32 v80, 0, v80
	v_lshl_add_u64 v[82:83], v[116:117], 0, v[82:83]
	v_cvt_pk_f16_f32 v79, v79, v80
	v_cvt_pk_f16_f32 v78, v78, v84
	s_waitcnt vmcnt(2)
	v_add_f32_e32 v75, v75, v19
	ds_write_b64 v199, v[78:79]
	v_add_f32_e32 v74, v74, v18
	v_max_f32_e32 v78, 0, v75
	v_add_f32_e32 v75, v76, v20
	v_add_f32_e32 v76, v77, v21
	v_max_f32_e32 v74, 0, v74
	v_max_f32_e32 v75, 0, v75
	v_max_f32_e32 v76, 0, v76
	v_cvt_pk_f16_f32 v75, v75, v76
	v_cvt_pk_f16_f32 v74, v74, v78
	s_waitcnt vmcnt(2)
	v_add_f32_e32 v71, v71, v7
	ds_write_b64 v199, v[74:75] offset:32
	v_add_f32_e32 v70, v70, v6
	v_max_f32_e32 v74, 0, v71
	v_add_f32_e32 v71, v72, v8
	v_add_f32_e32 v72, v73, v9
	v_max_f32_e32 v70, 0, v70
	v_max_f32_e32 v71, 0, v71
	v_max_f32_e32 v72, 0, v72
	v_cvt_pk_f16_f32 v71, v71, v72
	v_cvt_pk_f16_f32 v70, v70, v74
	s_waitcnt vmcnt(2)
	v_add_f32_e32 v67, v67, v3
	ds_write_b64 v199, v[70:71] offset:64
	v_add_f32_e32 v66, v66, v2
	v_max_f32_e32 v70, 0, v67
	v_add_f32_e32 v67, v68, v4
	v_add_f32_e32 v68, v69, v5
	v_max_f32_e32 v66, 0, v66
	v_max_f32_e32 v67, 0, v67
	v_max_f32_e32 v68, 0, v68
	v_cvt_pk_f16_f32 v67, v67, v68
	v_cvt_pk_f16_f32 v66, v66, v70
	ds_write_b64 v199, v[66:67] offset:96
	s_waitcnt lgkmcnt(0)
	ds_read_b128 v[208:211], v202
	ds_read_b128 v[212:215], v202 offset:1152
	ds_bpermute_b32 v216, v203, v82
	ds_bpermute_b32 v217, v203, v83
	ds_bpermute_b32 v218, v204, v82
	ds_bpermute_b32 v219, v204, v83
	v_add_u32_e32 v222, 32, v205
	v_cmp_gt_u32_e64 s[38:39], s18, v222
	v_add_u32_e32 v222, 8, v222
	v_cmp_gt_u32_e64 s[40:41], s18, v222
	s_waitcnt lgkmcnt(0)
	v_lshl_add_u64 v[216:217], v[216:217], 0, v[220:221]
	v_lshl_add_u64 v[218:219], v[218:219], 0, v[220:221]
	s_mov_b64 s[42:43], exec
	s_and_b64 exec, s[42:43], s[38:39]
	global_store_dwordx4 v[216:217], v[208:211], off sc1
	s_and_b64 exec, s[42:43], s[40:41]
	global_store_dwordx4 v[218:219], v[212:215], off sc1
	s_mov_b64 exec, s[42:43]
.LBB3_44:
	s_or_b64 exec, exec, s[2:3]
	v_add_u32_e32 v66, 48, v184
	v_cmp_gt_u32_e32 vcc, s18, v66
	s_mov_b64 s[2:3], exec
	s_cbranch_execz .LBB3_46
	s_waitcnt vmcnt(3)
	v_add_f32_e32 v63, v63, v27
	v_ashrrev_i32_e32 v121, 31, v120
	v_add_f32_e32 v62, v62, v26
	v_max_f32_e32 v68, 0, v63
	v_add_f32_e32 v63, v64, v28
	v_add_f32_e32 v64, v65, v29
	v_lshlrev_b64 v[66:67], 11, v[120:121]
	v_max_f32_e32 v62, 0, v62
	v_max_f32_e32 v63, 0, v63
	v_max_f32_e32 v64, 0, v64
	v_lshl_add_u64 v[66:67], v[116:117], 0, v[66:67]
	v_cvt_pk_f16_f32 v63, v63, v64
	v_cvt_pk_f16_f32 v62, v62, v68
	s_waitcnt vmcnt(2)
	v_add_f32_e32 v59, v59, v19
	ds_write_b64 v199, v[62:63]
	v_add_f32_e32 v58, v58, v18
	v_max_f32_e32 v62, 0, v59
	v_add_f32_e32 v59, v60, v20
	v_add_f32_e32 v60, v61, v21
	v_max_f32_e32 v58, 0, v58
	v_max_f32_e32 v59, 0, v59
	v_max_f32_e32 v60, 0, v60
	v_cvt_pk_f16_f32 v59, v59, v60
	v_cvt_pk_f16_f32 v58, v58, v62
	s_waitcnt vmcnt(2)
	v_add_f32_e32 v55, v55, v7
	ds_write_b64 v199, v[58:59] offset:32
	v_add_f32_e32 v54, v54, v6
	v_max_f32_e32 v58, 0, v55
	v_add_f32_e32 v55, v56, v8
	v_add_f32_e32 v56, v57, v9
	v_max_f32_e32 v54, 0, v54
	v_max_f32_e32 v55, 0, v55
	v_max_f32_e32 v56, 0, v56
	v_cvt_pk_f16_f32 v55, v55, v56
	v_cvt_pk_f16_f32 v54, v54, v58
	s_waitcnt vmcnt(2)
	v_add_f32_e32 v51, v51, v3
	ds_write_b64 v199, v[54:55] offset:64
	v_add_f32_e32 v50, v50, v2
	v_max_f32_e32 v54, 0, v51
	v_add_f32_e32 v51, v52, v4
	v_add_f32_e32 v52, v53, v5
	v_max_f32_e32 v50, 0, v50
	v_max_f32_e32 v51, 0, v51
	v_max_f32_e32 v52, 0, v52
	v_cvt_pk_f16_f32 v51, v51, v52
	v_cvt_pk_f16_f32 v50, v50, v54
	ds_write_b64 v199, v[50:51] offset:96
	s_waitcnt lgkmcnt(0)
	ds_read_b128 v[208:211], v202
	ds_read_b128 v[212:215], v202 offset:1152
	ds_bpermute_b32 v216, v203, v66
	ds_bpermute_b32 v217, v203, v67
	ds_bpermute_b32 v218, v204, v66
	ds_bpermute_b32 v219, v204, v67
	v_add_u32_e32 v222, 48, v205
	v_cmp_gt_u32_e64 s[38:39], s18, v222
	v_add_u32_e32 v222, 8, v222
	v_cmp_gt_u32_e64 s[40:41], s18, v222
	s_waitcnt lgkmcnt(0)
	v_lshl_add_u64 v[216:217], v[216:217], 0, v[220:221]
	v_lshl_add_u64 v[218:219], v[218:219], 0, v[220:221]
	s_mov_b64 s[42:43], exec
	s_and_b64 exec, s[42:43], s[38:39]
	global_store_dwordx4 v[216:217], v[208:211], off sc1
	s_and_b64 exec, s[42:43], s[40:41]
	global_store_dwordx4 v[218:219], v[212:215], off sc1
	s_mov_b64 exec, s[42:43]
.LBB3_46:
	s_or_b64 exec, exec, s[2:3]
	v_add_u32_e32 v50, 64, v184
	v_cmp_gt_u32_e32 vcc, s18, v50
	s_mov_b64 s[2:3], exec
	s_cbranch_execz .LBB3_48
	s_waitcnt vmcnt(3)
	v_add_f32_e32 v47, v47, v27
	v_ashrrev_i32_e32 v119, 31, v118
	v_add_f32_e32 v46, v46, v26
	v_max_f32_e32 v52, 0, v47
	v_add_f32_e32 v47, v48, v28
	v_add_f32_e32 v48, v49, v29
	v_lshlrev_b64 v[50:51], 11, v[118:119]
	v_max_f32_e32 v46, 0, v46
	v_max_f32_e32 v47, 0, v47
	v_max_f32_e32 v48, 0, v48
	v_lshl_add_u64 v[50:51], v[116:117], 0, v[50:51]
	v_cvt_pk_f16_f32 v47, v47, v48
	v_cvt_pk_f16_f32 v46, v46, v52
	s_waitcnt vmcnt(2)
	v_add_f32_e32 v43, v43, v19
	ds_write_b64 v199, v[46:47]
	v_add_f32_e32 v42, v42, v18
	v_max_f32_e32 v46, 0, v43
	v_add_f32_e32 v43, v44, v20
	v_add_f32_e32 v44, v45, v21
	v_max_f32_e32 v42, 0, v42
	v_max_f32_e32 v43, 0, v43
	v_max_f32_e32 v44, 0, v44
	v_cvt_pk_f16_f32 v43, v43, v44
	v_cvt_pk_f16_f32 v42, v42, v46
	s_waitcnt vmcnt(2)
	v_add_f32_e32 v39, v39, v7
	ds_write_b64 v199, v[42:43] offset:32
	v_add_f32_e32 v38, v38, v6
	v_max_f32_e32 v42, 0, v39
	v_add_f32_e32 v39, v40, v8
	v_add_f32_e32 v40, v41, v9
	v_max_f32_e32 v38, 0, v38
	v_max_f32_e32 v39, 0, v39
	v_max_f32_e32 v40, 0, v40
	v_cvt_pk_f16_f32 v39, v39, v40
	v_cvt_pk_f16_f32 v38, v38, v42
	s_waitcnt vmcnt(2)
	v_add_f32_e32 v35, v35, v3
	ds_write_b64 v199, v[38:39] offset:64
	v_add_f32_e32 v34, v34, v2
	v_max_f32_e32 v38, 0, v35
	v_add_f32_e32 v35, v36, v4
	v_add_f32_e32 v36, v37, v5
	v_max_f32_e32 v34, 0, v34
	v_max_f32_e32 v35, 0, v35
	v_max_f32_e32 v36, 0, v36
	v_cvt_pk_f16_f32 v35, v35, v36
	v_cvt_pk_f16_f32 v34, v34, v38
	ds_write_b64 v199, v[34:35] offset:96
	s_waitcnt lgkmcnt(0)
	ds_read_b128 v[208:211], v202
	ds_read_b128 v[212:215], v202 offset:1152
	ds_bpermute_b32 v216, v203, v50
	ds_bpermute_b32 v217, v203, v51
	ds_bpermute_b32 v218, v204, v50
	ds_bpermute_b32 v219, v204, v51
	v_add_u32_e32 v222, 64, v205
	v_cmp_gt_u32_e64 s[38:39], s18, v222
	v_add_u32_e32 v222, 8, v222
	v_cmp_gt_u32_e64 s[40:41], s18, v222
	s_waitcnt lgkmcnt(0)
	v_lshl_add_u64 v[216:217], v[216:217], 0, v[220:221]
	v_lshl_add_u64 v[218:219], v[218:219], 0, v[220:221]
	s_mov_b64 s[42:43], exec
	s_and_b64 exec, s[42:43], s[38:39]
	global_store_dwordx4 v[216:217], v[208:211], off sc1
	s_and_b64 exec, s[42:43], s[40:41]
	global_store_dwordx4 v[218:219], v[212:215], off sc1
	s_mov_b64 exec, s[42:43]
.LBB3_48:
	s_or_b64 exec, exec, s[2:3]
	v_add_u32_e32 v34, 0x50, v184
	v_cmp_gt_u32_e32 vcc, s18, v34
	s_mov_b64 s[2:3], exec
	s_cbranch_execz .LBB3_50
	s_waitcnt vmcnt(1)
	v_add_f32_e32 v7, v15, v7
	v_ashrrev_i32_e32 v115, 31, v114
	v_add_f32_e32 v6, v14, v6
	v_max_f32_e32 v14, 0, v7
	v_add_f32_e32 v7, v16, v8
	v_add_f32_e32 v8, v17, v9
	v_lshlrev_b64 v[34:35], 11, v[114:115]
	v_max_f32_e32 v6, 0, v6
	v_max_f32_e32 v7, 0, v7
	v_max_f32_e32 v8, 0, v8
	v_lshl_add_u64 v[34:35], v[116:117], 0, v[34:35]
	v_add_f32_e32 v27, v31, v27
	v_add_f32_e32 v19, v23, v19
	v_cvt_pk_f16_f32 v7, v7, v8
	v_cvt_pk_f16_f32 v6, v6, v14
	s_waitcnt vmcnt(0)
	v_add_f32_e32 v3, v11, v3
	v_add_f32_e32 v26, v30, v26
	v_max_f32_e32 v30, 0, v27
	v_add_f32_e32 v27, v32, v28
	v_add_f32_e32 v28, v33, v29
	v_add_f32_e32 v18, v22, v18
	v_max_f32_e32 v22, 0, v19
	v_add_f32_e32 v19, v24, v20
	v_add_f32_e32 v20, v25, v21
	ds_write_b64 v199, v[6:7] offset:64
	v_add_f32_e32 v2, v10, v2
	v_max_f32_e32 v6, 0, v3
	v_add_f32_e32 v3, v12, v4
	v_add_f32_e32 v4, v13, v5
	v_max_f32_e32 v26, 0, v26
	v_max_f32_e32 v27, 0, v27
	v_max_f32_e32 v28, 0, v28
	v_max_f32_e32 v18, 0, v18
	v_max_f32_e32 v19, 0, v19
	v_max_f32_e32 v20, 0, v20
	v_max_f32_e32 v2, 0, v2
	v_max_f32_e32 v3, 0, v3
	v_max_f32_e32 v4, 0, v4
	v_cvt_pk_f16_f32 v27, v27, v28
	v_cvt_pk_f16_f32 v26, v26, v30
	v_cvt_pk_f16_f32 v19, v19, v20
	v_cvt_pk_f16_f32 v18, v18, v22
	v_cvt_pk_f16_f32 v3, v3, v4
	v_cvt_pk_f16_f32 v2, v2, v6
	ds_write_b64 v199, v[26:27]
	ds_write_b64 v199, v[18:19] offset:32
	ds_write_b64 v199, v[2:3] offset:96
	s_waitcnt lgkmcnt(0)
	ds_read_b128 v[208:211], v202
	ds_read_b128 v[212:215], v202 offset:1152
	ds_bpermute_b32 v216, v203, v34
	ds_bpermute_b32 v217, v203, v35
	ds_bpermute_b32 v218, v204, v34
	ds_bpermute_b32 v219, v204, v35
	v_add_u32_e32 v222, 80, v205
	v_cmp_gt_u32_e64 s[38:39], s18, v222
	v_add_u32_e32 v222, 8, v222
	v_cmp_gt_u32_e64 s[40:41], s18, v222
	s_waitcnt lgkmcnt(0)
	v_lshl_add_u64 v[216:217], v[216:217], 0, v[220:221]
	v_lshl_add_u64 v[218:219], v[218:219], 0, v[220:221]
	s_mov_b64 s[42:43], exec
	s_and_b64 exec, s[42:43], s[38:39]
	global_store_dwordx4 v[216:217], v[208:211], off sc1
	s_and_b64 exec, s[42:43], s[40:41]
	global_store_dwordx4 v[218:219], v[212:215], off sc1
	s_mov_b64 exec, s[42:43]

.LBB3_53:
	v_add_u32_e32 v104, v81, v83
	v_add_u32_e32 v102, v89, v83
	ds_read_b128 v[106:109], v104 offset:49152
	ds_read_b128 v[110:113], v104 offset:51200
	ds_read_b128 v[114:117], v102
	ds_read_b128 v[118:121], v102 offset:2048
	v_add_u32_e32 v103, v89, v87
	v_add_u32_e32 v105, v81, v87
	s_waitcnt lgkmcnt(1)
	v_mfma_f32_16x16x32_f16 v[46:49], v[106:109], v[114:117], v[46:49]
	v_lshl_add_u64 v[154:155], v[96:97], 0, v[84:85]
	v_lshl_add_u64 v[156:157], v[98:99], 0, v[84:85]
	v_lshl_add_u64 v[160:161], v[94:95], 0, v[84:85]
	v_mfma_f32_16x16x32_f16 v[38:41], v[110:113], v[114:117], v[38:41]
	v_lshl_add_u64 v[158:159], v[100:101], 0, v[84:85]
	v_add_co_u32_e32 v162, vcc, s14, v160
	s_waitcnt lgkmcnt(0)
	v_mfma_f32_16x16x32_f16 v[34:37], v[106:109], v[118:121], v[34:37]
	v_addc_co_u32_e32 v163, vcc, 0, v161, vcc
	s_add_i32 s4, s4, 2
	v_mfma_f32_16x16x32_f16 v[30:33], v[110:113], v[118:121], v[30:33]
	ds_read_b128 v[114:117], v102 offset:4096
	ds_read_b128 v[118:121], v102 offset:6144
	v_lshl_add_u64 v[96:97], v[96:97], 0, s[2:3]
	v_lshl_add_u64 v[98:99], v[98:99], 0, s[2:3]
	s_waitcnt lgkmcnt(1)
	v_mfma_f32_16x16x32_f16 v[42:45], v[106:109], v[114:117], v[42:45]
	v_lshl_add_u64 v[100:101], v[100:101], 0, s[2:3]
	v_lshl_add_u64 v[94:95], v[94:95], 0, s[2:3]
	s_cmp_lt_u32 s4, 27
	v_mfma_f32_16x16x32_f16 v[50:53], v[110:113], v[114:117], v[50:53]
	s_waitcnt lgkmcnt(0)
	v_mfma_f32_16x16x32_f16 v[54:57], v[106:109], v[118:121], v[54:57]
	v_mfma_f32_16x16x32_f16 v[58:61], v[110:113], v[118:121], v[58:61]
	ds_read_b128 v[114:117], v102 offset:8192
	ds_read_b128 v[118:121], v102 offset:10240
	s_waitcnt lgkmcnt(1)
	v_mfma_f32_16x16x32_f16 v[62:65], v[106:109], v[114:117], v[62:65]
	v_mfma_f32_16x16x32_f16 v[66:69], v[110:113], v[114:117], v[66:69]
	ds_read_b128 v[114:117], v105 offset:49152
	ds_read_b128 v[122:125], v105 offset:51200
	s_waitcnt lgkmcnt(2)
	v_mfma_f32_16x16x32_f16 v[74:77], v[106:109], v[118:121], v[74:77]
	v_mfma_f32_16x16x32_f16 v[70:73], v[110:113], v[118:121], v[70:73]
	ds_read_b128 v[106:109], v103
	ds_read_b128 v[110:113], v103 offset:2048
	s_waitcnt lgkmcnt(1)
	v_mfma_f32_16x16x32_f16 v[46:49], v[114:117], v[106:109], v[46:49]
	v_mfma_f32_16x16x32_f16 v[38:41], v[122:125], v[106:109], v[38:41]
	v_add_u32_e32 v106, v93, v83
	v_add_u32_e32 v107, v93, v87
	s_waitcnt lgkmcnt(0)
	v_mfma_f32_16x16x32_f16 v[34:37], v[114:117], v[110:113], v[34:37]
	v_mfma_f32_16x16x32_f16 v[30:33], v[122:125], v[110:113], v[30:33]
	ds_read_b128 v[108:111], v103 offset:4096
	ds_read_b128 v[118:121], v103 offset:6144
	global_load_dwordx4 v[126:129], v[154:155], off offset:256
	ds_read_b128 v[130:133], v103 offset:8192
	ds_read_b128 v[134:137], v103 offset:10240
	s_waitcnt vmcnt(3)
	ds_write_b128 v1, v[26:29] offset:24576
	s_waitcnt lgkmcnt(4)
	v_mfma_f32_16x16x32_f16 v[42:45], v[114:117], v[108:111], v[42:45]
	v_mfma_f32_16x16x32_f16 v[50:53], v[122:125], v[108:111], v[50:53]
	global_load_dwordx4 v[108:111], v[156:157], off offset:256
	global_load_dwordx4 v[138:141], v[158:159], off offset:256
	s_waitcnt vmcnt(4)
	ds_write_b128 v1, v[22:25] offset:32768
	s_waitcnt vmcnt(3)
	ds_write_b128 v1, v[18:21] offset:40960
	ds_write_b128 v91, v[10:13] offset:16384
	ds_write_b128 v91, v[14:17] offset:24576
	s_waitcnt lgkmcnt(7)
	v_mfma_f32_16x16x32_f16 v[26:29], v[114:117], v[118:121], v[54:57]
	v_mfma_f32_16x16x32_f16 v[54:57], v[122:125], v[118:121], v[58:61]
	global_load_dwordx4 v[118:121], v[160:161], off offset:256
	global_load_dwordx4 v[142:145], v[162:163], off offset:256
	s_waitcnt lgkmcnt(0)
	s_barrier
	v_mfma_f32_16x16x32_f16 v[10:13], v[114:117], v[130:133], v[62:65]
	ds_read_b128 v[22:25], v106 offset:16384
	ds_read_b128 v[58:61], v106 offset:18432
	v_mfma_f32_16x16x32_f16 v[14:17], v[122:125], v[130:133], v[66:69]
	v_mfma_f32_16x16x32_f16 v[62:65], v[122:125], v[134:137], v[70:73]
	s_nop 1
	ds_read_b128 v[66:69], v102 offset:24576
	ds_read_b128 v[70:73], v102 offset:26624
	s_waitcnt lgkmcnt(1)
	v_mfma_f32_16x16x32_f16 v[46:49], v[22:25], v[66:69], v[46:49]
	v_mfma_f32_16x16x32_f16 v[38:41], v[58:61], v[66:69], v[38:41]
	s_waitcnt lgkmcnt(0)
	v_mfma_f32_16x16x32_f16 v[34:37], v[22:25], v[70:73], v[34:37]
	v_mfma_f32_16x16x32_f16 v[30:33], v[58:61], v[70:73], v[30:33]
	ds_read_b128 v[66:69], v102 offset:28672
	ds_read_b128 v[70:73], v102 offset:30720
	s_waitcnt lgkmcnt(1)
	v_mfma_f32_16x16x32_f16 v[42:45], v[22:25], v[66:69], v[42:45]
	v_mfma_f32_16x16x32_f16 v[50:53], v[58:61], v[66:69], v[50:53]
	s_waitcnt lgkmcnt(0)
	v_mfma_f32_16x16x32_f16 v[26:29], v[22:25], v[70:73], v[26:29]
	v_mfma_f32_16x16x32_f16 v[66:69], v[58:61], v[70:73], v[54:57]
	s_nop 2
	ds_read_b128 v[54:57], v102 offset:32768
	ds_read_b128 v[70:73], v102 offset:34816
	v_mfma_f32_16x16x32_f16 v[18:21], v[114:117], v[134:137], v[74:77]
	ds_read_b128 v[130:133], v107 offset:16384
	ds_read_b128 v[134:137], v107 offset:18432
	s_waitcnt lgkmcnt(3)
	v_mfma_f32_16x16x32_f16 v[74:77], v[22:25], v[54:57], v[10:13]
	v_mfma_f32_16x16x32_f16 v[112:115], v[58:61], v[54:57], v[14:17]
	s_nop 1
	ds_read_b128 v[10:13], v103 offset:24576
	ds_read_b128 v[14:17], v103 offset:26624
	s_waitcnt lgkmcnt(1)
	v_mfma_f32_16x16x32_f16 v[46:49], v[130:133], v[10:13], v[46:49]
	v_mfma_f32_16x16x32_f16 v[38:41], v[134:137], v[10:13], v[38:41]
	s_waitcnt lgkmcnt(0)
	v_mfma_f32_16x16x32_f16 v[34:37], v[130:133], v[14:17], v[34:37]
	v_mfma_f32_16x16x32_f16 v[30:33], v[134:137], v[14:17], v[30:33]
	ds_read_b128 v[10:13], v103 offset:28672
	ds_read_b128 v[14:17], v103 offset:30720
	ds_read_b128 v[146:149], v103 offset:32768
	ds_read_b128 v[150:153], v103 offset:34816
	v_mfma_f32_16x16x32_f16 v[122:125], v[22:25], v[70:73], v[18:21]
	s_waitcnt lgkmcnt(3)
	v_mfma_f32_16x16x32_f16 v[42:45], v[130:133], v[10:13], v[42:45]
	v_mfma_f32_16x16x32_f16 v[50:53], v[134:137], v[10:13], v[50:53]
	s_waitcnt lgkmcnt(2)
	v_mfma_f32_16x16x32_f16 v[54:57], v[130:133], v[14:17], v[26:29]
	s_nop 2
	global_load_dwordx4 v[26:29], v[154:155], off offset:384
	global_load_dwordx4 v[22:25], v[156:157], off offset:384
	global_load_dwordx4 v[18:21], v[158:159], off offset:384
	global_load_dwordx4 v[10:13], v[160:161], off offset:384
	v_mfma_f32_16x16x32_f16 v[70:73], v[58:61], v[70:73], v[62:65]
	v_mfma_f32_16x16x32_f16 v[58:61], v[134:137], v[14:17], v[66:69]
	global_load_dwordx4 v[14:17], v[162:163], off offset:384
	s_waitcnt vmcnt(9)
	ds_write_b128 v1, v[126:129]
	s_waitcnt vmcnt(8)
	ds_write_b128 v1, v[108:111] offset:8192
	s_waitcnt vmcnt(7)
	ds_write_b128 v1, v[138:141] offset:16384
	s_waitcnt vmcnt(6)
	ds_write_b128 v1, v[118:121] offset:49152
	s_waitcnt vmcnt(5)
	ds_write_b128 v1, v[142:145] offset:57344
	s_waitcnt lgkmcnt(0)
	v_mfma_f32_16x16x32_f16 v[62:65], v[130:133], v[146:149], v[74:77]
	s_barrier
	v_mfma_f32_16x16x32_f16 v[66:69], v[134:137], v[146:149], v[112:115]
	v_mfma_f32_16x16x32_f16 v[74:77], v[130:133], v[150:153], v[122:125]
	v_mfma_f32_16x16x32_f16 v[70:73], v[134:137], v[150:153], v[70:73]
	s_cbranch_scc1 .LBB3_53
	ds_read_b128 v[94:97], v104 offset:49152
	ds_read_b128 v[98:101], v104 offset:51200
	ds_read_b128 v[108:111], v102
	ds_read_b128 v[112:115], v102 offset:2048
	v_add_u32_e32 v81, 0x10000, v1
	s_lshl_b64 s[0:1], s[0:1], 1
	s_add_u32 s0, s10, s0
	s_waitcnt lgkmcnt(1)
	v_mfma_f32_16x16x32_f16 v[46:49], v[94:97], v[108:111], v[46:49]
	s_addc_u32 s1, s11, s1
	v_cmp_gt_u32_e32 vcc, s18, v79
	v_mfma_f32_16x16x32_f16 v[38:41], v[98:101], v[108:111], v[38:41]
	s_waitcnt lgkmcnt(0)
	v_mfma_f32_16x16x32_f16 v[34:37], v[94:97], v[112:115], v[34:37]
	v_mfma_f32_16x16x32_f16 v[30:33], v[98:101], v[112:115], v[30:33]
	ds_read_b128 v[108:111], v102 offset:4096
	ds_read_b128 v[112:115], v102 offset:6144
	s_waitcnt lgkmcnt(1)
	v_mfma_f32_16x16x32_f16 v[42:45], v[94:97], v[108:111], v[42:45]
	v_mfma_f32_16x16x32_f16 v[50:53], v[98:101], v[108:111], v[50:53]
	s_waitcnt lgkmcnt(0)
	v_mfma_f32_16x16x32_f16 v[54:57], v[94:97], v[112:115], v[54:57]
	v_mfma_f32_16x16x32_f16 v[58:61], v[98:101], v[112:115], v[58:61]
	ds_read_b128 v[108:111], v102 offset:8192
	ds_read_b128 v[112:115], v102 offset:10240
	s_waitcnt lgkmcnt(1)
	v_mfma_f32_16x16x32_f16 v[62:65], v[94:97], v[108:111], v[62:65]
	s_waitcnt lgkmcnt(0)
	v_mfma_f32_16x16x32_f16 v[74:77], v[94:97], v[112:115], v[74:77]
	ds_read_b128 v[94:97], v105 offset:49152
	v_mfma_f32_16x16x32_f16 v[66:69], v[98:101], v[108:111], v[66:69]
	v_mfma_f32_16x16x32_f16 v[70:73], v[98:101], v[112:115], v[70:73]
	ds_read_b128 v[98:101], v105 offset:51200
	ds_read_b128 v[108:111], v103
	ds_read_b128 v[112:115], v103 offset:2048
	s_waitcnt lgkmcnt(1)
	v_mfma_f32_16x16x32_f16 v[46:49], v[94:97], v[108:111], v[46:49]
	v_mfma_f32_16x16x32_f16 v[38:41], v[98:101], v[108:111], v[38:41]
	s_waitcnt lgkmcnt(0)
	v_mfma_f32_16x16x32_f16 v[34:37], v[94:97], v[112:115], v[34:37]
	v_mfma_f32_16x16x32_f16 v[30:33], v[98:101], v[112:115], v[30:33]
	ds_read_b128 v[108:111], v103 offset:4096
	ds_read_b128 v[112:115], v103 offset:6144
	s_waitcnt lgkmcnt(1)
	v_mfma_f32_16x16x32_f16 v[42:45], v[94:97], v[108:111], v[42:45]
	v_mfma_f32_16x16x32_f16 v[50:53], v[98:101], v[108:111], v[50:53]
	s_waitcnt lgkmcnt(0)
	v_mfma_f32_16x16x32_f16 v[54:57], v[94:97], v[112:115], v[54:57]
	v_mfma_f32_16x16x32_f16 v[58:61], v[98:101], v[112:115], v[58:61]
	ds_read_b128 v[108:111], v103 offset:8192
	ds_read_b128 v[112:115], v103 offset:10240
	s_waitcnt vmcnt(4)
	ds_write_b128 v1, v[26:29] offset:24576
	s_waitcnt vmcnt(3)
	ds_write_b128 v1, v[22:25] offset:32768
	s_waitcnt vmcnt(2)
	ds_write_b128 v1, v[18:21] offset:40960
	s_waitcnt vmcnt(1)
	ds_write_b128 v81, v[10:13]
	s_waitcnt vmcnt(0)
	ds_write_b128 v81, v[14:17] offset:8192
	s_waitcnt lgkmcnt(0)
	s_barrier
	ds_read_b128 v[10:13], v106 offset:16384
	ds_read_b128 v[18:21], v106 offset:18432
	ds_read_b128 v[22:25], v102 offset:24576
	ds_read_b128 v[26:29], v102 offset:26624
	s_waitcnt lgkmcnt(1)
	v_mfma_f32_16x16x32_f16 v[46:49], v[10:13], v[22:25], v[46:49]
	v_mfma_f32_16x16x32_f16 v[22:25], v[18:21], v[22:25], v[38:41]
	s_waitcnt lgkmcnt(0)
	v_mfma_f32_16x16x32_f16 v[34:37], v[10:13], v[26:29], v[34:37]
	v_mfma_f32_16x16x32_f16 v[26:29], v[18:21], v[26:29], v[30:33]
	s_nop 2
	ds_read_b128 v[30:33], v102 offset:28672
	ds_read_b128 v[38:41], v102 offset:30720
	v_mfma_f32_16x16x32_f16 v[62:65], v[94:97], v[108:111], v[62:65]
	v_mfma_f32_16x16x32_f16 v[74:77], v[94:97], v[112:115], v[74:77]
	v_mfma_f32_16x16x32_f16 v[14:17], v[98:101], v[112:115], v[70:73]
	s_waitcnt lgkmcnt(1)
	v_mfma_f32_16x16x32_f16 v[70:73], v[10:13], v[30:33], v[42:45]
	s_waitcnt lgkmcnt(0)
	v_mfma_f32_16x16x32_f16 v[94:97], v[10:13], v[38:41], v[54:57]
	v_mfma_f32_16x16x32_f16 v[58:61], v[18:21], v[38:41], v[58:61]
	ds_read_b128 v[38:41], v102 offset:32768
	ds_read_b128 v[42:45], v102 offset:34816
	v_mfma_f32_16x16x32_f16 v[66:69], v[98:101], v[108:111], v[66:69]
	s_waitcnt lgkmcnt(1)
	v_mfma_f32_16x16x32_f16 v[62:65], v[10:13], v[38:41], v[62:65]
	s_waitcnt lgkmcnt(0)
	v_mfma_f32_16x16x32_f16 v[10:13], v[10:13], v[42:45], v[74:77]
	s_nop 2
	ds_read_b128 v[74:77], v107 offset:16384
	v_mfma_f32_16x16x32_f16 v[30:33], v[18:21], v[30:33], v[50:53]
	v_mfma_f32_16x16x32_f16 v[66:69], v[18:21], v[38:41], v[66:69]
	v_mfma_f32_16x16x32_f16 v[98:101], v[18:21], v[42:45], v[14:17]
	ds_read_b128 v[104:107], v107 offset:18432
	s_nop 1
	ds_read_b128 v[14:17], v103 offset:24576
	ds_read_b128 v[18:21], v103 offset:26624
	s_waitcnt lgkmcnt(1)
	v_mfma_f32_16x16x32_f16 v[54:57], v[74:77], v[14:17], v[46:49]
	v_mfma_f32_16x16x32_f16 v[50:53], v[104:107], v[14:17], v[22:25]
	s_waitcnt lgkmcnt(0)
	v_mfma_f32_16x16x32_f16 v[46:49], v[74:77], v[18:21], v[34:37]
	v_mfma_f32_16x16x32_f16 v[42:45], v[104:107], v[18:21], v[26:29]
	ds_read_b128 v[14:17], v103 offset:28672
	ds_read_b128 v[18:21], v103 offset:30720
	s_waitcnt lgkmcnt(1)
	v_mfma_f32_16x16x32_f16 v[38:41], v[74:77], v[14:17], v[70:73]
	v_mfma_f32_16x16x32_f16 v[34:37], v[104:107], v[14:17], v[30:33]
	s_waitcnt lgkmcnt(0)
	v_mfma_f32_16x16x32_f16 v[26:29], v[104:107], v[18:21], v[58:61]
	ds_read_b128 v[14:17], v103 offset:32768
	s_nop 1
	ds_read_b128 v[58:61], v103 offset:34816
	s_waitcnt lgkmcnt(1)
	v_mfma_f32_16x16x32_f16 v[22:25], v[74:77], v[14:17], v[62:65]
	s_nop 2
	v_lshlrev_b32_e32 v62, 1, v92
	v_mov_b32_e32 v63, 0
	v_mfma_f32_16x16x32_f16 v[30:33], v[74:77], v[18:21], v[94:97]
	v_mfma_f32_16x16x32_f16 v[18:21], v[104:107], v[14:17], v[66:69]
	s_waitcnt lgkmcnt(0)
	v_mfma_f32_16x16x32_f16 v[14:17], v[74:77], v[58:61], v[10:13]
	s_nop 2
	v_lshl_add_u64 v[10:11], s[0:1], 0, v[62:63]
	v_lshlrev_b32_e32 v62, 1, v0
	v_lshl_add_u64 v[0:1], v[10:11], 0, v[62:63]
	v_mfma_f32_16x16x32_f16 v[10:13], v[104:107], v[58:61], v[98:101]
	v_mbcnt_lo_u32_b32 v196, -1, 0
	v_mbcnt_hi_u32_b32 v196, -1, v196
	v_and_b32_e32 v197, 15, v196
	v_lshrrev_b32_e32 v198, 4, v196
	v_lshrrev_b32_e32 v222, 10, v81
	s_nop 0
	v_readfirstlane_b32 s36, v222
	s_nop 3
	s_and_b32 s36, s36, 7
	s_mulk_i32 s36, 0x500
	v_mul_u32_u24_e32 v199, 0x50, v197
	v_lshl_add_u32 v199, v198, 3, v199
	v_add_u32_e32 v199, s36, v199
	v_lshrrev_b32_e32 v200, 2, v196
	v_and_b32_e32 v201, 3, v196
	v_mul_u32_u24_e32 v202, 0x50, v200
	v_lshl_add_u32 v202, v201, 4, v202
	v_add_u32_e32 v202, s36, v202
	v_lshlrev_b32_e32 v203, 2, v200
	v_add_u32_e32 v204, 32, v203
	v_lshlrev_b32_e32 v220, 4, v201
	v_mov_b32_e32 v221, 0
	v_sub_u32_e32 v205, v79, v197
	v_add_u32_e32 v205, v205, v200
	s_mov_b64 s[0:1], exec
	s_cbranch_execz .LBB3_56
	v_add_f32_e32 v55, v7, v55
	v_ashrrev_i32_e32 v91, 31, v90
	v_add_f32_e32 v54, v6, v54
	v_max_f32_e32 v60, 0, v55
	v_add_f32_e32 v55, v8, v56
	v_add_f32_e32 v56, v9, v57
	v_lshlrev_b64 v[58:59], 11, v[90:91]
	v_max_f32_e32 v54, 0, v54
	v_max_f32_e32 v55, 0, v55
	v_max_f32_e32 v56, 0, v56
	v_lshl_add_u64 v[58:59], v[0:1], 0, v[58:59]
	v_cvt_pk_f16_f32 v55, v55, v56
	v_cvt_pk_f16_f32 v54, v54, v60
	v_add_f32_e32 v51, v3, v51
	ds_write_b64 v199, v[54:55]
	v_add_f32_e32 v50, v2, v50
	v_max_f32_e32 v54, 0, v51
	v_add_f32_e32 v51, v4, v52
	v_add_f32_e32 v52, v5, v53
	v_max_f32_e32 v50, 0, v50
	v_max_f32_e32 v51, 0, v51
	v_max_f32_e32 v52, 0, v52
	v_cvt_pk_f16_f32 v51, v51, v52
	v_cvt_pk_f16_f32 v50, v50, v54
	ds_write_b64 v199, v[50:51] offset:32
	s_waitcnt lgkmcnt(0)
	ds_read_b128 v[208:211], v202
	ds_bpermute_b32 v216, v203, v58
	ds_bpermute_b32 v217, v203, v59
	v_add_u32_e32 v222, 0, v205
	v_cmp_gt_u32_e64 s[38:39], s18, v222
	s_waitcnt lgkmcnt(0)
	v_lshl_add_u64 v[216:217], v[216:217], 0, v[220:221]
	s_mov_b64 s[42:43], exec
	s_and_b64 exec, s[42:43], s[38:39]
	global_store_dwordx4 v[216:217], v[208:211], off sc1
	s_mov_b64 exec, s[42:43]
.LBB3_56:
	s_or_b64 exec, exec, s[0:1]
	v_or_b32_e32 v50, 16, v79
	v_cmp_gt_u32_e32 vcc, s18, v50
	s_mov_b64 s[0:1], exec
	s_cbranch_execz .LBB3_58
	v_add_f32_e32 v47, v7, v47
	v_ashrrev_i32_e32 v89, 31, v88
	v_add_f32_e32 v46, v6, v46
	v_max_f32_e32 v52, 0, v47
	v_add_f32_e32 v47, v8, v48
	v_add_f32_e32 v48, v9, v49
	v_lshlrev_b64 v[50:51], 11, v[88:89]
	v_max_f32_e32 v46, 0, v46
	v_max_f32_e32 v47, 0, v47
	v_max_f32_e32 v48, 0, v48
	v_lshl_add_u64 v[50:51], v[0:1], 0, v[50:51]
	v_cvt_pk_f16_f32 v47, v47, v48
	v_cvt_pk_f16_f32 v46, v46, v52
	v_add_f32_e32 v43, v3, v43
	ds_write_b64 v199, v[46:47]
	v_add_f32_e32 v42, v2, v42
	v_max_f32_e32 v46, 0, v43
	v_add_f32_e32 v43, v4, v44
	v_add_f32_e32 v44, v5, v45
	v_max_f32_e32 v42, 0, v42
	v_max_f32_e32 v43, 0, v43
	v_max_f32_e32 v44, 0, v44
	v_cvt_pk_f16_f32 v43, v43, v44
	v_cvt_pk_f16_f32 v42, v42, v46
	ds_write_b64 v199, v[42:43] offset:32
	s_waitcnt lgkmcnt(0)
	ds_read_b128 v[208:211], v202
	ds_bpermute_b32 v216, v203, v50
	ds_bpermute_b32 v217, v203, v51
	v_add_u32_e32 v222, 16, v205
	v_cmp_gt_u32_e64 s[38:39], s18, v222
	s_waitcnt lgkmcnt(0)
	v_lshl_add_u64 v[216:217], v[216:217], 0, v[220:221]
	s_mov_b64 s[42:43], exec
	s_and_b64 exec, s[42:43], s[38:39]
	global_store_dwordx4 v[216:217], v[208:211], off sc1
	s_mov_b64 exec, s[42:43]
.LBB3_58:
	s_or_b64 exec, exec, s[0:1]
	v_add_u32_e32 v42, 32, v79
	v_cmp_gt_u32_e32 vcc, s18, v42
	s_mov_b64 s[0:1], exec
	s_cbranch_execz .LBB3_60
	v_add_f32_e32 v39, v7, v39
	v_ashrrev_i32_e32 v87, 31, v86
	v_add_f32_e32 v38, v6, v38
	v_max_f32_e32 v44, 0, v39
	v_add_f32_e32 v39, v8, v40
	v_add_f32_e32 v40, v9, v41
	v_lshlrev_b64 v[42:43], 11, v[86:87]
	v_max_f32_e32 v38, 0, v38
	v_max_f32_e32 v39, 0, v39
	v_max_f32_e32 v40, 0, v40
	v_lshl_add_u64 v[42:43], v[0:1], 0, v[42:43]
	v_cvt_pk_f16_f32 v39, v39, v40
	v_cvt_pk_f16_f32 v38, v38, v44
	v_add_f32_e32 v35, v3, v35
	ds_write_b64 v199, v[38:39]
	v_add_f32_e32 v34, v2, v34
	v_max_f32_e32 v38, 0, v35
	v_add_f32_e32 v35, v4, v36
	v_add_f32_e32 v36, v5, v37
	v_max_f32_e32 v34, 0, v34
	v_max_f32_e32 v35, 0, v35
	v_max_f32_e32 v36, 0, v36
	v_cvt_pk_f16_f32 v35, v35, v36
	v_cvt_pk_f16_f32 v34, v34, v38
	ds_write_b64 v199, v[34:35] offset:32
	s_waitcnt lgkmcnt(0)
	ds_read_b128 v[208:211], v202
	ds_bpermute_b32 v216, v203, v42
	ds_bpermute_b32 v217, v203, v43
	v_add_u32_e32 v222, 32, v205
	v_cmp_gt_u32_e64 s[38:39], s18, v222
	s_waitcnt lgkmcnt(0)
	v_lshl_add_u64 v[216:217], v[216:217], 0, v[220:221]
	s_mov_b64 s[42:43], exec
	s_and_b64 exec, s[42:43], s[38:39]
	global_store_dwordx4 v[216:217], v[208:211], off sc1
	s_mov_b64 exec, s[42:43]
.LBB3_60:
	s_or_b64 exec, exec, s[0:1]
	v_add_u32_e32 v34, 48, v79
	v_cmp_gt_u32_e32 vcc, s18, v34
	s_mov_b64 s[0:1], exec
	s_cbranch_execz .LBB3_62
	v_add_f32_e32 v31, v7, v31
	v_ashrrev_i32_e32 v83, 31, v82
	v_add_f32_e32 v30, v6, v30
	v_max_f32_e32 v36, 0, v31
	v_add_f32_e32 v31, v8, v32
	v_add_f32_e32 v32, v9, v33
	v_lshlrev_b64 v[34:35], 11, v[82:83]
	v_max_f32_e32 v30, 0, v30
	v_max_f32_e32 v31, 0, v31
	v_max_f32_e32 v32, 0, v32
	v_lshl_add_u64 v[34:35], v[0:1], 0, v[34:35]
	v_cvt_pk_f16_f32 v31, v31, v32
	v_cvt_pk_f16_f32 v30, v30, v36
	v_add_f32_e32 v27, v3, v27
	ds_write_b64 v199, v[30:31]
	v_add_f32_e32 v26, v2, v26
	v_max_f32_e32 v30, 0, v27
	v_add_f32_e32 v27, v4, v28
	v_add_f32_e32 v28, v5, v29
	v_max_f32_e32 v26, 0, v26
	v_max_f32_e32 v27, 0, v27
	v_max_f32_e32 v28, 0, v28
	v_cvt_pk_f16_f32 v27, v27, v28
	v_cvt_pk_f16_f32 v26, v26, v30
	ds_write_b64 v199, v[26:27] offset:32
	s_waitcnt lgkmcnt(0)
	ds_read_b128 v[208:211], v202
	ds_bpermute_b32 v216, v203, v34
	ds_bpermute_b32 v217, v203, v35
	v_add_u32_e32 v222, 48, v205
	v_cmp_gt_u32_e64 s[38:39], s18, v222
	s_waitcnt lgkmcnt(0)
	v_lshl_add_u64 v[216:217], v[216:217], 0, v[220:221]
	s_mov_b64 s[42:43], exec
	s_and_b64 exec, s[42:43], s[38:39]
	global_store_dwordx4 v[216:217], v[208:211], off sc1
	s_mov_b64 exec, s[42:43]
.LBB3_62:
	s_or_b64 exec, exec, s[0:1]
	v_add_u32_e32 v26, 64, v79
	v_cmp_gt_u32_e32 vcc, s18, v26
	s_mov_b64 s[0:1], exec
	s_cbranch_execz .LBB3_64
	v_add_f32_e32 v23, v7, v23
	v_ashrrev_i32_e32 v81, 31, v80
	v_add_f32_e32 v22, v6, v22
	v_max_f32_e32 v28, 0, v23
	v_add_f32_e32 v23, v8, v24
	v_add_f32_e32 v24, v9, v25
	v_lshlrev_b64 v[26:27], 11, v[80:81]
	v_max_f32_e32 v22, 0, v22
	v_max_f32_e32 v23, 0, v23
	v_max_f32_e32 v24, 0, v24
	v_lshl_add_u64 v[26:27], v[0:1], 0, v[26:27]
	v_cvt_pk_f16_f32 v23, v23, v24
	v_cvt_pk_f16_f32 v22, v22, v28
	v_add_f32_e32 v19, v3, v19
	ds_write_b64 v199, v[22:23]
	v_add_f32_e32 v18, v2, v18
	v_max_f32_e32 v22, 0, v19
	v_add_f32_e32 v19, v4, v20
	v_add_f32_e32 v20, v5, v21
	v_max_f32_e32 v18, 0, v18
	v_max_f32_e32 v19, 0, v19
	v_max_f32_e32 v20, 0, v20
	v_cvt_pk_f16_f32 v19, v19, v20
	v_cvt_pk_f16_f32 v18, v18, v22
	ds_write_b64 v199, v[18:19] offset:32
	s_waitcnt lgkmcnt(0)
	ds_read_b128 v[208:211], v202
	ds_bpermute_b32 v216, v203, v26
	ds_bpermute_b32 v217, v203, v27
	v_add_u32_e32 v222, 64, v205
	v_cmp_gt_u32_e64 s[38:39], s18, v222
	s_waitcnt lgkmcnt(0)
	v_lshl_add_u64 v[216:217], v[216:217], 0, v[220:221]
	s_mov_b64 s[42:43], exec
	s_and_b64 exec, s[42:43], s[38:39]
	global_store_dwordx4 v[216:217], v[208:211], off sc1
	s_mov_b64 exec, s[42:43]
.LBB3_64:
	s_or_b64 exec, exec, s[0:1]
	v_add_u32_e32 v18, 0x50, v79
	v_cmp_gt_u32_e32 vcc, s18, v18
	s_mov_b64 s[0:1], exec
	s_cbranch_execz .LBB3_66
	v_add_f32_e32 v7, v7, v15
	v_ashrrev_i32_e32 v79, 31, v78
	v_add_f32_e32 v6, v6, v14
	v_max_f32_e32 v14, 0, v7
	v_add_f32_e32 v7, v8, v16
	v_add_f32_e32 v8, v9, v17
	v_lshlrev_b64 v[18:19], 11, v[78:79]
	v_max_f32_e32 v6, 0, v6
	v_max_f32_e32 v7, 0, v7
	v_max_f32_e32 v8, 0, v8
	v_lshl_add_u64 v[0:1], v[0:1], 0, v[18:19]
	v_cvt_pk_f16_f32 v7, v7, v8
	v_cvt_pk_f16_f32 v6, v6, v14
	v_add_f32_e32 v3, v3, v11
	ds_write_b64 v199, v[6:7]
	v_add_f32_e32 v2, v2, v10
	v_max_f32_e32 v6, 0, v3
	v_add_f32_e32 v3, v4, v12
	v_add_f32_e32 v4, v5, v13
	v_max_f32_e32 v2, 0, v2
	v_max_f32_e32 v3, 0, v3
	v_max_f32_e32 v4, 0, v4
	v_cvt_pk_f16_f32 v3, v3, v4
	v_cvt_pk_f16_f32 v2, v2, v6
	ds_write_b64 v199, v[2:3] offset:32
	s_waitcnt lgkmcnt(0)
	ds_read_b128 v[208:211], v202
	ds_bpermute_b32 v216, v203, v0
	ds_bpermute_b32 v217, v203, v1
	v_add_u32_e32 v222, 80, v205
	v_cmp_gt_u32_e64 s[38:39], s18, v222
	s_waitcnt lgkmcnt(0)
	v_lshl_add_u64 v[216:217], v[216:217], 0, v[220:221]
	s_mov_b64 s[42:43], exec
	s_and_b64 exec, s[42:43], s[38:39]
	global_store_dwordx4 v[216:217], v[208:211], off sc1
	s_mov_b64 exec, s[42:43]

.LBB4_37:
	s_or_b64 exec, exec, s[6:7]
	s_waitcnt vmcnt(3)
	ds_write_b128 v154, v[42:45]
	s_waitcnt vmcnt(2)
	ds_write_b128 v154, v[46:49] offset:8192
	s_waitcnt vmcnt(1)
	ds_write_b128 v154, v[50:53] offset:16384
	s_waitcnt vmcnt(0)
	ds_write_b128 v154, v[54:57] offset:24576
	s_waitcnt lgkmcnt(0)
	s_barrier
	ds_read_b128 v[26:29], v162 offset:57344
	ds_read_b128 v[34:37], v161 offset:12288
	ds_read_b128 v[42:45], v162 offset:59392
	ds_read_b128 v[46:49], v161 offset:14336
	ds_read_b128 v[54:57], v162 offset:61440
	s_waitcnt lgkmcnt(3)
	v_mfma_f32_16x16x32_f16 v[50:53], v[26:29], v[34:37], v[78:81]
	s_lshl_b64 s[2:3], s[16:17], 1
	s_add_u32 s2, s10, s2
	s_addc_u32 s3, s11, s3
	s_waitcnt lgkmcnt(2)
	v_mfma_f32_16x16x32_f16 v[78:81], v[42:45], v[34:37], v[82:85]
	v_cmp_gt_u32_e32 vcc, s24, v133
	s_waitcnt lgkmcnt(0)
	v_mfma_f32_16x16x32_f16 v[82:85], v[54:57], v[34:37], v[86:89]
	s_nop 2
	ds_read_b128 v[86:89], v162 offset:63488
	ds_read_b128 v[90:93], v160 offset:12288
	ds_read_b128 v[98:101], v163 offset:59392
	ds_read_b128 v[102:105], v163 offset:61440
	s_waitcnt lgkmcnt(3)
	v_mfma_f32_16x16x32_f16 v[22:25], v[86:89], v[34:37], v[22:25]
	v_mfma_f32_16x16x32_f16 v[34:37], v[26:29], v[46:49], v[58:61]
	v_mfma_f32_16x16x32_f16 v[94:97], v[42:45], v[46:49], v[62:65]
	v_mfma_f32_16x16x32_f16 v[66:69], v[54:57], v[46:49], v[66:69]
	v_mfma_f32_16x16x32_f16 v[70:73], v[86:89], v[46:49], v[70:73]
	ds_read_b128 v[46:49], v161 offset:16384
	s_waitcnt lgkmcnt(0)
	v_mfma_f32_16x16x32_f16 v[26:29], v[26:29], v[46:49], v[30:33]
	s_nop 2
	ds_read_b128 v[30:33], v163 offset:57344
	v_mfma_f32_16x16x32_f16 v[58:61], v[98:101], v[90:93], v[78:81]
	s_nop 2
	ds_read_b128 v[78:81], v163 offset:63488
	v_mfma_f32_16x16x32_f16 v[18:21], v[54:57], v[46:49], v[18:21]
	s_waitcnt lgkmcnt(1)
	v_mfma_f32_16x16x32_f16 v[62:65], v[30:33], v[90:93], v[50:53]
	v_mfma_f32_16x16x32_f16 v[54:57], v[102:105], v[90:93], v[82:85]
	s_waitcnt lgkmcnt(0)
	v_mfma_f32_16x16x32_f16 v[50:53], v[78:81], v[90:93], v[22:25]
	s_nop 2
	ds_read_b128 v[22:25], v160 offset:14336
	ds_read_b128 v[82:85], v160 offset:16384
	v_mfma_f32_16x16x32_f16 v[74:77], v[42:45], v[46:49], v[74:77]
	v_mfma_f32_16x16x32_f16 v[86:89], v[86:89], v[46:49], v[38:41]
	s_waitcnt lgkmcnt(1)
	v_mfma_f32_16x16x32_f16 v[38:41], v[102:105], v[22:25], v[66:69]
	s_nop 2
	v_lshlrev_b32_e32 v66, 1, v135
	v_mov_b32_e32 v67, 0
	v_mfma_f32_16x16x32_f16 v[46:49], v[30:33], v[22:25], v[34:37]
	v_mfma_f32_16x16x32_f16 v[42:45], v[98:101], v[22:25], v[94:97]
	v_mfma_f32_16x16x32_f16 v[34:37], v[78:81], v[22:25], v[70:73]
	s_waitcnt lgkmcnt(0)
	v_mfma_f32_16x16x32_f16 v[22:25], v[102:105], v[82:85], v[18:21]
	s_nop 2
	v_lshl_add_u64 v[18:19], s[2:3], 0, v[66:67]
	v_lshlrev_b32_e32 v66, 1, v131
	v_mfma_f32_16x16x32_f16 v[30:33], v[30:33], v[82:85], v[26:29]
	v_lshl_add_u64 v[66:67], v[18:19], 0, v[66:67]
	v_mfma_f32_16x16x32_f16 v[26:29], v[98:101], v[82:85], v[74:77]
	v_mfma_f32_16x16x32_f16 v[18:21], v[78:81], v[82:85], v[86:89]
	v_mbcnt_lo_u32_b32 v196, -1, 0
	v_mbcnt_hi_u32_b32 v196, -1, v196
	v_and_b32_e32 v197, 15, v196
	v_lshrrev_b32_e32 v198, 4, v196
	v_lshrrev_b32_e32 v222, 10, v137
	s_nop 0
	v_readfirstlane_b32 s36, v222
	s_nop 3
	s_and_b32 s36, s36, 7
	s_mulk_i32 s36, 0x900
	s_add_u32 s36, s36, 0x6000
	v_mul_u32_u24_e32 v199, 0x90, v197
	v_lshl_add_u32 v199, v198, 3, v199
	v_add_u32_e32 v199, s36, v199
	v_lshrrev_b32_e32 v200, 3, v196
	v_and_b32_e32 v201, 7, v196
	v_mul_u32_u24_e32 v202, 0x90, v200
	v_lshl_add_u32 v202, v201, 4, v202
	v_add_u32_e32 v202, s36, v202
	v_lshlrev_b32_e32 v203, 2, v200
	v_add_u32_e32 v204, 32, v203
	v_lshlrev_b32_e32 v220, 4, v201
	v_mov_b32_e32 v221, 0
	v_sub_u32_e32 v205, v133, v197
	v_add_u32_e32 v205, v205, v200
	s_mov_b64 s[2:3], exec
	s_cbranch_execz .LBB4_39
	v_add_f32_e32 v63, v15, v63
	v_ashrrev_i32_e32 v137, 31, v136
	v_add_f32_e32 v62, v14, v62
	v_max_f32_e32 v70, 0, v63
	v_add_f32_e32 v63, v16, v64
	v_add_f32_e32 v64, v17, v65
	v_lshlrev_b64 v[68:69], 11, v[136:137]
	v_max_f32_e32 v62, 0, v62
	v_max_f32_e32 v63, 0, v63
	v_max_f32_e32 v64, 0, v64
	v_lshl_add_u64 v[68:69], v[66:67], 0, v[68:69]
	v_cvt_pk_f16_f32 v63, v63, v64
	v_cvt_pk_f16_f32 v62, v62, v70
	v_add_f32_e32 v59, v11, v59
	ds_write_b64 v199, v[62:63]
	v_add_f32_e32 v58, v10, v58
	v_max_f32_e32 v62, 0, v59
	v_add_f32_e32 v59, v12, v60
	v_add_f32_e32 v60, v13, v61
	v_max_f32_e32 v58, 0, v58
	v_max_f32_e32 v59, 0, v59
	v_max_f32_e32 v60, 0, v60
	v_cvt_pk_f16_f32 v59, v59, v60
	v_cvt_pk_f16_f32 v58, v58, v62
	v_add_f32_e32 v55, v7, v55
	ds_write_b64 v199, v[58:59] offset:32
	v_add_f32_e32 v54, v6, v54
	v_max_f32_e32 v58, 0, v55
	v_add_f32_e32 v55, v8, v56
	v_add_f32_e32 v56, v9, v57
	v_max_f32_e32 v54, 0, v54
	v_max_f32_e32 v55, 0, v55
	v_max_f32_e32 v56, 0, v56
	v_cvt_pk_f16_f32 v55, v55, v56
	v_cvt_pk_f16_f32 v54, v54, v58
	v_add_f32_e32 v51, v3, v51
	ds_write_b64 v199, v[54:55] offset:64
	v_add_f32_e32 v50, v2, v50
	v_max_f32_e32 v54, 0, v51
	v_add_f32_e32 v51, v4, v52
	v_add_f32_e32 v52, v5, v53
	v_max_f32_e32 v50, 0, v50
	v_max_f32_e32 v51, 0, v51
	v_max_f32_e32 v52, 0, v52
	v_cvt_pk_f16_f32 v51, v51, v52
	v_cvt_pk_f16_f32 v50, v50, v54
	ds_write_b64 v199, v[50:51] offset:96
	s_waitcnt lgkmcnt(0)
	ds_read_b128 v[208:211], v202
	ds_read_b128 v[212:215], v202 offset:1152
	ds_bpermute_b32 v216, v203, v68
	ds_bpermute_b32 v217, v203, v69
	ds_bpermute_b32 v218, v204, v68
	ds_bpermute_b32 v219, v204, v69
	v_add_u32_e32 v222, 0, v205
	v_cmp_gt_u32_e64 s[38:39], s24, v222
	v_add_u32_e32 v222, 8, v222
	v_cmp_gt_u32_e64 s[40:41], s24, v222
	s_waitcnt lgkmcnt(0)
	v_lshl_add_u64 v[216:217], v[216:217], 0, v[220:221]
	v_lshl_add_u64 v[218:219], v[218:219], 0, v[220:221]
	s_mov_b64 s[42:43], exec
	s_and_b64 exec, s[42:43], s[38:39]
	global_store_dwordx4 v[216:217], v[208:211], off sc1
	s_and_b64 exec, s[42:43], s[40:41]
	global_store_dwordx4 v[218:219], v[212:215], off sc1
	s_mov_b64 exec, s[42:43]
.LBB4_39:
	s_or_b64 exec, exec, s[2:3]
	v_add_u32_e32 v50, 16, v133
	v_cmp_gt_u32_e32 vcc, s24, v50
	s_mov_b64 s[2:3], exec
	s_cbranch_execz .LBB4_41
	v_add_f32_e32 v47, v15, v47
	v_ashrrev_i32_e32 v135, 31, v134
	v_add_f32_e32 v46, v14, v46
	v_max_f32_e32 v52, 0, v47
	v_add_f32_e32 v47, v16, v48
	v_add_f32_e32 v48, v17, v49
	v_lshlrev_b64 v[50:51], 11, v[134:135]
	v_max_f32_e32 v46, 0, v46
	v_max_f32_e32 v47, 0, v47
	v_max_f32_e32 v48, 0, v48
	v_lshl_add_u64 v[50:51], v[66:67], 0, v[50:51]
	v_cvt_pk_f16_f32 v47, v47, v48
	v_cvt_pk_f16_f32 v46, v46, v52
	v_add_f32_e32 v43, v11, v43
	ds_write_b64 v199, v[46:47]
	v_add_f32_e32 v42, v10, v42
	v_max_f32_e32 v46, 0, v43
	v_add_f32_e32 v43, v12, v44
	v_add_f32_e32 v44, v13, v45
	v_max_f32_e32 v42, 0, v42
	v_max_f32_e32 v43, 0, v43
	v_max_f32_e32 v44, 0, v44
	v_cvt_pk_f16_f32 v43, v43, v44
	v_cvt_pk_f16_f32 v42, v42, v46
	v_add_f32_e32 v39, v7, v39
	ds_write_b64 v199, v[42:43] offset:32
	v_add_f32_e32 v38, v6, v38
	v_max_f32_e32 v42, 0, v39
	v_add_f32_e32 v39, v8, v40
	v_add_f32_e32 v40, v9, v41
	v_max_f32_e32 v38, 0, v38
	v_max_f32_e32 v39, 0, v39
	v_max_f32_e32 v40, 0, v40
	v_cvt_pk_f16_f32 v39, v39, v40
	v_cvt_pk_f16_f32 v38, v38, v42
	v_add_f32_e32 v35, v3, v35
	ds_write_b64 v199, v[38:39] offset:64
	v_add_f32_e32 v34, v2, v34
	v_max_f32_e32 v38, 0, v35
	v_add_f32_e32 v35, v4, v36
	v_add_f32_e32 v36, v5, v37
	v_max_f32_e32 v34, 0, v34
	v_max_f32_e32 v35, 0, v35
	v_max_f32_e32 v36, 0, v36
	v_cvt_pk_f16_f32 v35, v35, v36
	v_cvt_pk_f16_f32 v34, v34, v38
	ds_write_b64 v199, v[34:35] offset:96
	s_waitcnt lgkmcnt(0)
	ds_read_b128 v[208:211], v202
	ds_read_b128 v[212:215], v202 offset:1152
	ds_bpermute_b32 v216, v203, v50
	ds_bpermute_b32 v217, v203, v51
	ds_bpermute_b32 v218, v204, v50
	ds_bpermute_b32 v219, v204, v51
	v_add_u32_e32 v222, 16, v205
	v_cmp_gt_u32_e64 s[38:39], s24, v222
	v_add_u32_e32 v222, 8, v222
	v_cmp_gt_u32_e64 s[40:41], s24, v222
	s_waitcnt lgkmcnt(0)
	v_lshl_add_u64 v[216:217], v[216:217], 0, v[220:221]
	v_lshl_add_u64 v[218:219], v[218:219], 0, v[220:221]
	s_mov_b64 s[42:43], exec
	s_and_b64 exec, s[42:43], s[38:39]
	global_store_dwordx4 v[216:217], v[208:211], off sc1
	s_and_b64 exec, s[42:43], s[40:41]
	global_store_dwordx4 v[218:219], v[212:215], off sc1
	s_mov_b64 exec, s[42:43]
.LBB4_41:
	s_or_b64 exec, exec, s[2:3]
	v_add_u32_e32 v34, 32, v133
	v_cmp_gt_u32_e32 vcc, s24, v34
	s_mov_b64 s[2:3], exec
	s_cbranch_execz .LBB4_43
	v_add_f32_e32 v15, v15, v31
	v_ashrrev_i32_e32 v133, 31, v132
	v_add_f32_e32 v14, v14, v30
	v_max_f32_e32 v30, 0, v15
	v_add_f32_e32 v15, v16, v32
	v_add_f32_e32 v16, v17, v33
	v_lshlrev_b64 v[34:35], 11, v[132:133]
	v_max_f32_e32 v14, 0, v14
	v_max_f32_e32 v15, 0, v15
	v_max_f32_e32 v16, 0, v16
	v_lshl_add_u64 v[34:35], v[66:67], 0, v[34:35]
	v_cvt_pk_f16_f32 v15, v15, v16
	v_cvt_pk_f16_f32 v14, v14, v30
	v_add_f32_e32 v11, v11, v27
	ds_write_b64 v199, v[14:15]
	v_add_f32_e32 v10, v10, v26
	v_max_f32_e32 v14, 0, v11
	v_add_f32_e32 v11, v12, v28
	v_add_f32_e32 v12, v13, v29
	v_max_f32_e32 v10, 0, v10
	v_max_f32_e32 v11, 0, v11
	v_max_f32_e32 v12, 0, v12
	v_cvt_pk_f16_f32 v11, v11, v12
	v_cvt_pk_f16_f32 v10, v10, v14
	v_add_f32_e32 v7, v7, v23
	ds_write_b64 v199, v[10:11] offset:32
	v_add_f32_e32 v6, v6, v22
	v_max_f32_e32 v10, 0, v7
	v_add_f32_e32 v7, v8, v24
	v_add_f32_e32 v8, v9, v25
	v_max_f32_e32 v6, 0, v6
	v_max_f32_e32 v7, 0, v7
	v_max_f32_e32 v8, 0, v8
	v_cvt_pk_f16_f32 v7, v7, v8
	v_cvt_pk_f16_f32 v6, v6, v10
	v_add_f32_e32 v3, v3, v19
	ds_write_b64 v199, v[6:7] offset:64
	v_add_f32_e32 v2, v2, v18
	v_max_f32_e32 v6, 0, v3
	v_add_f32_e32 v3, v4, v20
	v_add_f32_e32 v4, v5, v21
	v_max_f32_e32 v2, 0, v2
	v_max_f32_e32 v3, 0, v3
	v_max_f32_e32 v4, 0, v4
	v_cvt_pk_f16_f32 v3, v3, v4
	v_cvt_pk_f16_f32 v2, v2, v6
	ds_write_b64 v199, v[2:3] offset:96
	s_waitcnt lgkmcnt(0)
	ds_read_b128 v[208:211], v202
	ds_read_b128 v[212:215], v202 offset:1152
	ds_bpermute_b32 v216, v203, v34
	ds_bpermute_b32 v217, v203, v35
	ds_bpermute_b32 v218, v204, v34
	ds_bpermute_b32 v219, v204, v35
	v_add_u32_e32 v222, 32, v205
	v_cmp_gt_u32_e64 s[38:39], s24, v222
	v_add_u32_e32 v222, 8, v222
	v_cmp_gt_u32_e64 s[40:41], s24, v222
	s_waitcnt lgkmcnt(0)
	v_lshl_add_u64 v[216:217], v[216:217], 0, v[220:221]
	v_lshl_add_u64 v[218:219], v[218:219], 0, v[220:221]
	s_mov_b64 s[42:43], exec
	s_and_b64 exec, s[42:43], s[38:39]
	global_store_dwordx4 v[216:217], v[208:211], off sc1
	s_and_b64 exec, s[42:43], s[40:41]
	global_store_dwordx4 v[218:219], v[212:215], off sc1
	s_mov_b64 exec, s[42:43]

.LBB4_55:
	s_or_b64 exec, exec, s[4:5]
	s_waitcnt vmcnt(1)
	ds_write_b128 v78, v[14:17] offset:40960
	s_waitcnt vmcnt(0)
	ds_write_b128 v78, v[22:25] offset:49152
	s_waitcnt lgkmcnt(0)
	s_barrier
	ds_read_b128 v[14:17], v82 offset:40960
	ds_read_b128 v[18:21], v81 offset:12288
	ds_read_b128 v[22:25], v81 offset:14336
	ds_read_b128 v[46:49], v82 offset:43008
	ds_read_b128 v[50:53], v79 offset:12288
	s_waitcnt lgkmcnt(3)
	v_mfma_f32_16x16x32_f16 v[42:45], v[14:17], v[18:21], v[42:45]
	ds_read_b128 v[54:57], v80 offset:43008
	s_lshl_b64 s[0:1], s[0:1], 1
	s_add_u32 s0, s10, s0
	s_waitcnt lgkmcnt(2)
	v_mfma_f32_16x16x32_f16 v[10:13], v[46:49], v[18:21], v[10:13]
	s_addc_u32 s1, s11, s1
	v_lshlrev_b32_e32 v0, 1, v67
	v_mov_b32_e32 v1, 0
	v_mfma_f32_16x16x32_f16 v[18:21], v[14:17], v[22:25], v[34:37]
	v_cmp_gt_u32_e32 vcc, s24, v63
	v_mfma_f32_16x16x32_f16 v[34:37], v[46:49], v[22:25], v[38:41]
	ds_read_b128 v[22:25], v81 offset:16384
	s_nop 1
	ds_read_b128 v[38:41], v80 offset:40960
	s_waitcnt lgkmcnt(1)
	v_mfma_f32_16x16x32_f16 v[14:17], v[14:17], v[22:25], v[30:33]
	v_mfma_f32_16x16x32_f16 v[46:49], v[46:49], v[22:25], v[26:29]
	s_waitcnt lgkmcnt(0)
	v_mfma_f32_16x16x32_f16 v[30:33], v[38:41], v[50:53], v[42:45]
	v_mfma_f32_16x16x32_f16 v[26:29], v[54:57], v[50:53], v[10:13]
	s_nop 2
	ds_read_b128 v[10:13], v79 offset:14336
	ds_read_b128 v[42:45], v79 offset:16384
	s_waitcnt lgkmcnt(1)
	v_mfma_f32_16x16x32_f16 v[22:25], v[38:41], v[10:13], v[18:21]
	v_mfma_f32_16x16x32_f16 v[18:21], v[54:57], v[10:13], v[34:37]
	v_lshl_add_u64 v[10:11], s[0:1], 0, v[0:1]
	v_lshlrev_b32_e32 v0, 1, v65
	v_lshl_add_u64 v[0:1], v[10:11], 0, v[0:1]
	s_waitcnt lgkmcnt(0)
	v_mfma_f32_16x16x32_f16 v[14:17], v[38:41], v[42:45], v[14:17]
	v_mfma_f32_16x16x32_f16 v[10:13], v[54:57], v[42:45], v[46:49]
	v_mbcnt_lo_u32_b32 v196, -1, 0
	v_mbcnt_hi_u32_b32 v196, -1, v196
	v_and_b32_e32 v197, 15, v196
	v_lshrrev_b32_e32 v198, 4, v196
	v_lshrrev_b32_e32 v222, 10, v78
	s_nop 0
	v_readfirstlane_b32 s36, v222
	s_nop 3
	s_and_b32 s36, s36, 7
	s_mulk_i32 s36, 0x500
	s_add_u32 s36, s36, 0x6000
	v_mul_u32_u24_e32 v199, 0x50, v197
	v_lshl_add_u32 v199, v198, 3, v199
	v_add_u32_e32 v199, s36, v199
	v_lshrrev_b32_e32 v200, 2, v196
	v_and_b32_e32 v201, 3, v196
	v_mul_u32_u24_e32 v202, 0x50, v200
	v_lshl_add_u32 v202, v201, 4, v202
	v_add_u32_e32 v202, s36, v202
	v_lshlrev_b32_e32 v203, 2, v200
	v_add_u32_e32 v204, 32, v203
	v_lshlrev_b32_e32 v220, 4, v201
	v_mov_b32_e32 v221, 0
	v_sub_u32_e32 v205, v63, v197
	v_add_u32_e32 v205, v205, v200
	s_mov_b64 s[0:1], exec
	s_cbranch_execz .LBB4_57
	v_add_f32_e32 v31, v7, v31
	v_ashrrev_i32_e32 v67, 31, v66
	v_add_f32_e32 v30, v6, v30
	v_max_f32_e32 v36, 0, v31
	v_add_f32_e32 v31, v8, v32
	v_add_f32_e32 v32, v9, v33
	v_lshlrev_b64 v[34:35], 11, v[66:67]
	v_max_f32_e32 v30, 0, v30
	v_max_f32_e32 v31, 0, v31
	v_max_f32_e32 v32, 0, v32
	v_lshl_add_u64 v[34:35], v[0:1], 0, v[34:35]
	v_cvt_pk_f16_f32 v31, v31, v32
	v_cvt_pk_f16_f32 v30, v30, v36
	v_add_f32_e32 v27, v3, v27
	ds_write_b64 v199, v[30:31]
	v_add_f32_e32 v26, v2, v26
	v_max_f32_e32 v30, 0, v27
	v_add_f32_e32 v27, v4, v28
	v_add_f32_e32 v28, v5, v29
	v_max_f32_e32 v26, 0, v26
	v_max_f32_e32 v27, 0, v27
	v_max_f32_e32 v28, 0, v28
	v_cvt_pk_f16_f32 v27, v27, v28
	v_cvt_pk_f16_f32 v26, v26, v30
	ds_write_b64 v199, v[26:27] offset:32
	s_waitcnt lgkmcnt(0)
	ds_read_b128 v[208:211], v202
	ds_bpermute_b32 v216, v203, v34
	ds_bpermute_b32 v217, v203, v35
	v_add_u32_e32 v222, 0, v205
	v_cmp_gt_u32_e64 s[38:39], s24, v222
	s_waitcnt lgkmcnt(0)
	v_lshl_add_u64 v[216:217], v[216:217], 0, v[220:221]
	s_mov_b64 s[42:43], exec
	s_and_b64 exec, s[42:43], s[38:39]
	global_store_dwordx4 v[216:217], v[208:211], off sc1
	s_mov_b64 exec, s[42:43]
.LBB4_57:
	s_or_b64 exec, exec, s[0:1]
	v_add_u32_e32 v26, 16, v63
	v_cmp_gt_u32_e32 vcc, s24, v26
	s_mov_b64 s[0:1], exec
	s_cbranch_execz .LBB4_59
	v_add_f32_e32 v23, v7, v23
	v_ashrrev_i32_e32 v65, 31, v64
	v_add_f32_e32 v22, v6, v22
	v_max_f32_e32 v28, 0, v23
	v_add_f32_e32 v23, v8, v24
	v_add_f32_e32 v24, v9, v25
	v_lshlrev_b64 v[26:27], 11, v[64:65]
	v_max_f32_e32 v22, 0, v22
	v_max_f32_e32 v23, 0, v23
	v_max_f32_e32 v24, 0, v24
	v_lshl_add_u64 v[26:27], v[0:1], 0, v[26:27]
	v_cvt_pk_f16_f32 v23, v23, v24
	v_cvt_pk_f16_f32 v22, v22, v28
	v_add_f32_e32 v19, v3, v19
	ds_write_b64 v199, v[22:23]
	v_add_f32_e32 v18, v2, v18
	v_max_f32_e32 v22, 0, v19
	v_add_f32_e32 v19, v4, v20
	v_add_f32_e32 v20, v5, v21
	v_max_f32_e32 v18, 0, v18
	v_max_f32_e32 v19, 0, v19
	v_max_f32_e32 v20, 0, v20
	v_cvt_pk_f16_f32 v19, v19, v20
	v_cvt_pk_f16_f32 v18, v18, v22
	ds_write_b64 v199, v[18:19] offset:32
	s_waitcnt lgkmcnt(0)
	ds_read_b128 v[208:211], v202
	ds_bpermute_b32 v216, v203, v26
	ds_bpermute_b32 v217, v203, v27
	v_add_u32_e32 v222, 16, v205
	v_cmp_gt_u32_e64 s[38:39], s24, v222
	s_waitcnt lgkmcnt(0)
	v_lshl_add_u64 v[216:217], v[216:217], 0, v[220:221]
	s_mov_b64 s[42:43], exec
	s_and_b64 exec, s[42:43], s[38:39]
	global_store_dwordx4 v[216:217], v[208:211], off sc1
	s_mov_b64 exec, s[42:43]
.LBB4_59:
	s_or_b64 exec, exec, s[0:1]
	v_add_u32_e32 v18, 32, v63
	v_cmp_gt_u32_e32 vcc, s24, v18
	s_mov_b64 s[0:1], exec
	s_cbranch_execz .LBB4_61
	v_add_f32_e32 v7, v7, v15
	v_ashrrev_i32_e32 v63, 31, v62
	v_add_f32_e32 v6, v6, v14
	v_max_f32_e32 v14, 0, v7
	v_add_f32_e32 v7, v8, v16
	v_add_f32_e32 v8, v9, v17
	v_lshlrev_b64 v[18:19], 11, v[62:63]
	v_max_f32_e32 v6, 0, v6
	v_max_f32_e32 v7, 0, v7
	v_max_f32_e32 v8, 0, v8
	v_lshl_add_u64 v[0:1], v[0:1], 0, v[18:19]
	v_cvt_pk_f16_f32 v7, v7, v8
	v_cvt_pk_f16_f32 v6, v6, v14
	v_add_f32_e32 v3, v3, v11
	ds_write_b64 v199, v[6:7]
	v_add_f32_e32 v2, v2, v10
	v_max_f32_e32 v6, 0, v3
	v_add_f32_e32 v3, v4, v12
	v_add_f32_e32 v4, v5, v13
	v_max_f32_e32 v2, 0, v2
	v_max_f32_e32 v3, 0, v3
	v_max_f32_e32 v4, 0, v4
	v_cvt_pk_f16_f32 v3, v3, v4
	v_cvt_pk_f16_f32 v2, v2, v6
	ds_write_b64 v199, v[2:3] offset:32
	s_waitcnt lgkmcnt(0)
	ds_read_b128 v[208:211], v202
	ds_bpermute_b32 v216, v203, v0
	ds_bpermute_b32 v217, v203, v1
	v_add_u32_e32 v222, 32, v205
	v_cmp_gt_u32_e64 s[38:39], s24, v222
	s_waitcnt lgkmcnt(0)
	v_lshl_add_u64 v[216:217], v[216:217], 0, v[220:221]
	s_mov_b64 s[42:43], exec
	s_and_b64 exec, s[42:43], s[38:39]
	global_store_dwordx4 v[216:217], v[208:211], off sc1
	s_mov_b64 exec, s[42:43]

.LBB5_17:
	s_lshl_b64 s[10:11], s[10:11], 1
	s_add_u32 s10, s6, s10
	s_addc_u32 s11, s7, s11
	s_lshl_b32 s12, s23, 1
	s_add_u32 s10, s10, s12
	s_addc_u32 s11, s11, 0
	v_lshlrev_b32_e32 v76, 1, v75
	v_mov_b32_e32 v77, 0
	v_lshl_add_u64 v[76:77], s[10:11], 0, v[76:77]
	v_cmp_gt_u32_e32 vcc, s20, v68
	v_mbcnt_lo_u32_b32 v196, -1, 0
	v_mbcnt_hi_u32_b32 v196, -1, v196
	v_and_b32_e32 v197, 15, v196
	v_lshrrev_b32_e32 v198, 4, v196
	v_readfirstlane_b32 s36, v68
	s_nop 3
	s_cmp_ge_u32 s36, 48
	s_cselect_b32 s36, 2, 0
	s_lshr_b32 s37, s23, 6
	s_add_u32 s36, s36, s37
	s_mulk_i32 s36, 0x900
	s_add_u32 s36, s36, 0xa000
	v_mul_u32_u24_e32 v199, 0x90, v197
	v_lshl_add_u32 v199, v198, 3, v199
	v_add_u32_e32 v199, s36, v199
	v_lshrrev_b32_e32 v200, 3, v196
	v_and_b32_e32 v201, 7, v196
	v_mul_u32_u24_e32 v202, 0x90, v200
	v_lshl_add_u32 v202, v201, 4, v202
	v_add_u32_e32 v202, s36, v202
	v_lshlrev_b32_e32 v203, 2, v200
	v_add_u32_e32 v204, 32, v203
	v_lshlrev_b32_e32 v220, 4, v201
	v_mov_b32_e32 v221, 0
	v_sub_u32_e32 v205, v68, v197
	v_add_u32_e32 v205, v205, v200
	s_mov_b64 s[10:11], exec
	s_cbranch_execz .LBB5_19
	v_add_f32_e32 v63, v15, v63
	v_ashrrev_i32_e32 v75, 31, v74
	v_add_f32_e32 v62, v14, v62
	v_max_f32_e32 v69, 0, v63
	v_add_f32_e32 v63, v16, v64
	v_add_f32_e32 v64, v17, v65
	v_lshlrev_b64 v[74:75], 11, v[74:75]
	v_max_f32_e32 v62, 0, v62
	v_max_f32_e32 v63, 0, v63
	v_max_f32_e32 v64, 0, v64
	v_lshl_add_u64 v[74:75], v[76:77], 0, v[74:75]
	v_cvt_pk_f16_f32 v63, v63, v64
	v_cvt_pk_f16_f32 v62, v62, v69
	v_add_f32_e32 v59, v11, v59
	ds_write_b64 v199, v[62:63]
	v_add_f32_e32 v58, v10, v58
	v_max_f32_e32 v62, 0, v59
	v_add_f32_e32 v59, v12, v60
	v_add_f32_e32 v60, v13, v61
	v_max_f32_e32 v58, 0, v58
	v_max_f32_e32 v59, 0, v59
	v_max_f32_e32 v60, 0, v60
	v_cvt_pk_f16_f32 v59, v59, v60
	v_cvt_pk_f16_f32 v58, v58, v62
	v_add_f32_e32 v55, v7, v55
	ds_write_b64 v199, v[58:59] offset:32
	v_add_f32_e32 v54, v6, v54
	v_max_f32_e32 v58, 0, v55
	v_add_f32_e32 v55, v8, v56
	v_add_f32_e32 v56, v9, v57
	v_max_f32_e32 v54, 0, v54
	v_max_f32_e32 v55, 0, v55
	v_max_f32_e32 v56, 0, v56
	v_cvt_pk_f16_f32 v55, v55, v56
	v_cvt_pk_f16_f32 v54, v54, v58
	v_add_f32_e32 v47, v3, v47
	ds_write_b64 v199, v[54:55] offset:64
	v_add_f32_e32 v46, v2, v46
	v_max_f32_e32 v54, 0, v47
	v_add_f32_e32 v47, v4, v48
	v_add_f32_e32 v48, v5, v49
	v_max_f32_e32 v46, 0, v46
	v_max_f32_e32 v47, 0, v47
	v_max_f32_e32 v48, 0, v48
	v_cvt_pk_f16_f32 v47, v47, v48
	v_cvt_pk_f16_f32 v46, v46, v54
	ds_write_b64 v199, v[46:47] offset:96
	s_waitcnt lgkmcnt(0)
	ds_read_b128 v[208:211], v202
	ds_read_b128 v[212:215], v202 offset:1152
	ds_bpermute_b32 v216, v203, v74
	ds_bpermute_b32 v217, v203, v75
	ds_bpermute_b32 v218, v204, v74
	ds_bpermute_b32 v219, v204, v75
	v_add_u32_e32 v222, 0, v205
	v_cmp_gt_u32_e64 s[38:39], s20, v222
	v_add_u32_e32 v222, 8, v222
	v_cmp_gt_u32_e64 s[40:41], s20, v222
	s_waitcnt lgkmcnt(0)
	v_lshl_add_u64 v[216:217], v[216:217], 0, v[220:221]
	v_lshl_add_u64 v[218:219], v[218:219], 0, v[220:221]
	s_mov_b64 s[42:43], exec
	s_and_b64 exec, s[42:43], s[38:39]
	global_store_dwordx4 v[216:217], v[208:211], off sc1
	s_and_b64 exec, s[42:43], s[40:41]
	global_store_dwordx4 v[218:219], v[212:215], off sc1
	s_mov_b64 exec, s[42:43]
.LBB5_19:
	s_or_b64 exec, exec, s[10:11]
	v_add_u32_e32 v46, 16, v68
	v_cmp_gt_u32_e32 vcc, s20, v46
	s_mov_b64 s[10:11], exec
	s_cbranch_execz .LBB5_21
	v_add_f32_e32 v43, v15, v43
	v_ashrrev_i32_e32 v73, 31, v72
	v_add_f32_e32 v42, v14, v42
	v_max_f32_e32 v48, 0, v43
	v_add_f32_e32 v43, v16, v44
	v_add_f32_e32 v44, v17, v45
	v_lshlrev_b64 v[46:47], 11, v[72:73]
	v_max_f32_e32 v42, 0, v42
	v_max_f32_e32 v43, 0, v43
	v_max_f32_e32 v44, 0, v44
	v_lshl_add_u64 v[46:47], v[76:77], 0, v[46:47]
	v_cvt_pk_f16_f32 v43, v43, v44
	v_cvt_pk_f16_f32 v42, v42, v48
	v_add_f32_e32 v39, v11, v39
	ds_write_b64 v199, v[42:43]
	v_add_f32_e32 v38, v10, v38
	v_max_f32_e32 v42, 0, v39
	v_add_f32_e32 v39, v12, v40
	v_add_f32_e32 v40, v13, v41
	v_max_f32_e32 v38, 0, v38
	v_max_f32_e32 v39, 0, v39
	v_max_f32_e32 v40, 0, v40
	v_cvt_pk_f16_f32 v39, v39, v40
	v_cvt_pk_f16_f32 v38, v38, v42
	v_add_f32_e32 v35, v7, v35
	ds_write_b64 v199, v[38:39] offset:32
	v_add_f32_e32 v34, v6, v34
	v_max_f32_e32 v38, 0, v35
	v_add_f32_e32 v35, v8, v36
	v_add_f32_e32 v36, v9, v37
	v_max_f32_e32 v34, 0, v34
	v_max_f32_e32 v35, 0, v35
	v_max_f32_e32 v36, 0, v36
	v_cvt_pk_f16_f32 v35, v35, v36
	v_cvt_pk_f16_f32 v34, v34, v38
	v_add_f32_e32 v31, v3, v31
	ds_write_b64 v199, v[34:35] offset:64
	v_add_f32_e32 v30, v2, v30
	v_max_f32_e32 v34, 0, v31
	v_add_f32_e32 v31, v4, v32
	v_add_f32_e32 v32, v5, v33
	v_max_f32_e32 v30, 0, v30
	v_max_f32_e32 v31, 0, v31
	v_max_f32_e32 v32, 0, v32
	v_cvt_pk_f16_f32 v31, v31, v32
	v_cvt_pk_f16_f32 v30, v30, v34
	ds_write_b64 v199, v[30:31] offset:96
	s_waitcnt lgkmcnt(0)
	ds_read_b128 v[208:211], v202
	ds_read_b128 v[212:215], v202 offset:1152
	ds_bpermute_b32 v216, v203, v46
	ds_bpermute_b32 v217, v203, v47
	ds_bpermute_b32 v218, v204, v46
	ds_bpermute_b32 v219, v204, v47
	v_add_u32_e32 v222, 16, v205
	v_cmp_gt_u32_e64 s[38:39], s20, v222
	v_add_u32_e32 v222, 8, v222
	v_cmp_gt_u32_e64 s[40:41], s20, v222
	s_waitcnt lgkmcnt(0)
	v_lshl_add_u64 v[216:217], v[216:217], 0, v[220:221]
	v_lshl_add_u64 v[218:219], v[218:219], 0, v[220:221]
	s_mov_b64 s[42:43], exec
	s_and_b64 exec, s[42:43], s[38:39]
	global_store_dwordx4 v[216:217], v[208:211], off sc1
	s_and_b64 exec, s[42:43], s[40:41]
	global_store_dwordx4 v[218:219], v[212:215], off sc1
	s_mov_b64 exec, s[42:43]
.LBB5_21:
	s_or_b64 exec, exec, s[10:11]
	v_add_u32_e32 v30, 32, v68
	v_cmp_gt_u32_e32 vcc, s20, v30
	s_mov_b64 s[10:11], exec
	s_cbranch_execz .LBB5_23
	v_add_f32_e32 v15, v15, v27
	v_ashrrev_i32_e32 v71, 31, v70
	v_add_f32_e32 v14, v14, v26
	v_max_f32_e32 v26, 0, v15
	v_add_f32_e32 v15, v16, v28
	v_add_f32_e32 v16, v17, v29
	v_lshlrev_b64 v[30:31], 11, v[70:71]
	v_max_f32_e32 v14, 0, v14
	v_max_f32_e32 v15, 0, v15
	v_max_f32_e32 v16, 0, v16
	v_lshl_add_u64 v[30:31], v[76:77], 0, v[30:31]
	v_cvt_pk_f16_f32 v15, v15, v16
	v_cvt_pk_f16_f32 v14, v14, v26
	v_add_f32_e32 v11, v11, v23
	ds_write_b64 v199, v[14:15]
	v_add_f32_e32 v10, v10, v22
	v_max_f32_e32 v14, 0, v11
	v_add_f32_e32 v11, v12, v24
	v_add_f32_e32 v12, v13, v25
	v_max_f32_e32 v10, 0, v10
	v_max_f32_e32 v11, 0, v11
	v_max_f32_e32 v12, 0, v12
	v_cvt_pk_f16_f32 v11, v11, v12
	v_cvt_pk_f16_f32 v10, v10, v14
	v_add_f32_e32 v7, v7, v19
	ds_write_b64 v199, v[10:11] offset:32
	v_add_f32_e32 v6, v6, v18
	v_max_f32_e32 v10, 0, v7
	v_add_f32_e32 v7, v8, v20
	v_add_f32_e32 v8, v9, v21
	v_max_f32_e32 v6, 0, v6
	v_max_f32_e32 v7, 0, v7
	v_max_f32_e32 v8, 0, v8
	v_cvt_pk_f16_f32 v7, v7, v8
	v_cvt_pk_f16_f32 v6, v6, v10
	v_add_f32_e32 v3, v3, v51
	ds_write_b64 v199, v[6:7] offset:64
	v_add_f32_e32 v2, v2, v50
	v_max_f32_e32 v6, 0, v3
	v_add_f32_e32 v3, v4, v52
	v_add_f32_e32 v4, v5, v53
	v_max_f32_e32 v2, 0, v2
	v_max_f32_e32 v3, 0, v3
	v_max_f32_e32 v4, 0, v4
	v_cvt_pk_f16_f32 v3, v3, v4
	v_cvt_pk_f16_f32 v2, v2, v6
	ds_write_b64 v199, v[2:3] offset:96
	s_waitcnt lgkmcnt(0)
	ds_read_b128 v[208:211], v202
	ds_read_b128 v[212:215], v202 offset:1152
	ds_bpermute_b32 v216, v203, v30
	ds_bpermute_b32 v217, v203, v31
	ds_bpermute_b32 v218, v204, v30
	ds_bpermute_b32 v219, v204, v31
	v_add_u32_e32 v222, 32, v205
	v_cmp_gt_u32_e64 s[38:39], s20, v222
	v_add_u32_e32 v222, 8, v222
	v_cmp_gt_u32_e64 s[40:41], s20, v222
	s_waitcnt lgkmcnt(0)
	v_lshl_add_u64 v[216:217], v[216:217], 0, v[220:221]
	v_lshl_add_u64 v[218:219], v[218:219], 0, v[220:221]
	s_mov_b64 s[42:43], exec
	s_and_b64 exec, s[42:43], s[38:39]
	global_store_dwordx4 v[216:217], v[208:211], off sc1
	s_and_b64 exec, s[42:43], s[40:41]
	global_store_dwordx4 v[218:219], v[212:215], off sc1
	s_mov_b64 exec, s[42:43]

.LBB5_26:
	s_mul_i32 s4, s13, 0xa000
	s_add_i32 s4, s4, 0
	v_add_u32_e32 v35, s4, v43
	s_add_i32 s4, s4, s12
	v_add_u32_e32 v80, s4, v41
	s_waitcnt vmcnt(5)
	s_barrier
	v_add_u32_e32 v60, v80, v39
	ds_read_b128 v[56:59], v60 offset:24576
	ds_read_b128 v[60:63], v60 offset:26624
	v_add_u32_e32 v68, v35, v39
	ds_read_b128 v[52:55], v68
	v_add_u32_e32 v35, v35, v37
	s_waitcnt lgkmcnt(0)
	v_mfma_f32_16x16x32_f16 v[26:29], v[56:59], v[52:55], v[26:29]
	ds_read_b128 v[64:67], v68 offset:2048
	v_add_u32_e32 v82, v80, v37
	s_cmp_gt_i32 s13, 0
	v_mfma_f32_16x16x32_f16 v[30:33], v[60:63], v[52:55], v[30:33]
	ds_read_b128 v[52:55], v68 offset:4096
	s_cselect_b32 s4, -1, 2
	s_add_i32 s4, s4, s13
	s_waitcnt lgkmcnt(0)
	v_mfma_f32_16x16x32_f16 v[22:25], v[56:59], v[64:67], v[22:25]
	ds_read_b128 v[68:71], v35
	s_mul_i32 s4, s4, 0xa000
	s_add_i32 s4, s9, s4
	v_mfma_f32_16x16x32_f16 v[18:21], v[60:63], v[64:67], v[18:21]
	ds_read_b128 v[64:67], v82 offset:24576
	v_lshl_add_u64 v[72:73], v[44:45], 0, s[2:3]
	s_mov_b32 m0, s4
	v_mfma_f32_16x16x32_f16 v[14:17], v[56:59], v[52:55], v[14:17]
	ds_read_b128 v[56:59], v82 offset:26624
	v_lshl_add_u64 v[74:75], v[46:47], 0, s[2:3]
	v_lshl_add_u64 v[76:77], v[0:1], 0, s[2:3]
	v_mfma_f32_16x16x32_f16 v[10:13], v[60:63], v[52:55], v[10:13]
	ds_read_b128 v[52:55], v35 offset:2048
	v_lshl_add_u64 v[78:79], v[48:49], 0, s[2:3]
	v_lshl_add_u64 v[80:81], v[50:51], 0, s[2:3]
	s_waitcnt lgkmcnt(0)
	v_mfma_f32_16x16x32_f16 v[26:29], v[64:67], v[68:71], v[26:29]
	ds_read_b128 v[60:63], v35 offset:4096
	v_mfma_f32_16x16x32_f16 v[30:33], v[56:59], v[68:71], v[30:33]
	global_load_lds_dwordx4 v[72:73], off
	s_add_i32 m0, s4, 0x1000
	v_mfma_f32_16x16x32_f16 v[22:25], v[64:67], v[52:55], v[22:25]
	global_load_lds_dwordx4 v[74:75], off
	s_add_i32 m0, s4, 0x2000
	v_mfma_f32_16x16x32_f16 v[18:21], v[56:59], v[52:55], v[18:21]
	global_load_lds_dwordx4 v[76:77], off
	s_add_i32 m0, s4, 0x6000
	s_waitcnt lgkmcnt(0)
	v_mfma_f32_16x16x32_f16 v[14:17], v[64:67], v[60:63], v[14:17]
	global_load_lds_dwordx4 v[78:79], off
	s_add_i32 m0, s4, 0x7000
	v_mfma_f32_16x16x32_f16 v[10:13], v[56:59], v[60:63], v[10:13]
	global_load_lds_dwordx4 v[80:81], off
	s_add_i32 s4, s13, 1
	s_cmp_lg_u32 s13, 2
	s_cselect_b32 s13, s4, 0
	s_add_u32 s2, s2, 0x80
	s_addc_u32 s3, s3, 0
	s_cmpk_lg_i32 s2, 0xf00
	s_cbranch_scc1 .LBB5_26
	s_add_i32 s2, s12, 0
	v_add_u32_e32 v0, s2, v41
	s_waitcnt vmcnt(5)
	s_barrier
	v_add_u32_e32 v1, v0, v39
	ds_read_b128 v[44:47], v1 offset:24576
	v_add_u32_e32 v35, 0, v43
	v_add_u32_e32 v43, v35, v39
	ds_read_b128 v[48:51], v43
	ds_read_b128 v[52:55], v1 offset:26624
	v_add_u32_e32 v1, v35, v37
	s_waitcnt lgkmcnt(0)
	v_mfma_f32_16x16x32_f16 v[26:29], v[44:47], v[48:51], v[26:29]
	ds_read_b128 v[56:59], v43 offset:2048
	v_add_u32_e32 v0, v0, v37
	s_add_i32 s2, s2, 0x10000
	v_mfma_f32_16x16x32_f16 v[30:33], v[52:55], v[48:51], v[30:33]
	ds_read_b128 v[48:51], v43 offset:4096
	s_lshl_b64 s[0:1], s[0:1], 1
	s_add_u32 s0, s6, s0
	s_waitcnt lgkmcnt(0)
	v_mfma_f32_16x16x32_f16 v[22:25], v[44:47], v[56:59], v[22:25]
	ds_read_b128 v[60:63], v1
	s_addc_u32 s1, s7, s1
	v_cmp_gt_u32_e32 vcc, s20, v34
	v_mfma_f32_16x16x32_f16 v[18:21], v[52:55], v[56:59], v[18:21]
	ds_read_b128 v[56:59], v0 offset:24576
	v_mfma_f32_16x16x32_f16 v[14:17], v[44:47], v[48:51], v[14:17]
	ds_read_b128 v[44:47], v0 offset:26624
	v_add_u32_e32 v0, s2, v41
	v_add_u32_e32 v35, v0, v39
	v_mfma_f32_16x16x32_f16 v[10:13], v[52:55], v[48:51], v[10:13]
	ds_read_b128 v[48:51], v1 offset:2048
	v_add_u32_e32 v0, v0, v37
	s_lshl_b32 s2, s8, 1
	s_waitcnt lgkmcnt(0)
	v_mfma_f32_16x16x32_f16 v[26:29], v[56:59], v[60:63], v[26:29]
	ds_read_b128 v[52:55], v1 offset:4096
	s_waitcnt vmcnt(0)
	s_barrier
	v_mfma_f32_16x16x32_f16 v[30:33], v[44:47], v[60:63], v[30:33]
	s_add_u32 s0, s0, s2
	s_addc_u32 s1, s1, 0
	v_mfma_f32_16x16x32_f16 v[22:25], v[56:59], v[48:51], v[22:25]
	v_mfma_f32_16x16x32_f16 v[18:21], v[44:47], v[48:51], v[18:21]
	s_waitcnt lgkmcnt(0)
	v_mfma_f32_16x16x32_f16 v[14:17], v[56:59], v[52:55], v[14:17]
	v_mfma_f32_16x16x32_f16 v[10:13], v[44:47], v[52:55], v[10:13]
	ds_read_b128 v[44:47], v35
	ds_read_b128 v[48:51], v43 offset:40960
	ds_read_b128 v[52:55], v35 offset:2048
	s_waitcnt lgkmcnt(0)
	v_mfma_f32_16x16x32_f16 v[26:29], v[44:47], v[48:51], v[26:29]
	ds_read_b128 v[56:59], v43 offset:43008
	v_mfma_f32_16x16x32_f16 v[48:51], v[52:55], v[48:51], v[30:33]
	s_nop 2
	ds_read_b128 v[30:33], v43 offset:45056
	s_waitcnt lgkmcnt(0)
	v_mfma_f32_16x16x32_f16 v[22:25], v[44:47], v[56:59], v[22:25]
	ds_read_b128 v[60:63], v1 offset:40960
	v_mfma_f32_16x16x32_f16 v[18:21], v[52:55], v[56:59], v[18:21]
	ds_read_b128 v[56:59], v0
	v_mfma_f32_16x16x32_f16 v[14:17], v[44:47], v[30:33], v[14:17]
	ds_read_b128 v[44:47], v0 offset:2048
	v_lshlrev_b32_e32 v0, 1, v42
	v_mfma_f32_16x16x32_f16 v[52:55], v[52:55], v[30:33], v[10:13]
	s_nop 2
	ds_read_b128 v[10:13], v1 offset:43008
	s_waitcnt lgkmcnt(0)
	v_mfma_f32_16x16x32_f16 v[30:33], v[56:59], v[60:63], v[26:29]
	ds_read_b128 v[64:67], v1 offset:45056
	v_mov_b32_e32 v1, 0
	v_lshl_add_u64 v[0:1], s[0:1], 0, v[0:1]
	v_mfma_f32_16x16x32_f16 v[26:29], v[44:47], v[60:63], v[48:51]
	v_mfma_f32_16x16x32_f16 v[22:25], v[56:59], v[10:13], v[22:25]
	v_mfma_f32_16x16x32_f16 v[18:21], v[44:47], v[10:13], v[18:21]
	s_waitcnt lgkmcnt(0)
	v_mfma_f32_16x16x32_f16 v[10:13], v[56:59], v[64:67], v[14:17]
	v_mfma_f32_16x16x32_f16 v[14:17], v[44:47], v[64:67], v[52:55]
	v_mbcnt_lo_u32_b32 v196, -1, 0
	v_mbcnt_hi_u32_b32 v196, -1, v196
	v_and_b32_e32 v197, 15, v196
	v_lshrrev_b32_e32 v198, 4, v196
	v_readfirstlane_b32 s36, v34
	s_nop 3
	s_cmp_ge_u32 s36, 48
	s_cselect_b32 s36, 2, 0
	s_add_u32 s36, s36, s18
	s_mulk_i32 s36, 0x500
	s_add_u32 s36, s36, 0x14000
	v_mul_u32_u24_e32 v199, 0x50, v197
	v_lshl_add_u32 v199, v198, 3, v199
	v_add_u32_e32 v199, s36, v199
	v_lshrrev_b32_e32 v200, 2, v196
	v_and_b32_e32 v201, 3, v196
	v_mul_u32_u24_e32 v202, 0x50, v200
	v_lshl_add_u32 v202, v201, 4, v202
	v_add_u32_e32 v202, s36, v202
	v_lshlrev_b32_e32 v203, 2, v200
	v_add_u32_e32 v204, 32, v203
	v_lshlrev_b32_e32 v220, 4, v201
	v_mov_b32_e32 v221, 0
	v_sub_u32_e32 v205, v34, v197
	v_add_u32_e32 v205, v205, v200
	s_mov_b64 s[0:1], exec
	s_cbranch_execz .LBB5_29
	v_add_f32_e32 v31, v7, v31
	s_waitcnt vmcnt(0)
	v_ashrrev_i32_e32 v41, 31, v40
	v_add_f32_e32 v30, v6, v30
	v_max_f32_e32 v35, 0, v31
	v_add_f32_e32 v31, v8, v32
	v_add_f32_e32 v32, v9, v33
	v_lshlrev_b64 v[40:41], 11, v[40:41]
	v_max_f32_e32 v30, 0, v30
	v_max_f32_e32 v31, 0, v31
	v_max_f32_e32 v32, 0, v32
	v_lshl_add_u64 v[40:41], v[0:1], 0, v[40:41]
	v_cvt_pk_f16_f32 v31, v31, v32
	v_cvt_pk_f16_f32 v30, v30, v35
	v_add_f32_e32 v27, v3, v27
	ds_write_b64 v199, v[30:31]
	v_add_f32_e32 v26, v2, v26
	v_max_f32_e32 v30, 0, v27
	v_add_f32_e32 v27, v4, v28
	v_add_f32_e32 v28, v5, v29
	v_max_f32_e32 v26, 0, v26
	v_max_f32_e32 v27, 0, v27
	v_max_f32_e32 v28, 0, v28
	v_cvt_pk_f16_f32 v27, v27, v28
	v_cvt_pk_f16_f32 v26, v26, v30
	ds_write_b64 v199, v[26:27] offset:32
	s_waitcnt lgkmcnt(0)
	ds_read_b128 v[208:211], v202
	ds_bpermute_b32 v216, v203, v40
	ds_bpermute_b32 v217, v203, v41
	v_add_u32_e32 v222, 0, v205
	v_cmp_gt_u32_e64 s[38:39], s20, v222
	s_waitcnt lgkmcnt(0)
	v_lshl_add_u64 v[216:217], v[216:217], 0, v[220:221]
	s_mov_b64 s[42:43], exec
	s_and_b64 exec, s[42:43], s[38:39]
	global_store_dwordx4 v[216:217], v[208:211], off sc1
	s_mov_b64 exec, s[42:43]
.LBB5_29:
	s_or_b64 exec, exec, s[0:1]
	v_add_u32_e32 v26, 16, v34
	v_cmp_gt_u32_e32 vcc, s20, v26
	s_mov_b64 s[0:1], exec
	s_cbranch_execz .LBB5_31
	v_add_f32_e32 v23, v7, v23
	s_waitcnt vmcnt(0)
	v_ashrrev_i32_e32 v39, 31, v38
	v_add_f32_e32 v22, v6, v22
	v_max_f32_e32 v28, 0, v23
	v_add_f32_e32 v23, v8, v24
	v_add_f32_e32 v24, v9, v25
	v_lshlrev_b64 v[26:27], 11, v[38:39]
	v_max_f32_e32 v22, 0, v22
	v_max_f32_e32 v23, 0, v23
	v_max_f32_e32 v24, 0, v24
	v_lshl_add_u64 v[26:27], v[0:1], 0, v[26:27]
	v_cvt_pk_f16_f32 v23, v23, v24
	v_cvt_pk_f16_f32 v22, v22, v28
	v_add_f32_e32 v19, v3, v19
	ds_write_b64 v199, v[22:23]
	v_add_f32_e32 v18, v2, v18
	v_max_f32_e32 v22, 0, v19
	v_add_f32_e32 v19, v4, v20
	v_add_f32_e32 v20, v5, v21
	v_max_f32_e32 v18, 0, v18
	v_max_f32_e32 v19, 0, v19
	v_max_f32_e32 v20, 0, v20
	v_cvt_pk_f16_f32 v19, v19, v20
	v_cvt_pk_f16_f32 v18, v18, v22
	ds_write_b64 v199, v[18:19] offset:32
	s_waitcnt lgkmcnt(0)
	ds_read_b128 v[208:211], v202
	ds_bpermute_b32 v216, v203, v26
	ds_bpermute_b32 v217, v203, v27
	v_add_u32_e32 v222, 16, v205
	v_cmp_gt_u32_e64 s[38:39], s20, v222
	s_waitcnt lgkmcnt(0)
	v_lshl_add_u64 v[216:217], v[216:217], 0, v[220:221]
	s_mov_b64 s[42:43], exec
	s_and_b64 exec, s[42:43], s[38:39]
	global_store_dwordx4 v[216:217], v[208:211], off sc1
	s_mov_b64 exec, s[42:43]
.LBB5_31:
	s_or_b64 exec, exec, s[0:1]
	v_add_u32_e32 v18, 32, v34
	v_cmp_gt_u32_e32 vcc, s20, v18
	s_mov_b64 s[0:1], exec
	s_cbranch_execz .LBB5_33
	v_add_f32_e32 v7, v7, v11
	s_waitcnt vmcnt(0)
	v_ashrrev_i32_e32 v37, 31, v36
	v_add_f32_e32 v6, v6, v10
	v_max_f32_e32 v10, 0, v7
	v_add_f32_e32 v7, v8, v12
	v_add_f32_e32 v8, v9, v13
	v_lshlrev_b64 v[18:19], 11, v[36:37]
	v_max_f32_e32 v6, 0, v6
	v_max_f32_e32 v7, 0, v7
	v_max_f32_e32 v8, 0, v8
	v_lshl_add_u64 v[0:1], v[0:1], 0, v[18:19]
	v_cvt_pk_f16_f32 v7, v7, v8
	v_cvt_pk_f16_f32 v6, v6, v10
	v_add_f32_e32 v3, v3, v15
	ds_write_b64 v199, v[6:7]
	v_add_f32_e32 v2, v2, v14
	v_max_f32_e32 v6, 0, v3
	v_add_f32_e32 v3, v4, v16
	v_add_f32_e32 v4, v5, v17
	v_max_f32_e32 v2, 0, v2
	v_max_f32_e32 v3, 0, v3
	v_max_f32_e32 v4, 0, v4
	v_cvt_pk_f16_f32 v3, v3, v4
	v_cvt_pk_f16_f32 v2, v2, v6
	ds_write_b64 v199, v[2:3] offset:32
	s_waitcnt lgkmcnt(0)
	ds_read_b128 v[208:211], v202
	ds_bpermute_b32 v216, v203, v0
	ds_bpermute_b32 v217, v203, v1
	v_add_u32_e32 v222, 32, v205
	v_cmp_gt_u32_e64 s[38:39], s20, v222
	s_waitcnt lgkmcnt(0)
	v_lshl_add_u64 v[216:217], v[216:217], 0, v[220:221]
	s_mov_b64 s[42:43], exec
	s_and_b64 exec, s[42:43], s[38:39]
	global_store_dwordx4 v[216:217], v[208:211], off sc1
	s_mov_b64 exec, s[42:43]

.LBB6_39:
	ds_read_b128 v[14:17], v180 offset:24576
	ds_read_b128 v[18:21], v179
	ds_read_b128 v[22:25], v179 offset:4096
	ds_read_b128 v[82:85], v180 offset:28672
	ds_read_b128 v[86:89], v181
	s_waitcnt vmcnt(10)
	v_pk_add_f16 v10, v34, v10
	v_pk_add_f16 v11, v35, v11
	s_waitcnt lgkmcnt(3)
	v_mfma_f32_16x16x32_f16 v[78:81], v[14:17], v[18:21], v[98:101]
	v_pk_add_f16 v12, v36, v12
	v_pk_add_f16 v13, v37, v13
	v_cndmask_b32_e64 v12, v36, v12, s[2:3]
	s_waitcnt lgkmcnt(1)
	v_mfma_f32_16x16x32_f16 v[18:21], v[82:85], v[18:21], v[90:93]
	ds_read_b128 v[98:101], v183 offset:24576
	v_cndmask_b32_e64 v13, v37, v13, s[2:3]
	v_cndmask_b32_e64 v11, v35, v11, s[2:3]
	v_mfma_f32_16x16x32_f16 v[90:93], v[14:17], v[22:25], v[94:97]
	v_cndmask_b32_e64 v10, v34, v10, s[2:3]
	v_cmp_gt_u32_e32 vcc, s18, v170
	s_nop 0
	ds_read_b128 v[94:97], v179 offset:8192
	v_mfma_f32_16x16x32_f16 v[22:25], v[82:85], v[22:25], v[110:113]
	s_waitcnt lgkmcnt(0)
	v_mfma_f32_16x16x32_f16 v[14:17], v[14:17], v[94:97], v[114:117]
	v_mfma_f32_16x16x32_f16 v[82:85], v[82:85], v[94:97], v[118:121]
	ds_read_b128 v[94:97], v183 offset:28672
	v_mfma_f32_16x16x32_f16 v[78:81], v[98:101], v[86:89], v[78:81]
	s_waitcnt lgkmcnt(0)
	v_mfma_f32_16x16x32_f16 v[18:21], v[94:97], v[86:89], v[18:21]
	ds_read_b128 v[86:89], v181 offset:4096
	ds_read_b128 v[102:105], v181 offset:8192
	s_waitcnt lgkmcnt(1)
	v_mfma_f32_16x16x32_f16 v[90:93], v[98:101], v[86:89], v[90:93]
	v_mfma_f32_16x16x32_f16 v[22:25], v[94:97], v[86:89], v[22:25]
	ds_read_b128 v[86:89], v184 offset:24576
	s_waitcnt lgkmcnt(1)
	v_mfma_f32_16x16x32_f16 v[14:17], v[98:101], v[102:105], v[14:17]
	v_mfma_f32_16x16x32_f16 v[82:85], v[94:97], v[102:105], v[82:85]
	ds_read_b128 v[94:97], v182
	ds_read_b128 v[98:101], v182 offset:4096
	ds_read_b128 v[102:105], v184 offset:28672
	ds_read_b128 v[106:109], v185
	s_waitcnt lgkmcnt(3)
	v_mfma_f32_16x16x32_f16 v[78:81], v[86:89], v[94:97], v[78:81]
	s_waitcnt lgkmcnt(1)
	v_mfma_f32_16x16x32_f16 v[18:21], v[102:105], v[94:97], v[18:21]
	ds_read_b128 v[94:97], v182 offset:8192
	v_mfma_f32_16x16x32_f16 v[90:93], v[86:89], v[98:101], v[90:93]
	s_waitcnt lgkmcnt(0)
	v_mfma_f32_16x16x32_f16 v[14:17], v[86:89], v[94:97], v[14:17]
	ds_read_b128 v[86:89], v186 offset:24576
	v_mfma_f32_16x16x32_f16 v[82:85], v[102:105], v[94:97], v[82:85]
	ds_read_b128 v[94:97], v186 offset:28672
	v_mfma_f32_16x16x32_f16 v[22:25], v[102:105], v[98:101], v[22:25]
	ds_read_b128 v[98:101], v185 offset:4096
	ds_read_b128 v[102:105], v185 offset:8192
	ds_write_b128 v151, v[10:13] offset:12288
	s_waitcnt vmcnt(9)
	v_pk_add_f16 v10, v38, v26
	v_pk_add_f16 v11, v39, v27
	v_pk_add_f16 v12, v40, v28
	v_pk_add_f16 v13, v41, v29
	v_cndmask_b32_e64 v12, v40, v12, s[2:3]
	v_cndmask_b32_e64 v13, v41, v13, s[2:3]
	v_cndmask_b32_e64 v11, v39, v11, s[2:3]
	v_cndmask_b32_e64 v10, v38, v10, s[2:3]
	ds_write_b128 v151, v[10:13] offset:16384
	s_waitcnt vmcnt(8)
	v_pk_add_f16 v10, v42, v30
	v_pk_add_f16 v11, v43, v31
	v_pk_add_f16 v12, v44, v32
	v_pk_add_f16 v13, v45, v33
	v_cndmask_b32_e64 v12, v44, v12, s[2:3]
	v_cndmask_b32_e64 v13, v45, v13, s[2:3]
	v_cndmask_b32_e64 v11, v43, v11, s[2:3]
	v_cndmask_b32_e64 v10, v42, v10, s[2:3]
	s_waitcnt lgkmcnt(3)
	v_mfma_f32_16x16x32_f16 v[90:93], v[86:89], v[98:101], v[90:93]
	s_lshl_b64 s[2:3], s[14:15], 1
	s_add_u32 s2, s10, s2
	s_addc_u32 s3, s11, s3
	v_mfma_f32_16x16x32_f16 v[22:25], v[94:97], v[98:101], v[22:25]
	v_add_u32_e32 v98, 0xe000, v151
	ds_write_b128 v151, v[10:13] offset:20480
	s_waitcnt vmcnt(7)
	ds_write_b128 v151, v[46:49] offset:57344
	s_waitcnt vmcnt(6)
	ds_write_b128 v151, v[50:53] offset:61440
	s_waitcnt vmcnt(5)
	ds_write_b128 v98, v[54:57] offset:8192
	s_waitcnt vmcnt(4)
	ds_write_b128 v98, v[58:61] offset:12288
	s_waitcnt vmcnt(3)
	ds_write_b128 v98, v[62:65] offset:16384
	s_waitcnt vmcnt(2)
	ds_write_b128 v98, v[66:69] offset:20480
	s_waitcnt vmcnt(1)
	ds_write_b128 v98, v[70:73] offset:24576
	s_waitcnt vmcnt(0)
	ds_write_b128 v98, v[74:77] offset:28672
	s_waitcnt lgkmcnt(0)
	s_barrier
	ds_read_b128 v[10:13], v180 offset:57344
	ds_read_b128 v[30:33], v179 offset:12288
	ds_read_b128 v[34:37], v179 offset:16384
	v_mfma_f32_16x16x32_f16 v[78:81], v[86:89], v[106:109], v[78:81]
	ds_read_b128 v[42:45], v180 offset:61440
	ds_read_b128 v[46:49], v181 offset:12288
	v_mfma_f32_16x16x32_f16 v[18:21], v[94:97], v[106:109], v[18:21]
	s_waitcnt lgkmcnt(3)
	v_mfma_f32_16x16x32_f16 v[38:41], v[10:13], v[30:33], v[78:81]
	s_waitcnt lgkmcnt(1)
	v_mfma_f32_16x16x32_f16 v[18:21], v[42:45], v[30:33], v[18:21]
	v_mfma_f32_16x16x32_f16 v[30:33], v[10:13], v[34:37], v[90:93]
	v_mfma_f32_16x16x32_f16 v[22:25], v[42:45], v[34:37], v[22:25]
	ds_read_b128 v[34:37], v179 offset:20480
	v_mfma_f32_16x16x32_f16 v[14:17], v[86:89], v[102:105], v[14:17]
	v_mfma_f32_16x16x32_f16 v[26:29], v[94:97], v[102:105], v[82:85]
	s_waitcnt lgkmcnt(0)
	v_mfma_f32_16x16x32_f16 v[10:13], v[10:13], v[34:37], v[14:17]
	s_nop 4
	ds_read_b128 v[14:17], v183 offset:57344
	v_mfma_f32_16x16x32_f16 v[26:29], v[42:45], v[34:37], v[26:29]
	ds_read_b128 v[34:37], v183 offset:61440
	s_waitcnt lgkmcnt(1)
	v_mfma_f32_16x16x32_f16 v[38:41], v[14:17], v[46:49], v[38:41]
	s_waitcnt lgkmcnt(0)
	v_mfma_f32_16x16x32_f16 v[18:21], v[34:37], v[46:49], v[18:21]
	ds_read_b128 v[42:45], v181 offset:16384
	ds_read_b128 v[46:49], v181 offset:20480
	s_waitcnt lgkmcnt(1)
	v_mfma_f32_16x16x32_f16 v[30:33], v[14:17], v[42:45], v[30:33]
	s_waitcnt lgkmcnt(0)
	v_mfma_f32_16x16x32_f16 v[10:13], v[14:17], v[46:49], v[10:13]
	ds_read_b128 v[14:17], v184 offset:57344
	v_mfma_f32_16x16x32_f16 v[22:25], v[34:37], v[42:45], v[22:25]
	v_mfma_f32_16x16x32_f16 v[26:29], v[34:37], v[46:49], v[26:29]
	ds_read_b128 v[34:37], v182 offset:12288
	ds_read_b128 v[42:45], v182 offset:16384
	ds_read_b128 v[46:49], v184 offset:61440
	ds_read_b128 v[50:53], v185 offset:12288
	ds_read_b128 v[54:57], v186 offset:61440
	s_waitcnt lgkmcnt(4)
	v_mfma_f32_16x16x32_f16 v[38:41], v[14:17], v[34:37], v[38:41]
	s_waitcnt lgkmcnt(2)
	v_mfma_f32_16x16x32_f16 v[18:21], v[46:49], v[34:37], v[18:21]
	v_mfma_f32_16x16x32_f16 v[34:37], v[14:17], v[42:45], v[30:33]
	v_mfma_f32_16x16x32_f16 v[42:45], v[46:49], v[42:45], v[22:25]
	s_nop 2
	ds_read_b128 v[22:25], v182 offset:20480
	s_waitcnt lgkmcnt(0)
	v_mfma_f32_16x16x32_f16 v[10:13], v[14:17], v[22:25], v[10:13]
	ds_read_b128 v[14:17], v186 offset:57344
	v_mfma_f32_16x16x32_f16 v[46:49], v[46:49], v[22:25], v[26:29]
	s_waitcnt lgkmcnt(0)
	v_mfma_f32_16x16x32_f16 v[30:33], v[14:17], v[50:53], v[38:41]
	v_mfma_f32_16x16x32_f16 v[26:29], v[54:57], v[50:53], v[18:21]
	s_nop 2
	ds_read_b128 v[18:21], v185 offset:16384
	ds_read_b128 v[38:41], v185 offset:20480
	s_waitcnt lgkmcnt(1)
	v_mfma_f32_16x16x32_f16 v[22:25], v[14:17], v[18:21], v[34:37]
	s_nop 2
	v_lshlrev_b32_e32 v34, 1, v149
	v_mov_b32_e32 v35, 0
	s_waitcnt lgkmcnt(0)
	v_mfma_f32_16x16x32_f16 v[14:17], v[14:17], v[38:41], v[10:13]
	s_nop 2
	v_lshl_add_u64 v[10:11], s[2:3], 0, v[34:35]
	v_lshlrev_b32_e32 v34, 1, v147
	v_mfma_f32_16x16x32_f16 v[18:21], v[54:57], v[18:21], v[42:45]
	v_lshl_add_u64 v[34:35], v[10:11], 0, v[34:35]
	v_mfma_f32_16x16x32_f16 v[10:13], v[54:57], v[38:41], v[46:49]
	v_mbcnt_lo_u32_b32 v196, -1, 0
	v_mbcnt_hi_u32_b32 v196, -1, v196
	v_and_b32_e32 v197, 15, v196
	v_lshrrev_b32_e32 v198, 4, v196
	v_lshrrev_b32_e32 v222, 10, v151
	s_nop 0
	v_readfirstlane_b32 s36, v222
	s_nop 3
	s_and_b32 s36, s36, 7
	s_mulk_i32 s36, 0x500
	s_add_u32 s36, s36, 0x6000
	v_mul_u32_u24_e32 v199, 0x50, v197
	v_lshl_add_u32 v199, v198, 3, v199
	v_add_u32_e32 v199, s36, v199
	v_lshrrev_b32_e32 v200, 2, v196
	v_and_b32_e32 v201, 3, v196
	v_mul_u32_u24_e32 v202, 0x50, v200
	v_lshl_add_u32 v202, v201, 4, v202
	v_add_u32_e32 v202, s36, v202
	v_lshlrev_b32_e32 v203, 2, v200
	v_add_u32_e32 v204, 32, v203
	v_lshlrev_b32_e32 v220, 4, v201
	v_mov_b32_e32 v221, 0
	v_sub_u32_e32 v205, v170, v197
	v_add_u32_e32 v205, v205, v200
	s_mov_b64 s[2:3], exec
	s_cbranch_execz .LBB6_41
	v_add_f32_e32 v31, v7, v31
	v_ashrrev_i32_e32 v153, 31, v152
	v_add_f32_e32 v30, v6, v30
	v_max_f32_e32 v38, 0, v31
	v_add_f32_e32 v31, v8, v32
	v_add_f32_e32 v32, v9, v33
	v_lshlrev_b64 v[36:37], 11, v[152:153]
	v_max_f32_e32 v30, 0, v30
	v_max_f32_e32 v31, 0, v31
	v_max_f32_e32 v32, 0, v32
	v_lshl_add_u64 v[36:37], v[34:35], 0, v[36:37]
	v_cvt_pk_f16_f32 v31, v31, v32
	v_cvt_pk_f16_f32 v30, v30, v38
	v_add_f32_e32 v27, v3, v27
	ds_write_b64 v199, v[30:31]
	v_add_f32_e32 v26, v2, v26
	v_max_f32_e32 v30, 0, v27
	v_add_f32_e32 v27, v4, v28
	v_add_f32_e32 v28, v5, v29
	v_max_f32_e32 v26, 0, v26
	v_max_f32_e32 v27, 0, v27
	v_max_f32_e32 v28, 0, v28
	v_cvt_pk_f16_f32 v27, v27, v28
	v_cvt_pk_f16_f32 v26, v26, v30
	ds_write_b64 v199, v[26:27] offset:32
	s_waitcnt lgkmcnt(0)
	ds_read_b128 v[208:211], v202
	ds_bpermute_b32 v216, v203, v36
	ds_bpermute_b32 v217, v203, v37
	v_add_u32_e32 v222, 0, v205
	v_cmp_gt_u32_e64 s[38:39], s18, v222
	s_waitcnt lgkmcnt(0)
	v_lshl_add_u64 v[216:217], v[216:217], 0, v[220:221]
	s_mov_b64 s[42:43], exec
	s_and_b64 exec, s[42:43], s[38:39]
	global_store_dwordx4 v[216:217], v[208:211], off sc1
	s_mov_b64 exec, s[42:43]
.LBB6_41:
	s_or_b64 exec, exec, s[2:3]
	v_or_b32_e32 v26, 16, v170
	v_cmp_gt_u32_e32 vcc, s18, v26
	s_mov_b64 s[2:3], exec
	s_cbranch_execz .LBB6_43
	v_add_f32_e32 v23, v7, v23
	v_ashrrev_i32_e32 v151, 31, v150
	v_add_f32_e32 v22, v6, v22
	v_max_f32_e32 v28, 0, v23
	v_add_f32_e32 v23, v8, v24
	v_add_f32_e32 v24, v9, v25
	v_lshlrev_b64 v[26:27], 11, v[150:151]
	v_max_f32_e32 v22, 0, v22
	v_max_f32_e32 v23, 0, v23
	v_max_f32_e32 v24, 0, v24
	v_lshl_add_u64 v[26:27], v[34:35], 0, v[26:27]
	v_cvt_pk_f16_f32 v23, v23, v24
	v_cvt_pk_f16_f32 v22, v22, v28
	v_add_f32_e32 v19, v3, v19
	ds_write_b64 v199, v[22:23]
	v_add_f32_e32 v18, v2, v18
	v_max_f32_e32 v22, 0, v19
	v_add_f32_e32 v19, v4, v20
	v_add_f32_e32 v20, v5, v21
	v_max_f32_e32 v18, 0, v18
	v_max_f32_e32 v19, 0, v19
	v_max_f32_e32 v20, 0, v20
	v_cvt_pk_f16_f32 v19, v19, v20
	v_cvt_pk_f16_f32 v18, v18, v22
	ds_write_b64 v199, v[18:19] offset:32
	s_waitcnt lgkmcnt(0)
	ds_read_b128 v[208:211], v202
	ds_bpermute_b32 v216, v203, v26
	ds_bpermute_b32 v217, v203, v27
	v_add_u32_e32 v222, 16, v205
	v_cmp_gt_u32_e64 s[38:39], s18, v222
	s_waitcnt lgkmcnt(0)
	v_lshl_add_u64 v[216:217], v[216:217], 0, v[220:221]
	s_mov_b64 s[42:43], exec
	s_and_b64 exec, s[42:43], s[38:39]
	global_store_dwordx4 v[216:217], v[208:211], off sc1
	s_mov_b64 exec, s[42:43]
.LBB6_43:
	s_or_b64 exec, exec, s[2:3]
	v_or_b32_e32 v18, 32, v170
	v_cmp_gt_u32_e32 vcc, s18, v18
	s_mov_b64 s[2:3], exec
	s_cbranch_execz .LBB6_45
	v_add_f32_e32 v7, v7, v15
	v_ashrrev_i32_e32 v149, 31, v148
	v_add_f32_e32 v6, v6, v14
	v_max_f32_e32 v14, 0, v7
	v_add_f32_e32 v7, v8, v16
	v_add_f32_e32 v8, v9, v17
	v_lshlrev_b64 v[18:19], 11, v[148:149]
	v_max_f32_e32 v6, 0, v6
	v_max_f32_e32 v7, 0, v7
	v_max_f32_e32 v8, 0, v8
	v_lshl_add_u64 v[18:19], v[34:35], 0, v[18:19]
	v_cvt_pk_f16_f32 v7, v7, v8
	v_cvt_pk_f16_f32 v6, v6, v14
	v_add_f32_e32 v3, v3, v11
	ds_write_b64 v199, v[6:7]
	v_add_f32_e32 v2, v2, v10
	v_max_f32_e32 v6, 0, v3
	v_add_f32_e32 v3, v4, v12
	v_add_f32_e32 v4, v5, v13
	v_max_f32_e32 v2, 0, v2
	v_max_f32_e32 v3, 0, v3
	v_max_f32_e32 v4, 0, v4
	v_cvt_pk_f16_f32 v3, v3, v4
	v_cvt_pk_f16_f32 v2, v2, v6
	ds_write_b64 v199, v[2:3] offset:32
	s_waitcnt lgkmcnt(0)
	ds_read_b128 v[208:211], v202
	ds_bpermute_b32 v216, v203, v18
	ds_bpermute_b32 v217, v203, v19
	v_add_u32_e32 v222, 32, v205
	v_cmp_gt_u32_e64 s[38:39], s18, v222
	s_waitcnt lgkmcnt(0)
	v_lshl_add_u64 v[216:217], v[216:217], 0, v[220:221]
	s_mov_b64 s[42:43], exec
	s_and_b64 exec, s[42:43], s[38:39]
	global_store_dwordx4 v[216:217], v[208:211], off sc1
	s_mov_b64 exec, s[42:43]

.LBB7_4:
	s_andn2_b64 vcc, exec, s[6:7]
	s_cbranch_vccnz .LBB7_11
	s_cmpk_gt_i32 s4, 0x1fe
	s_cbranch_scc1 .LBB7_11
	s_load_dwordx2 s[2:3], s[0:1], 0x18
	s_ashr_i32 s5, s4, 31
	s_lshl_b64 s[6:7], s[4:5], 2
	s_waitcnt lgkmcnt(0)
	s_add_u32 s2, s2, s6
	s_addc_u32 s3, s3, s7
	s_load_dword s11, s[2:3], 0x0
	s_waitcnt lgkmcnt(0)
	s_cmp_lt_i32 s11, 0
	s_cbranch_scc1 .LBB7_11
	s_load_dwordx2 s[2:3], s[0:1], 0x10
	s_lshl_b32 s4, s4, 6
	s_ashr_i32 s5, s4, 31
	s_lshl_b64 s[8:9], s[4:5], 2
	v_lshrrev_b32_e32 v1, 4, v0
	s_load_dwordx4 s[4:7], s[0:1], 0x0
	s_waitcnt lgkmcnt(0)
	s_add_u32 s2, s2, s8
	s_addc_u32 s3, s3, s9
	v_lshlrev_b32_e32 v3, 2, v1
	global_load_dword v2, v3, s[2:3]
	global_load_dword v4, v3, s[2:3] offset:128
	s_load_dwordx2 s[12:13], s[0:1], 0x20
	s_load_dwordx2 s[8:9], s[0:1], 0x30
	v_and_b32_e32 v96, 15, v0
	v_mov_b32_e32 v25, 0
	v_lshlrev_b32_e32 v24, 4, v96
	s_and_b32 s1, s11, 0xff
	v_lshl_add_u64 v[6:7], s[4:5], 0, v[24:25]
	s_lshr_b32 s4, s11, 8
	s_lshl_b32 s0, s1, 21
	s_waitcnt lgkmcnt(0)
	s_add_u32 s12, s12, s0
	s_addc_u32 s13, s13, 0
	s_lshl_b32 s0, s10, 7
	v_or_b32_e32 v8, s0, v1
	v_ashrrev_i32_e32 v9, 31, v8
	v_lshlrev_b64 v[8:9], 11, v[8:9]
	v_lshl_add_u64 v[8:9], s[12:13], 0, v[8:9]
	s_mov_b32 s14, 0x10000
	v_lshl_add_u64 v[8:9], v[8:9], 0, v[24:25]
	v_add_co_u32_e32 v10, vcc, s14, v8
	s_mov_b32 s15, 0x20000
	s_nop 0
	v_addc_co_u32_e32 v11, vcc, 0, v9, vcc
	v_add_co_u32_e32 v12, vcc, s15, v8
	s_mov_b32 s16, 0x30000
	s_nop 0
	v_addc_co_u32_e32 v13, vcc, 0, v9, vcc
	v_add_co_u32_e32 v14, vcc, s16, v8
	global_load_dwordx4 v[32:35], v[8:9], off
	s_nop 0
	v_addc_co_u32_e32 v15, vcc, 0, v9, vcc
	global_load_dwordx4 v[36:39], v[10:11], off
	global_load_dwordx4 v[40:43], v[12:13], off
	global_load_dwordx4 v[44:47], v[14:15], off
	v_bfe_u32 v30, v0, 6, 2
	v_bfe_u32 v29, v0, 4, 2
	s_movk_i32 s5, 0xf0
	s_lshl_b32 s1, s1, 12
	v_lshlrev_b32_e32 v21, 8, v96
	v_lshlrev_b32_e32 v24, 7, v30
	s_waitcnt vmcnt(5)
	v_ashrrev_i32_e32 v3, 31, v2
	s_waitcnt vmcnt(4)
	v_ashrrev_i32_e32 v5, 31, v4
	v_lshlrev_b64 v[2:3], 11, v[2:3]
	v_lshlrev_b64 v[4:5], 11, v[4:5]
	v_lshl_add_u64 v[16:17], v[6:7], 0, v[2:3]
	v_lshl_add_u64 v[18:19], v[6:7], 0, v[4:5]
	global_load_dwordx4 v[48:51], v[16:17], off
	global_load_dwordx4 v[52:55], v[18:19], off
	global_load_dwordx4 v[56:59], v[16:17], off offset:256
	global_load_dwordx4 v[60:63], v[18:19], off offset:256
	global_load_dwordx4 v[64:67], v[8:9], off offset:256
	global_load_dwordx4 v[68:71], v[10:11], off offset:256
	global_load_dwordx4 v[72:75], v[12:13], off offset:256
	global_load_dwordx4 v[76:79], v[14:15], off offset:256
	v_lshrrev_b32_e32 v2, 8, v0
	v_xor_b32_e32 v0, v1, v0
	v_lshlrev_b32_e32 v3, 8, v1
	v_lshlrev_b32_e32 v0, 4, v0
	v_and_or_b32 v0, v0, s5, v3
	s_add_u32 s5, s8, s1
	s_addc_u32 s10, s9, 0
	s_ashr_i32 s1, s0, 31
	s_lshl_b64 s[8:9], s[0:1], 2
	s_add_u32 s8, s5, s8
	v_lshlrev_b32_e32 v4, 13, v30
	v_bitop3_b32 v1, v1, v96, 3 bitop3:0x6c
	s_addc_u32 s9, s10, s9
	v_lshl_or_b32 v27, v2, 5, v96
	v_add3_u32 v97, 0, v4, v21
	v_lshlrev_b32_e32 v100, 4, v1
	v_add_u32_e32 v20, 0, v0
	v_lshl_add_u64 v[0:1], s[8:9], 0, v[24:25]
	v_lshlrev_b32_e32 v24, 4, v29
	v_lshlrev_b32_e32 v28, 2, v27
	v_add_u32_e32 v31, v97, v100
	v_lshl_add_u64 v[22:23], v[0:1], 0, v[24:25]
	v_lshlrev_b32_e32 v80, 13, v2
	global_load_dword v26, v28, s[2:3] offset:64
	global_load_dwordx4 v[4:7], v[22:23], off
	global_load_dwordx4 v[0:3], v[22:23], off offset:64
	v_bitop3_b32 v23, v29, v96, 4 bitop3:0x36
	v_lshlrev_b32_e32 v101, 4, v23
	v_add3_u32 v22, 0, v80, v21
	v_add_u32_e32 v21, v22, v100
	v_add_u32_e32 v23, v22, v101
	v_bitop3_b32 v24, v29, v96, 8 bitop3:0x36
	v_lshlrev_b32_e32 v102, 4, v24
	v_add_u32_e32 v24, v22, v102
	v_add_u32_e32 v104, 0x8000, v97
	v_add_u32_e32 v116, 0x8000, v20
	s_lshl_b64 s[0:1], s[0:1], 1
	s_add_u32 s0, s6, s0
	s_addc_u32 s1, s7, s1
	v_cmp_gt_u32_e32 vcc, s4, v27
	s_waitcnt vmcnt(14)
	ds_write_b128 v20, v[32:35] offset:32768
	s_waitcnt vmcnt(13)
	ds_write_b128 v20, v[36:39] offset:40960
	s_waitcnt vmcnt(12)
	ds_write_b128 v20, v[40:43] offset:49152
	s_waitcnt vmcnt(11)
	ds_write_b128 v20, v[44:47] offset:57344
	s_waitcnt vmcnt(10)
	ds_write_b128 v20, v[48:51]
	s_waitcnt vmcnt(9)
	ds_write_b128 v20, v[52:55] offset:8192
	s_waitcnt lgkmcnt(0)
	s_barrier
	ds_read_b128 v[34:37], v31 offset:32768
	v_add_u32_e32 v32, v97, v101
	ds_read_b128 v[38:41], v31 offset:36864
	ds_read_b128 v[42:45], v21
	ds_read_b128 v[46:49], v21 offset:4096
	ds_read_b128 v[80:83], v32 offset:32768
	ds_read_b128 v[88:91], v23
	ds_read_b128 v[92:95], v32 offset:36864
	s_waitcnt lgkmcnt(4)
	v_mfma_f32_16x16x32_f16 v[50:53], v[34:37], v[42:45], 0
	v_bitop3_b32 v33, v29, v96, 12 bitop3:0x36
	v_lshlrev_b32_e32 v103, 4, v33
	v_add_u32_e32 v33, v97, v103
	v_mfma_f32_16x16x32_f16 v[42:45], v[38:41], v[42:45], 0
	v_add_u32_e32 v22, v22, v103
	s_waitcnt lgkmcnt(3)
	v_mfma_f32_16x16x32_f16 v[84:87], v[34:37], v[46:49], 0
	v_add_u32_e32 v35, v97, v102
	v_add_u32_e32 v34, v104, v100
	v_mfma_f32_16x16x32_f16 v[36:39], v[38:41], v[46:49], 0
	ds_read_b128 v[46:49], v23 offset:4096
	s_waitcnt lgkmcnt(2)
	v_mfma_f32_16x16x32_f16 v[50:53], v[80:83], v[88:91], v[50:53]
	s_waitcnt lgkmcnt(1)
	v_mfma_f32_16x16x32_f16 v[40:43], v[92:95], v[88:91], v[42:45]
	ds_read_b128 v[88:91], v35 offset:32768
	s_waitcnt lgkmcnt(1)
	v_mfma_f32_16x16x32_f16 v[80:83], v[80:83], v[46:49], v[84:87]
	s_nop 2
	ds_read_b128 v[84:87], v24
	ds_read_b128 v[96:99], v35 offset:36864
	v_mfma_f32_16x16x32_f16 v[36:39], v[92:95], v[46:49], v[36:39]
	ds_read_b128 v[44:47], v24 offset:4096
	s_waitcnt lgkmcnt(2)
	v_mfma_f32_16x16x32_f16 v[48:51], v[88:91], v[84:87], v[50:53]
	s_nop 2
	ds_read_b128 v[52:55], v22
	ds_read_b128 v[92:95], v22 offset:4096
	s_waitcnt vmcnt(8)
	ds_write_b128 v20, v[56:59] offset:16384
	s_waitcnt lgkmcnt(4)
	v_mfma_f32_16x16x32_f16 v[40:43], v[96:99], v[84:87], v[40:43]
	ds_read_b128 v[56:59], v33 offset:32768
	ds_read_b128 v[84:87], v33 offset:36864
	s_waitcnt vmcnt(7)
	ds_write_b128 v20, v[60:63] offset:24576
	s_waitcnt vmcnt(6)
	ds_write_b128 v116, v[64:67] offset:32768
	s_waitcnt vmcnt(5)
	ds_write_b128 v116, v[68:71] offset:40960
	s_waitcnt vmcnt(4)
	ds_write_b128 v116, v[72:75] offset:49152
	s_waitcnt lgkmcnt(9)
	v_mfma_f32_16x16x32_f16 v[60:63], v[88:91], v[44:47], v[80:83]
	s_waitcnt vmcnt(3)
	ds_write_b128 v116, v[76:79] offset:57344
	v_mfma_f32_16x16x32_f16 v[36:39], v[96:99], v[44:47], v[36:39]
	global_load_dwordx4 v[44:47], v[16:17], off offset:512
	global_load_dwordx4 v[64:67], v[18:19], off offset:512
	global_load_dwordx4 v[68:71], v[8:9], off offset:512
	global_load_dwordx4 v[72:75], v[10:11], off offset:512
	global_load_dwordx4 v[76:79], v[12:13], off offset:512
	global_load_dwordx4 v[80:83], v[14:15], off offset:512
	s_waitcnt lgkmcnt(0)
	v_mfma_f32_16x16x32_f16 v[48:51], v[56:59], v[52:55], v[48:51]
	s_barrier
	v_mfma_f32_16x16x32_f16 v[40:43], v[84:87], v[52:55], v[40:43]
	v_mfma_f32_16x16x32_f16 v[52:55], v[56:59], v[92:95], v[60:63]
	ds_read_b128 v[56:59], v34 offset:32768
	s_nop 1
	ds_read_b128 v[60:63], v34 offset:36864
	v_mfma_f32_16x16x32_f16 v[84:87], v[84:87], v[92:95], v[36:39]
	s_nop 2
	ds_read_b128 v[36:39], v21 offset:16384
	ds_read_b128 v[88:91], v21 offset:20480
	s_waitcnt lgkmcnt(1)
	v_mfma_f32_16x16x32_f16 v[48:51], v[56:59], v[36:39], v[48:51]
	v_mfma_f32_16x16x32_f16 v[38:41], v[60:63], v[36:39], v[40:43]
	v_add_u32_e32 v36, v104, v101
	v_add_u32_e32 v37, v104, v102
	s_waitcnt lgkmcnt(0)
	v_mfma_f32_16x16x32_f16 v[52:55], v[56:59], v[88:91], v[52:55]
	ds_read_b128 v[56:59], v36 offset:32768
	ds_read_b128 v[92:95], v36 offset:36864
	v_mfma_f32_16x16x32_f16 v[60:63], v[60:63], v[88:91], v[84:87]
	s_nop 2
	ds_read_b128 v[84:87], v23 offset:16384
	ds_read_b128 v[88:91], v23 offset:20480
	s_waitcnt lgkmcnt(1)
	v_mfma_f32_16x16x32_f16 v[48:51], v[56:59], v[84:87], v[48:51]
	v_mfma_f32_16x16x32_f16 v[38:41], v[92:95], v[84:87], v[38:41]
	s_waitcnt lgkmcnt(0)
	v_mfma_f32_16x16x32_f16 v[52:55], v[56:59], v[88:91], v[52:55]
	ds_read_b128 v[56:59], v37 offset:32768
	ds_read_b128 v[84:87], v37 offset:36864
	v_mfma_f32_16x16x32_f16 v[60:63], v[92:95], v[88:91], v[60:63]
	ds_read_b128 v[88:91], v24 offset:16384
	ds_read_b128 v[92:95], v24 offset:20480
	s_waitcnt lgkmcnt(1)
	v_mfma_f32_16x16x32_f16 v[40:43], v[84:87], v[88:91], v[38:41]
	s_nop 2
	v_add_u32_e32 v38, v104, v103
	v_mfma_f32_16x16x32_f16 v[48:51], v[56:59], v[88:91], v[48:51]
	s_waitcnt lgkmcnt(0)
	v_mfma_f32_16x16x32_f16 v[52:55], v[56:59], v[92:95], v[52:55]
	ds_read_b128 v[56:59], v38 offset:32768
	ds_read_b128 v[88:91], v38 offset:36864
	global_load_dwordx4 v[96:99], v[16:17], off offset:768
	v_mfma_f32_16x16x32_f16 v[60:63], v[84:87], v[92:95], v[60:63]
	ds_read_b128 v[84:87], v22 offset:16384
	ds_read_b128 v[92:95], v22 offset:20480
	global_load_dwordx4 v[100:103], v[18:19], off offset:768
	global_load_dwordx4 v[104:107], v[8:9], off offset:768
	global_load_dwordx4 v[108:111], v[10:11], off offset:768
	global_load_dwordx4 v[112:115], v[12:13], off offset:768
	s_waitcnt lgkmcnt(1)
	v_mfma_f32_16x16x32_f16 v[48:51], v[56:59], v[84:87], v[48:51]
	v_mfma_f32_16x16x32_f16 v[40:43], v[88:91], v[84:87], v[40:43]
	global_load_dwordx4 v[84:87], v[14:15], off offset:768
	s_waitcnt vmcnt(11)
	ds_write_b128 v20, v[44:47]
	s_waitcnt vmcnt(10)
	ds_write_b128 v20, v[64:67] offset:8192
	s_waitcnt vmcnt(9)
	ds_write_b128 v20, v[68:71] offset:32768
	s_waitcnt vmcnt(8)
	ds_write_b128 v20, v[72:75] offset:40960
	s_waitcnt vmcnt(7)
	ds_write_b128 v20, v[76:79] offset:49152
	s_waitcnt vmcnt(6)
	ds_write_b128 v20, v[80:83] offset:57344
	s_waitcnt lgkmcnt(0)
	s_barrier
	ds_read_b128 v[44:47], v31 offset:32768
	v_mfma_f32_16x16x32_f16 v[52:55], v[56:59], v[92:95], v[52:55]
	v_mfma_f32_16x16x32_f16 v[56:59], v[88:91], v[92:95], v[60:63]
	s_nop 2
	ds_read_b128 v[60:63], v31 offset:36864
	ds_read_b128 v[64:67], v21
	ds_read_b128 v[68:71], v21 offset:4096
	s_waitcnt lgkmcnt(1)
	v_mfma_f32_16x16x32_f16 v[48:51], v[44:47], v[64:67], v[48:51]
	v_mfma_f32_16x16x32_f16 v[40:43], v[60:63], v[64:67], v[40:43]
	s_waitcnt lgkmcnt(0)
	v_mfma_f32_16x16x32_f16 v[44:47], v[44:47], v[68:71], v[52:55]
	s_nop 2
	ds_read_b128 v[52:55], v32 offset:32768
	ds_read_b128 v[64:67], v32 offset:36864
	v_mfma_f32_16x16x32_f16 v[56:59], v[60:63], v[68:71], v[56:59]
	ds_read_b128 v[60:63], v23
	ds_read_b128 v[68:71], v23 offset:4096
	s_waitcnt lgkmcnt(1)
	v_mfma_f32_16x16x32_f16 v[48:51], v[52:55], v[60:63], v[48:51]
	v_mfma_f32_16x16x32_f16 v[40:43], v[64:67], v[60:63], v[40:43]
	s_waitcnt lgkmcnt(0)
	v_mfma_f32_16x16x32_f16 v[44:47], v[52:55], v[68:71], v[44:47]
	ds_read_b128 v[52:55], v35 offset:32768
	ds_read_b128 v[60:63], v35 offset:36864
	v_mfma_f32_16x16x32_f16 v[56:59], v[64:67], v[68:71], v[56:59]
	ds_read_b128 v[64:67], v24
	ds_read_b128 v[68:71], v24 offset:4096
	ds_read_b128 v[72:75], v22
	ds_read_b128 v[76:79], v22 offset:4096
	s_waitcnt vmcnt(5)
	ds_write_b128 v20, v[96:99] offset:16384
	s_waitcnt lgkmcnt(4)
	v_mfma_f32_16x16x32_f16 v[48:51], v[52:55], v[64:67], v[48:51]
	v_mfma_f32_16x16x32_f16 v[40:43], v[60:63], v[64:67], v[40:43]
	ds_read_b128 v[64:67], v33 offset:32768
	ds_read_b128 v[80:83], v33 offset:36864
	s_waitcnt vmcnt(4)
	ds_write_b128 v20, v[100:103] offset:24576
	s_waitcnt vmcnt(3)
	ds_write_b128 v116, v[104:107] offset:32768
	s_waitcnt vmcnt(2)
	ds_write_b128 v116, v[108:111] offset:40960
	s_waitcnt vmcnt(1)
	ds_write_b128 v116, v[112:115] offset:49152
	s_waitcnt lgkmcnt(9)
	v_mfma_f32_16x16x32_f16 v[44:47], v[52:55], v[68:71], v[44:47]
	s_waitcnt vmcnt(0)
	ds_write_b128 v116, v[84:87] offset:57344
	v_mfma_f32_16x16x32_f16 v[52:55], v[60:63], v[68:71], v[56:59]
	s_nop 2
	global_load_dwordx4 v[56:59], v[16:17], off offset:1024
	global_load_dwordx4 v[60:63], v[18:19], off offset:1024
	global_load_dwordx4 v[68:71], v[8:9], off offset:1024
	global_load_dwordx4 v[84:87], v[10:11], off offset:1024
	global_load_dwordx4 v[88:91], v[12:13], off offset:1024
	global_load_dwordx4 v[92:95], v[14:15], off offset:1024
	s_waitcnt lgkmcnt(0)
	v_mfma_f32_16x16x32_f16 v[48:51], v[64:67], v[72:75], v[48:51]
	s_barrier
	v_mfma_f32_16x16x32_f16 v[40:43], v[80:83], v[72:75], v[40:43]
	v_mfma_f32_16x16x32_f16 v[44:47], v[64:67], v[76:79], v[44:47]
	ds_read_b128 v[64:67], v34 offset:32768
	ds_read_b128 v[72:75], v34 offset:36864
	v_mfma_f32_16x16x32_f16 v[52:55], v[80:83], v[76:79], v[52:55]
	ds_read_b128 v[76:79], v21 offset:16384
	ds_read_b128 v[80:83], v21 offset:20480
	s_waitcnt lgkmcnt(1)
	v_mfma_f32_16x16x32_f16 v[48:51], v[64:67], v[76:79], v[48:51]
	v_mfma_f32_16x16x32_f16 v[40:43], v[72:75], v[76:79], v[40:43]
	s_waitcnt lgkmcnt(0)
	v_mfma_f32_16x16x32_f16 v[44:47], v[64:67], v[80:83], v[44:47]
	ds_read_b128 v[64:67], v36 offset:32768
	ds_read_b128 v[76:79], v36 offset:36864
	v_mfma_f32_16x16x32_f16 v[52:55], v[72:75], v[80:83], v[52:55]
	ds_read_b128 v[72:75], v23 offset:16384
	ds_read_b128 v[80:83], v23 offset:20480
	s_waitcnt lgkmcnt(1)
	v_mfma_f32_16x16x32_f16 v[48:51], v[64:67], v[72:75], v[48:51]
	v_mfma_f32_16x16x32_f16 v[40:43], v[76:79], v[72:75], v[40:43]
	s_waitcnt lgkmcnt(0)
	v_mfma_f32_16x16x32_f16 v[44:47], v[64:67], v[80:83], v[44:47]
	ds_read_b128 v[64:67], v37 offset:32768
	ds_read_b128 v[72:75], v37 offset:36864
	v_mfma_f32_16x16x32_f16 v[52:55], v[76:79], v[80:83], v[52:55]
	ds_read_b128 v[76:79], v24 offset:16384
	ds_read_b128 v[80:83], v24 offset:20480
	s_waitcnt lgkmcnt(1)
	v_mfma_f32_16x16x32_f16 v[48:51], v[64:67], v[76:79], v[48:51]
	v_mfma_f32_16x16x32_f16 v[40:43], v[72:75], v[76:79], v[40:43]
	s_waitcnt lgkmcnt(0)
	v_mfma_f32_16x16x32_f16 v[44:47], v[64:67], v[80:83], v[44:47]
	ds_read_b128 v[64:67], v38 offset:32768
	ds_read_b128 v[76:79], v22 offset:16384
	ds_read_b128 v[96:99], v38 offset:36864
	global_load_dwordx4 v[100:103], v[10:11], off offset:1280
	v_mfma_f32_16x16x32_f16 v[52:55], v[72:75], v[80:83], v[52:55]
	global_load_dwordx4 v[72:75], v[8:9], off offset:1280
	ds_read_b128 v[80:83], v22 offset:20480
	global_load_dwordx4 v[104:107], v[12:13], off offset:1280
	global_load_dwordx4 v[108:111], v[14:15], off offset:1280
	s_waitcnt lgkmcnt(2)
	v_mfma_f32_16x16x32_f16 v[48:51], v[64:67], v[76:79], v[48:51]
	s_waitcnt lgkmcnt(1)
	v_mfma_f32_16x16x32_f16 v[40:43], v[96:99], v[76:79], v[40:43]
	global_load_dwordx4 v[76:79], v[16:17], off offset:1280
	global_load_dwordx4 v[112:115], v[18:19], off offset:1280
	s_waitcnt vmcnt(11)
	ds_write_b128 v20, v[56:59]
	s_waitcnt vmcnt(10)
	ds_write_b128 v20, v[60:63] offset:8192
	s_waitcnt vmcnt(9)
	ds_write_b128 v20, v[68:71] offset:32768
	s_waitcnt vmcnt(8)
	ds_write_b128 v20, v[84:87] offset:40960
	s_waitcnt vmcnt(7)
	ds_write_b128 v20, v[88:91] offset:49152
	s_waitcnt vmcnt(6)
	ds_write_b128 v20, v[92:95] offset:57344
	s_waitcnt lgkmcnt(0)
	s_barrier
	ds_read_b128 v[56:59], v31 offset:32768
	v_mfma_f32_16x16x32_f16 v[44:47], v[64:67], v[80:83], v[44:47]
	ds_read_b128 v[60:63], v31 offset:36864
	ds_read_b128 v[64:67], v21
	ds_read_b128 v[68:71], v21 offset:4096
	v_mfma_f32_16x16x32_f16 v[52:55], v[96:99], v[80:83], v[52:55]
	s_waitcnt lgkmcnt(1)
	v_mfma_f32_16x16x32_f16 v[48:51], v[56:59], v[64:67], v[48:51]
	v_mfma_f32_16x16x32_f16 v[40:43], v[60:63], v[64:67], v[40:43]
	s_waitcnt lgkmcnt(0)
	v_mfma_f32_16x16x32_f16 v[44:47], v[56:59], v[68:71], v[44:47]
	ds_read_b128 v[56:59], v32 offset:32768
	ds_read_b128 v[64:67], v32 offset:36864
	v_mfma_f32_16x16x32_f16 v[52:55], v[60:63], v[68:71], v[52:55]
	ds_read_b128 v[60:63], v23
	ds_read_b128 v[68:71], v23 offset:4096
	s_waitcnt lgkmcnt(1)
	v_mfma_f32_16x16x32_f16 v[48:51], v[56:59], v[60:63], v[48:51]
	v_mfma_f32_16x16x32_f16 v[40:43], v[64:67], v[60:63], v[40:43]
	s_waitcnt lgkmcnt(0)
	v_mfma_f32_16x16x32_f16 v[44:47], v[56:59], v[68:71], v[44:47]
	ds_read_b128 v[56:59], v35 offset:32768
	ds_read_b128 v[60:63], v35 offset:36864
	v_mfma_f32_16x16x32_f16 v[52:55], v[64:67], v[68:71], v[52:55]
	ds_read_b128 v[64:67], v24
	ds_read_b128 v[68:71], v24 offset:4096
	s_waitcnt vmcnt(4)
	ds_write_b128 v116, v[72:75] offset:32768
	s_waitcnt lgkmcnt(2)
	v_mfma_f32_16x16x32_f16 v[48:51], v[56:59], v[64:67], v[48:51]
	v_mfma_f32_16x16x32_f16 v[40:43], v[60:63], v[64:67], v[40:43]
	ds_read_b128 v[64:67], v33 offset:32768
	s_waitcnt lgkmcnt(2)
	v_mfma_f32_16x16x32_f16 v[44:47], v[56:59], v[68:71], v[44:47]
	ds_read_b128 v[56:59], v22
	ds_read_b128 v[72:75], v33 offset:36864
	ds_write_b128 v116, v[100:103] offset:40960
	s_waitcnt vmcnt(3)
	ds_write_b128 v116, v[104:107] offset:49152
	v_mfma_f32_16x16x32_f16 v[52:55], v[60:63], v[68:71], v[52:55]
	ds_read_b128 v[60:63], v22 offset:4096
	s_waitcnt vmcnt(2)
	ds_write_b128 v116, v[108:111] offset:57344
	s_waitcnt vmcnt(1)
	ds_write_b128 v20, v[76:79] offset:16384
	s_waitcnt vmcnt(0)
	ds_write_b128 v20, v[112:115] offset:24576
	s_waitcnt lgkmcnt(7)
	v_mfma_f32_16x16x32_f16 v[48:51], v[64:67], v[56:59], v[48:51]
	s_waitcnt lgkmcnt(6)
	v_mfma_f32_16x16x32_f16 v[40:43], v[72:75], v[56:59], v[40:43]
	global_load_dwordx4 v[56:59], v[16:17], off offset:1536
	global_load_dwordx4 v[68:71], v[18:19], off offset:1536
	global_load_dwordx4 v[76:79], v[8:9], off offset:1536
	global_load_dwordx4 v[80:83], v[10:11], off offset:1536
	s_waitcnt lgkmcnt(3)
	v_mfma_f32_16x16x32_f16 v[44:47], v[64:67], v[60:63], v[44:47]
	global_load_dwordx4 v[64:67], v[12:13], off offset:1536
	global_load_dwordx4 v[84:87], v[14:15], off offset:1536
	s_waitcnt lgkmcnt(0)
	s_barrier
	ds_read_b128 v[88:91], v34 offset:32768
	v_mfma_f32_16x16x32_f16 v[52:55], v[72:75], v[60:63], v[52:55]
	ds_read_b128 v[60:63], v34 offset:36864
	ds_read_b128 v[72:75], v21 offset:16384
	ds_read_b128 v[92:95], v21 offset:20480
	s_waitcnt lgkmcnt(1)
	v_mfma_f32_16x16x32_f16 v[48:51], v[88:91], v[72:75], v[48:51]
	v_mfma_f32_16x16x32_f16 v[40:43], v[60:63], v[72:75], v[40:43]
	ds_read_b128 v[72:75], v36 offset:32768
	s_waitcnt lgkmcnt(1)
	v_mfma_f32_16x16x32_f16 v[44:47], v[88:91], v[92:95], v[44:47]
	v_mfma_f32_16x16x32_f16 v[52:55], v[60:63], v[92:95], v[52:55]
	ds_read_b128 v[60:63], v36 offset:36864
	ds_read_b128 v[88:91], v23 offset:16384
	ds_read_b128 v[92:95], v23 offset:20480
	s_waitcnt lgkmcnt(1)
	v_mfma_f32_16x16x32_f16 v[48:51], v[72:75], v[88:91], v[48:51]
	v_mfma_f32_16x16x32_f16 v[40:43], v[60:63], v[88:91], v[40:43]
	s_waitcnt lgkmcnt(0)
	v_mfma_f32_16x16x32_f16 v[44:47], v[72:75], v[92:95], v[44:47]
	ds_read_b128 v[72:75], v37 offset:32768
	ds_read_b128 v[88:91], v37 offset:36864
	v_mfma_f32_16x16x32_f16 v[52:55], v[60:63], v[92:95], v[52:55]
	ds_read_b128 v[60:63], v24 offset:16384
	ds_read_b128 v[92:95], v24 offset:20480
	s_waitcnt lgkmcnt(1)
	v_mfma_f32_16x16x32_f16 v[48:51], v[72:75], v[60:63], v[48:51]
	v_mfma_f32_16x16x32_f16 v[40:43], v[88:91], v[60:63], v[40:43]
	s_waitcnt lgkmcnt(0)
	v_mfma_f32_16x16x32_f16 v[44:47], v[72:75], v[92:95], v[44:47]
	ds_read_b128 v[60:63], v38 offset:32768
	ds_read_b128 v[72:75], v38 offset:36864
	v_mfma_f32_16x16x32_f16 v[52:55], v[88:91], v[92:95], v[52:55]
	ds_read_b128 v[88:91], v22 offset:16384
	ds_read_b128 v[92:95], v22 offset:20480
	global_load_dwordx4 v[96:99], v[16:17], off offset:1792
	global_load_dwordx4 v[100:103], v[18:19], off offset:1792
	s_waitcnt lgkmcnt(1)
	v_mfma_f32_16x16x32_f16 v[48:51], v[60:63], v[88:91], v[48:51]
	v_mfma_f32_16x16x32_f16 v[16:19], v[72:75], v[88:91], v[40:43]
	s_nop 2
	global_load_dwordx4 v[40:43], v[8:9], off offset:1792
	global_load_dwordx4 v[88:91], v[10:11], off offset:1792
	global_load_dwordx4 v[104:107], v[12:13], off offset:1792
	global_load_dwordx4 v[108:111], v[14:15], off offset:1792
	s_waitcnt vmcnt(11)
	ds_write_b128 v20, v[56:59]
	s_waitcnt vmcnt(10)
	ds_write_b128 v20, v[68:71] offset:8192
	s_waitcnt vmcnt(9)
	ds_write_b128 v20, v[76:79] offset:32768
	s_waitcnt vmcnt(8)
	ds_write_b128 v20, v[80:83] offset:40960
	s_waitcnt vmcnt(7)
	ds_write_b128 v20, v[64:67] offset:49152
	s_waitcnt vmcnt(6)
	ds_write_b128 v20, v[84:87] offset:57344
	s_waitcnt lgkmcnt(0)
	s_barrier
	ds_read_b128 v[12:15], v31 offset:32768
	v_mfma_f32_16x16x32_f16 v[8:11], v[60:63], v[92:95], v[44:47]
	v_mfma_f32_16x16x32_f16 v[44:47], v[72:75], v[92:95], v[52:55]
	s_nop 2
	ds_read_b128 v[52:55], v31 offset:36864
	ds_read_b128 v[56:59], v21
	ds_read_b128 v[60:63], v21 offset:4096
	s_waitcnt lgkmcnt(1)
	v_mfma_f32_16x16x32_f16 v[48:51], v[12:15], v[56:59], v[48:51]
	v_mfma_f32_16x16x32_f16 v[16:19], v[52:55], v[56:59], v[16:19]
	s_waitcnt lgkmcnt(0)
	v_mfma_f32_16x16x32_f16 v[8:11], v[12:15], v[60:63], v[8:11]
	ds_read_b128 v[12:15], v32 offset:32768
	ds_read_b128 v[56:59], v32 offset:36864
	v_mfma_f32_16x16x32_f16 v[44:47], v[52:55], v[60:63], v[44:47]
	ds_read_b128 v[52:55], v23
	ds_read_b128 v[60:63], v23 offset:4096
	s_waitcnt lgkmcnt(1)
	v_mfma_f32_16x16x32_f16 v[48:51], v[12:15], v[52:55], v[48:51]
	v_mfma_f32_16x16x32_f16 v[16:19], v[56:59], v[52:55], v[16:19]
	s_waitcnt lgkmcnt(0)
	v_mfma_f32_16x16x32_f16 v[8:11], v[12:15], v[60:63], v[8:11]
	ds_read_b128 v[12:15], v35 offset:32768
	ds_read_b128 v[52:55], v35 offset:36864
	v_mfma_f32_16x16x32_f16 v[44:47], v[56:59], v[60:63], v[44:47]
	ds_read_b128 v[56:59], v24
	ds_read_b128 v[60:63], v24 offset:4096
	s_waitcnt lgkmcnt(1)
	v_mfma_f32_16x16x32_f16 v[48:51], v[12:15], v[56:59], v[48:51]
	s_waitcnt lgkmcnt(0)
	v_mfma_f32_16x16x32_f16 v[8:11], v[12:15], v[60:63], v[8:11]
	ds_read_b128 v[12:15], v33 offset:32768
	v_mfma_f32_16x16x32_f16 v[16:19], v[52:55], v[56:59], v[16:19]
	v_mfma_f32_16x16x32_f16 v[44:47], v[52:55], v[60:63], v[44:47]
	ds_read_b128 v[52:55], v33 offset:36864
	ds_read_b128 v[56:59], v22
	ds_read_b128 v[60:63], v22 offset:4096
	s_waitcnt vmcnt(5)
	ds_write_b128 v20, v[96:99] offset:16384
	s_waitcnt vmcnt(4)
	ds_write_b128 v20, v[100:103] offset:24576
	s_waitcnt lgkmcnt(3)
	v_mfma_f32_16x16x32_f16 v[48:51], v[12:15], v[56:59], v[48:51]
	s_waitcnt lgkmcnt(2)
	v_mfma_f32_16x16x32_f16 v[8:11], v[12:15], v[60:63], v[8:11]
	v_add_u32_e32 v12, 0x10000, v20
	s_waitcnt vmcnt(3)
	ds_write_b128 v12, v[40:43]
	s_waitcnt vmcnt(2)
	ds_write_b128 v12, v[88:91] offset:8192
	s_waitcnt vmcnt(1)
	ds_write_b128 v12, v[104:107] offset:16384
	s_waitcnt vmcnt(0)
	ds_write_b128 v12, v[108:111] offset:24576
	s_waitcnt lgkmcnt(0)
	s_barrier
	ds_read_b128 v[12:15], v34 offset:32768
	v_mfma_f32_16x16x32_f16 v[16:19], v[52:55], v[56:59], v[16:19]
	v_mfma_f32_16x16x32_f16 v[40:43], v[52:55], v[60:63], v[44:47]
	ds_read_b128 v[32:35], v34 offset:36864
	s_nop 1
	ds_read_b128 v[44:47], v21 offset:16384
	ds_read_b128 v[52:55], v21 offset:20480
	s_waitcnt lgkmcnt(1)
	v_mfma_f32_16x16x32_f16 v[48:51], v[12:15], v[44:47], v[48:51]
	s_waitcnt lgkmcnt(0)
	v_mfma_f32_16x16x32_f16 v[8:11], v[12:15], v[52:55], v[8:11]
	ds_read_b128 v[12:15], v36 offset:32768
	v_mfma_f32_16x16x32_f16 v[16:19], v[32:35], v[44:47], v[16:19]
	v_mfma_f32_16x16x32_f16 v[32:35], v[32:35], v[52:55], v[40:43]
	s_nop 2
	ds_read_b128 v[40:43], v36 offset:36864
	ds_read_b128 v[44:47], v23 offset:16384
	ds_read_b128 v[52:55], v23 offset:20480
	s_waitcnt lgkmcnt(1)
	v_mfma_f32_16x16x32_f16 v[48:51], v[12:15], v[44:47], v[48:51]
	s_waitcnt lgkmcnt(0)
	v_mfma_f32_16x16x32_f16 v[8:11], v[12:15], v[52:55], v[8:11]
	ds_read_b128 v[12:15], v37 offset:32768
	v_mfma_f32_16x16x32_f16 v[16:19], v[40:43], v[44:47], v[16:19]
	v_mfma_f32_16x16x32_f16 v[32:35], v[40:43], v[52:55], v[32:35]
	ds_read_b128 v[40:43], v37 offset:36864
	ds_read_b128 v[44:47], v24 offset:16384
	ds_read_b128 v[52:55], v24 offset:20480
	v_lshlrev_b32_e32 v24, 6, v30
	s_waitcnt lgkmcnt(1)
	v_mfma_f32_16x16x32_f16 v[48:51], v[12:15], v[44:47], v[48:51]
	s_waitcnt lgkmcnt(0)
	v_mfma_f32_16x16x32_f16 v[8:11], v[12:15], v[52:55], v[8:11]
	ds_read_b128 v[12:15], v38 offset:32768
	v_mfma_f32_16x16x32_f16 v[16:19], v[40:43], v[44:47], v[16:19]
	v_mfma_f32_16x16x32_f16 v[32:35], v[40:43], v[52:55], v[32:35]
	ds_read_b128 v[36:39], v38 offset:36864
	ds_read_b128 v[40:43], v22 offset:16384
	ds_read_b128 v[44:47], v22 offset:20480
	s_waitcnt lgkmcnt(1)
	v_mfma_f32_16x16x32_f16 v[20:23], v[12:15], v[40:43], v[48:51]
	s_waitcnt lgkmcnt(0)
	v_mfma_f32_16x16x32_f16 v[12:15], v[12:15], v[44:47], v[8:11]
	s_nop 2
	v_lshl_add_u64 v[8:9], s[0:1], 0, v[24:25]
	v_lshlrev_b32_e32 v24, 3, v29
	v_mfma_f32_16x16x32_f16 v[16:19], v[36:39], v[40:43], v[16:19]
	v_lshl_add_u64 v[30:31], v[8:9], 0, v[24:25]
	v_mfma_f32_16x16x32_f16 v[8:11], v[36:39], v[44:47], v[32:35]
	v_mbcnt_lo_u32_b32 v196, -1, 0
	v_mbcnt_hi_u32_b32 v196, -1, v196
	v_and_b32_e32 v197, 15, v196
	v_lshrrev_b32_e32 v198, 4, v196
	v_lshrrev_b32_e32 v222, 10, v116
	s_nop 0
	v_readfirstlane_b32 s36, v222
	s_nop 3
	s_and_b32 s36, s36, 7
	s_mulk_i32 s36, 0x500
	s_add_u32 s36, s36, 0x8000
	v_mul_u32_u24_e32 v199, 0x50, v197
	v_lshl_add_u32 v199, v198, 3, v199
	v_add_u32_e32 v199, s36, v199
	v_lshrrev_b32_e32 v200, 2, v196
	v_and_b32_e32 v201, 3, v196
	v_mul_u32_u24_e32 v202, 0x50, v200
	v_lshl_add_u32 v202, v201, 4, v202
	v_add_u32_e32 v202, s36, v202
	v_lshlrev_b32_e32 v203, 2, v200
	v_add_u32_e32 v204, 32, v203
	v_lshlrev_b32_e32 v220, 4, v201
	v_mov_b32_e32 v221, 0
	v_sub_u32_e32 v205, v27, v197
	v_add_u32_e32 v205, v205, v200
	s_mov_b64 s[0:1], exec
	s_cbranch_execz .LBB7_9
	v_mov_b32_e32 v29, v25
	v_lshl_add_u64 v[24:25], s[2:3], 0, v[28:29]
	global_load_dword v24, v[24:25], off
	s_nop 0
	v_add_f32_e32 v16, v0, v16
	v_add_f32_e32 v17, v1, v17
	v_add_f32_e32 v18, v2, v18
	v_add_f32_e32 v19, v3, v19
	v_add_f32_e32 v20, v4, v20
	v_add_f32_e32 v21, v5, v21
	v_max_f32_e32 v25, 0, v16
	v_max_f32_e32 v28, 0, v17
	v_max_f32_e32 v18, 0, v18
	v_max_f32_e32 v19, 0, v19
	v_add_f32_e32 v22, v6, v22
	v_add_f32_e32 v23, v7, v23
	v_max_f32_e32 v20, 0, v20
	v_max_f32_e32 v21, 0, v21
	v_cvt_pk_f16_f32 v19, v18, v19
	v_cvt_pk_f16_f32 v18, v25, v28
	v_max_f32_e32 v22, 0, v22
	v_max_f32_e32 v23, 0, v23
	v_cvt_pk_f16_f32 v16, v20, v21
	v_cvt_pk_f16_f32 v17, v22, v23
	s_waitcnt vmcnt(0)
	v_ashrrev_i32_e32 v25, 31, v24
	v_lshlrev_b64 v[20:21], 11, v[24:25]
	v_lshl_add_u64 v[20:21], v[30:31], 0, v[20:21]
	ds_write_b64 v199, v[16:17]
	ds_write_b64 v199, v[18:19] offset:32
	s_waitcnt lgkmcnt(0)
	ds_read_b128 v[208:211], v202
	ds_bpermute_b32 v216, v203, v20
	ds_bpermute_b32 v217, v203, v21
	v_add_u32_e32 v222, 0, v205
	v_cmp_gt_u32_e64 s[38:39], s4, v222
	s_waitcnt lgkmcnt(0)
	v_lshl_add_u64 v[216:217], v[216:217], 0, v[220:221]
	s_mov_b64 s[42:43], exec
	s_and_b64 exec, s[42:43], s[38:39]
	global_store_dwordx4 v[216:217], v[208:211], off sc1
	s_mov_b64 exec, s[42:43]
.LBB7_9:
	s_or_b64 exec, exec, s[0:1]
	s_nop 2
	v_or_b32_e32 v16, 16, v27
	v_cmp_gt_u32_e32 vcc, s4, v16
	s_mov_b64 s[0:1], exec
	s_cbranch_execz .LBB7_11
	v_add_f32_e32 v5, v5, v13
	v_ashrrev_i32_e32 v27, 31, v26
	v_add_f32_e32 v4, v4, v12
	v_max_f32_e32 v12, 0, v5
	v_add_f32_e32 v5, v6, v14
	v_add_f32_e32 v6, v7, v15
	v_lshlrev_b64 v[16:17], 11, v[26:27]
	v_max_f32_e32 v4, 0, v4
	v_max_f32_e32 v5, 0, v5
	v_max_f32_e32 v6, 0, v6
	v_lshl_add_u64 v[16:17], v[30:31], 0, v[16:17]
	v_cvt_pk_f16_f32 v5, v5, v6
	v_cvt_pk_f16_f32 v4, v4, v12
	v_add_f32_e32 v1, v1, v9
	ds_write_b64 v199, v[4:5]
	v_add_f32_e32 v0, v0, v8
	v_max_f32_e32 v4, 0, v1
	v_add_f32_e32 v1, v2, v10
	v_add_f32_e32 v2, v3, v11
	v_max_f32_e32 v0, 0, v0
	v_max_f32_e32 v1, 0, v1
	v_max_f32_e32 v2, 0, v2
	v_cvt_pk_f16_f32 v1, v1, v2
	v_cvt_pk_f16_f32 v0, v0, v4
	ds_write_b64 v199, v[0:1] offset:32
	s_waitcnt lgkmcnt(0)
	ds_read_b128 v[208:211], v202
	ds_bpermute_b32 v216, v203, v16
	ds_bpermute_b32 v217, v203, v17
	v_add_u32_e32 v222, 16, v205
	v_cmp_gt_u32_e64 s[38:39], s4, v222
	s_waitcnt lgkmcnt(0)
	v_lshl_add_u64 v[216:217], v[216:217], 0, v[220:221]
	s_mov_b64 s[42:43], exec
	s_and_b64 exec, s[42:43], s[38:39]
	global_store_dwordx4 v[216:217], v[208:211], off sc1
	s_mov_b64 exec, s[42:43]
